# final: adds the s_nop wait state between every m0 write and its LDS-DMA load that the load-phase reorder had left adjacent
# speedup vs baseline: 1.0025x; 1.0025x over previous
; #define GM_STAGE(bufoff, gbase, voff) do { _Pragma("unroll") for (int _i = 0; _i < 2; ++_i) \
;         __builtin_amdgcn_global_load_lds((const unsigned*)((const char*)(gbase) + (voff)[_i]), (LAS unsigned*)(lds + (bufoff) + ldsw + _i * 8192), 16, 0, 0); } while (0)
; #define GM_LDA(dst, b, h) do { _Pragma("unroll") for (int m = 0; m < 4; ++m) _Pragma("unroll") for (int k = 0; k < 2; ++k) dst[m][k] = *(const LAS s16x8*)(lds + GM_SA(b, h) + aoff + m * 2048 + k * 1024); } while (0)
; #define GM_LDB(dst, b, h) do { _Pragma("unroll") for (int n = 0; n < 2; ++n) _Pragma("unroll") for (int k = 0; k < 2; ++k) dst[n][k] = *(const LAS s16x8*)(lds + GM_SB(b, h) + boff + n * 2048 + k * 1024); } while (0)
; #define GM_MMA(ai, bj, At, Bt) do { __builtin_amdgcn_s_setprio(1); _Pragma("unroll") for (int m = 0; m < 4; ++m) _Pragma("unroll") for (int n = 0; n < 2; ++n) _Pragma("unroll") for (int k = 0; k < 2; ++k) \
;         acc[ai][bj][m][n] = mma16<BF>(Bt[n][k], At[m][k], acc[ai][bj][m][n]); __builtin_amdgcn_s_setprio(0); } while (0)
; #define GM_WAIT_V(n) asm volatile("s_waitcnt vmcnt(" #n ")" ::: "memory")
; #define GM_WAIT_L(n) asm volatile("s_waitcnt lgkmcnt(" #n ")" ::: "memory")
; template <bool BF, bool GATHER = false, class Epi, class Hook>
; __device__ __forceinline__ void gemm_phase(LAS unsigned char* lds, const Gemm g, const Order& S, const Epi& E, Hook& HK) {
;     ...
;             const bool last = (t == nt - 2);
;             const char* a1 = cA + (size_t)(t + 1) * kstep;
;             const char* a2 = last ? nA : cA + (size_t)(t + 2) * kstep; const char* b2 = last ? nB : cB + (size_t)(t + 2) * kstep;
;             const char* a3 = a2 + kstep; const char* b3 = b2 + kstep;
;             unsigned s0[2], s1[2];
;             if constexpr (GATHER) { s0[0] = last ? nA0[0] : gA0[0]; s0[1] = last ? nA0[1] : gA0[1]; s1[0] = last ? nA1[0] : gA1[0]; s1[1] = last ? nA1[1] : gA1[1]; }
;             GM_LDB(B0, 0, 0); GM_LDB(B1, 0, 1); GM_SCHED; GM_LDA(At, 0, 0); GM_STA_H1(GM_SA(1, 1), a1, gA1);
;             GM_WAIT_V(8); GM_WAIT_L(0); GM_BAR; GM_MMA(0, 0, At, B0); GM_MMA(0, 1, At, B1); GM_BAR; GM_SCHED;
;             GM_LDA(At, 0, 1); GM_STAGE(GM_SB(0, 0), b2, voffB); GM_STAGE(GM_SB(0, 1), b2 + hstepB, voffB); GM_STA_H0(GM_SA(0, 0), a2, s0);
;             GM_WAIT_V(8); GM_WAIT_L(0); GM_BAR; GM_MMA(1, 0, At, B0); GM_MMA(1, 1, At, B1); GM_BAR; GM_SCHED;
.LBB0_380:
	s_add_u32 s28, s2, 0xfffc0080
	s_addc_u32 s29, s3, -1
	s_cmp_eq_u32 s51, 12
	s_cselect_b32 s31, s9, s29
	s_cselect_b32 s30, s19, s28
	s_cselect_b32 s29, s21, s50
	s_cselect_b32 s28, s48, s49
	v_lshl_add_u64 v[150:151], s[2:3], 0, v[138:139]
	s_add_i32 m0, s27, 0xc000
	s_nop 0
	global_load_lds_dwordx4 v[150:151], off
	v_lshl_add_u64 v[150:151], s[2:3], 0, v[140:141]
	s_add_i32 m0, s27, 0xe000
	s_nop 0
	global_load_lds_dwordx4 v[150:151], off
	ds_read_b128 v[146:149], v158
	ds_read_b128 v[162:165], v158 offset:1024
	ds_read_b128 v[166:169], v158 offset:2048
	ds_read_b128 v[170:173], v158 offset:3072
	ds_read_b128 v[174:177], v159
	ds_read_b128 v[178:181], v159 offset:1024
	ds_read_b128 v[182:185], v159 offset:2048
	ds_read_b128 v[186:189], v159 offset:3072
	ds_read_b128 v[190:193], v160
	ds_read_b128 v[194:197], v160 offset:1024
	ds_read_b128 v[198:201], v160 offset:2048
	ds_read_b128 v[202:205], v160 offset:3072
	ds_read_b128 v[206:209], v160 offset:4096
	ds_read_b128 v[210:213], v160 offset:5120
	ds_read_b128 v[214:217], v160 offset:6144
	ds_read_b128 v[218:221], v160 offset:7168
	s_waitcnt vmcnt(8)
	s_waitcnt lgkmcnt(0)
	s_barrier
	v_mfma_f32_16x16x32_f16 v[126:129], v[146:149], v[190:193], v[126:129]
	v_mfma_f32_16x16x32_f16 v[122:125], v[166:169], v[190:193], v[122:125]
	v_mfma_f32_16x16x32_f16 v[110:113], v[146:149], v[198:201], v[110:113]
	v_mfma_f32_16x16x32_f16 v[106:109], v[166:169], v[198:201], v[106:109]
	v_mfma_f32_16x16x32_f16 v[94:97], v[146:149], v[206:209], v[94:97]
	v_mfma_f32_16x16x32_f16 v[90:93], v[166:169], v[206:209], v[90:93]
	v_mfma_f32_16x16x32_f16 v[78:81], v[146:149], v[214:217], v[78:81]
	v_mfma_f32_16x16x32_f16 v[74:77], v[166:169], v[214:217], v[74:77]
	v_mfma_f32_16x16x32_f16 v[126:129], v[162:165], v[194:197], v[126:129]
	v_mfma_f32_16x16x32_f16 v[122:125], v[170:173], v[194:197], v[122:125]
	v_mfma_f32_16x16x32_f16 v[110:113], v[162:165], v[202:205], v[110:113]
	v_mfma_f32_16x16x32_f16 v[106:109], v[170:173], v[202:205], v[106:109]
	v_mfma_f32_16x16x32_f16 v[94:97], v[162:165], v[210:213], v[94:97]
	v_mfma_f32_16x16x32_f16 v[90:93], v[170:173], v[210:213], v[90:93]
	v_mfma_f32_16x16x32_f16 v[78:81], v[162:165], v[218:221], v[78:81]
	v_mfma_f32_16x16x32_f16 v[74:77], v[170:173], v[218:221], v[74:77]
	v_mfma_f32_16x16x32_f16 v[118:121], v[174:177], v[190:193], v[118:121]
	v_mfma_f32_16x16x32_f16 v[114:117], v[182:185], v[190:193], v[114:117]
	v_mfma_f32_16x16x32_f16 v[102:105], v[174:177], v[198:201], v[102:105]
	v_mfma_f32_16x16x32_f16 v[98:101], v[182:185], v[198:201], v[98:101]
	v_mfma_f32_16x16x32_f16 v[86:89], v[174:177], v[206:209], v[86:89]
	v_mfma_f32_16x16x32_f16 v[82:85], v[182:185], v[206:209], v[82:85]
	v_mfma_f32_16x16x32_f16 v[70:73], v[174:177], v[214:217], v[70:73]
	v_mfma_f32_16x16x32_f16 v[66:69], v[182:185], v[214:217], v[66:69]
	v_mfma_f32_16x16x32_f16 v[118:121], v[178:181], v[194:197], v[118:121]
	v_mfma_f32_16x16x32_f16 v[114:117], v[186:189], v[194:197], v[114:117]
	v_mfma_f32_16x16x32_f16 v[102:105], v[178:181], v[202:205], v[102:105]
	v_mfma_f32_16x16x32_f16 v[98:101], v[186:189], v[202:205], v[98:101]
	v_mfma_f32_16x16x32_f16 v[86:89], v[178:181], v[210:213], v[86:89]
	v_mfma_f32_16x16x32_f16 v[82:85], v[186:189], v[210:213], v[82:85]
	v_mfma_f32_16x16x32_f16 v[70:73], v[178:181], v[218:221], v[70:73]
	v_mfma_f32_16x16x32_f16 v[66:69], v[186:189], v[218:221], v[66:69]
	s_barrier
	s_add_i32 s52, s45, s35
	v_lshl_add_u64 v[150:151], s[28:29], 0, v[132:133]
	s_mov_b32 m0, s52
	s_nop 0
	global_load_lds_dwordx4 v[150:151], off
	s_add_i32 m0, s52, 0x2000
	s_add_u32 s52, s28, 0x40000
	v_lshl_add_u64 v[222:223], s[28:29], 0, v[136:137]
	s_addc_u32 s53, s29, 0
	s_add_i32 s54, s46, s35
	global_load_lds_dwordx4 v[222:223], off
	v_lshl_add_u64 v[224:225], s[52:53], 0, v[132:133]
	s_mov_b32 m0, s54
	v_lshl_add_u64 v[226:227], s[30:31], 0, v[134:135]
	global_load_lds_dwordx4 v[224:225], off
	v_lshl_add_u64 v[224:225], s[52:53], 0, v[136:137]
	s_add_i32 m0, s54, 0x2000
	s_nop 0
	global_load_lds_dwordx4 v[224:225], off
	v_lshl_add_u64 v[224:225], s[30:31], 0, v[130:131]
	s_mov_b32 m0, s27
	s_nop 0
	global_load_lds_dwordx4 v[224:225], off
	s_mov_b32 m0, s36
	s_nop 0
	global_load_lds_dwordx4 v[226:227], off
	ds_read_b128 v[190:193], v160 offset:16384
	ds_read_b128 v[194:197], v160 offset:17408
	ds_read_b128 v[198:201], v160 offset:18432
	ds_read_b128 v[202:205], v160 offset:19456
	ds_read_b128 v[206:209], v160 offset:20480
	ds_read_b128 v[210:213], v160 offset:21504
	ds_read_b128 v[214:217], v160 offset:22528
	ds_read_b128 v[218:221], v160 offset:23552
	s_waitcnt vmcnt(8)
	s_waitcnt lgkmcnt(0)
	s_barrier
; #define GM_LDA(dst, b, h) do { _Pragma("unroll") for (int m = 0; m < 4; ++m) _Pragma("unroll") for (int k = 0; k < 2; ++k) dst[m][k] = *(const LAS s16x8*)(lds + GM_SA(b, h) + aoff + m * 2048 + k * 1024); } while (0)
; #define GM_LDB(dst, b, h) do { _Pragma("unroll") for (int n = 0; n < 2; ++n) _Pragma("unroll") for (int k = 0; k < 2; ++k) dst[n][k] = *(const LAS s16x8*)(lds + GM_SB(b, h) + boff + n * 2048 + k * 1024); } while (0)
; #define GM_MMA(ai, bj, At, Bt) do { __builtin_amdgcn_s_setprio(1); _Pragma("unroll") for (int m = 0; m < 4; ++m) _Pragma("unroll") for (int n = 0; n < 2; ++n) _Pragma("unroll") for (int k = 0; k < 2; ++k) \
;         acc[ai][bj][m][n] = mma16<BF>(Bt[n][k], At[m][k], acc[ai][bj][m][n]); __builtin_amdgcn_s_setprio(0); } while (0)
; #define GM_WAIT_V(n) asm volatile("s_waitcnt vmcnt(" #n ")" ::: "memory")
; #define GM_WAIT_L(n) asm volatile("s_waitcnt lgkmcnt(" #n ")" ::: "memory")
; #define GM_BAR __builtin_amdgcn_s_barrier()
; #define GM_SCHED __builtin_amdgcn_sched_barrier(0)
; #define GM_STA_H1(buf, p, o1) do { if constexpr (GATHER) GM_STAGE(buf, p, o1); else GM_STAGE(buf, (p) + hstepB, voffA); } while (0)
; template <bool BF, bool GATHER = false, class Epi, class Hook>
; __device__ __forceinline__ void gemm_phase(LAS unsigned char* lds, const Gemm g, const Order& S, const Epi& E, Hook& HK) {
;     ...
;             GM_WAIT_V(8); GM_WAIT_L(0); GM_BAR; GM_MMA(1, 0, At, B0); GM_MMA(1, 1, At, B1); GM_BAR; GM_SCHED;
;             GM_LDB(B0, 1, 0); GM_LDB(B1, 1, 1); GM_SCHED; GM_LDA(At, 1, 0); GM_STA_H1(GM_SA(0, 1), a2, s1);
;             GM_WAIT_V(8); GM_WAIT_L(0); GM_BAR; GM_MMA(0, 0, At, B0); GM_MMA(0, 1, At, B1); GM_BAR; GM_SCHED;
	v_mfma_f32_16x16x32_f16 v[62:65], v[146:149], v[190:193], v[62:65]
	v_mfma_f32_16x16x32_f16 v[58:61], v[166:169], v[190:193], v[58:61]
	v_mfma_f32_16x16x32_f16 v[46:49], v[146:149], v[198:201], v[46:49]
	v_mfma_f32_16x16x32_f16 v[42:45], v[166:169], v[198:201], v[42:45]
	v_mfma_f32_16x16x32_f16 v[30:33], v[146:149], v[206:209], v[30:33]
	v_mfma_f32_16x16x32_f16 v[26:29], v[166:169], v[206:209], v[26:29]
	v_mfma_f32_16x16x32_f16 v[14:17], v[146:149], v[214:217], v[14:17]
	v_mfma_f32_16x16x32_f16 v[10:13], v[166:169], v[214:217], v[10:13]
	v_mfma_f32_16x16x32_f16 v[62:65], v[162:165], v[194:197], v[62:65]
	v_mfma_f32_16x16x32_f16 v[58:61], v[170:173], v[194:197], v[58:61]
	v_mfma_f32_16x16x32_f16 v[46:49], v[162:165], v[202:205], v[46:49]
	v_mfma_f32_16x16x32_f16 v[42:45], v[170:173], v[202:205], v[42:45]
	v_mfma_f32_16x16x32_f16 v[30:33], v[162:165], v[210:213], v[30:33]
	v_mfma_f32_16x16x32_f16 v[26:29], v[170:173], v[210:213], v[26:29]
	v_mfma_f32_16x16x32_f16 v[14:17], v[162:165], v[218:221], v[14:17]
	v_mfma_f32_16x16x32_f16 v[10:13], v[170:173], v[218:221], v[10:13]
	v_mfma_f32_16x16x32_f16 v[54:57], v[174:177], v[190:193], v[54:57]
	v_mfma_f32_16x16x32_f16 v[50:53], v[182:185], v[190:193], v[50:53]
	v_mfma_f32_16x16x32_f16 v[38:41], v[174:177], v[198:201], v[38:41]
	v_mfma_f32_16x16x32_f16 v[34:37], v[182:185], v[198:201], v[34:37]
	v_mfma_f32_16x16x32_f16 v[22:25], v[174:177], v[206:209], v[22:25]
	v_mfma_f32_16x16x32_f16 v[18:21], v[182:185], v[206:209], v[18:21]
	v_mfma_f32_16x16x32_f16 v[6:9], v[174:177], v[214:217], v[6:9]
	v_mfma_f32_16x16x32_f16 v[2:5], v[182:185], v[214:217], v[2:5]
	v_mfma_f32_16x16x32_f16 v[54:57], v[178:181], v[194:197], v[54:57]
	v_mfma_f32_16x16x32_f16 v[50:53], v[186:189], v[194:197], v[50:53]
	v_mfma_f32_16x16x32_f16 v[38:41], v[178:181], v[202:205], v[38:41]
	v_mfma_f32_16x16x32_f16 v[34:37], v[186:189], v[202:205], v[34:37]
	v_mfma_f32_16x16x32_f16 v[22:25], v[178:181], v[210:213], v[22:25]
	v_mfma_f32_16x16x32_f16 v[18:21], v[186:189], v[210:213], v[18:21]
	v_mfma_f32_16x16x32_f16 v[6:9], v[178:181], v[218:221], v[6:9]
	v_mfma_f32_16x16x32_f16 v[2:5], v[186:189], v[218:221], v[2:5]
	s_barrier
	s_add_u32 s30, s30, 0x40000
	s_addc_u32 s31, s31, 0
	s_mov_b32 m0, s37
	v_lshl_add_u64 v[228:229], s[30:31], 0, v[130:131]
	global_load_lds_dwordx4 v[228:229], off
	v_lshl_add_u64 v[228:229], s[30:31], 0, v[134:135]
	s_mov_b32 m0, s38
	s_nop 0
	global_load_lds_dwordx4 v[228:229], off
	s_mov_b32 s53, 0x1c000
	s_mov_b32 s52, 0x18000
	v_add_u32_e32 v244, s52, v153
	v_add_u32_e32 v245, s53, v153
	ds_read_b128 v[146:149], v244
	ds_read_b128 v[162:165], v244 offset:1024
	ds_read_b128 v[166:169], v244 offset:2048
	ds_read_b128 v[170:173], v244 offset:3072
	ds_read_b128 v[174:177], v245
	ds_read_b128 v[178:181], v245 offset:1024
	ds_read_b128 v[182:185], v245 offset:2048
	ds_read_b128 v[186:189], v245 offset:3072
	ds_read_b128 v[190:193], v160 offset:32768
	ds_read_b128 v[194:197], v160 offset:33792
	ds_read_b128 v[198:201], v160 offset:34816
	ds_read_b128 v[202:205], v160 offset:35840
	ds_read_b128 v[206:209], v160 offset:36864
	ds_read_b128 v[210:213], v160 offset:37888
	ds_read_b128 v[214:217], v160 offset:38912
	ds_read_b128 v[218:221], v160 offset:39936
	s_waitcnt vmcnt(8)
	s_waitcnt lgkmcnt(0)
	s_barrier
	v_mfma_f32_16x16x32_f16 v[126:129], v[146:149], v[190:193], v[126:129]
	v_mfma_f32_16x16x32_f16 v[122:125], v[166:169], v[190:193], v[122:125]
	v_mfma_f32_16x16x32_f16 v[110:113], v[146:149], v[198:201], v[110:113]
	v_mfma_f32_16x16x32_f16 v[106:109], v[166:169], v[198:201], v[106:109]
	v_mfma_f32_16x16x32_f16 v[94:97], v[146:149], v[206:209], v[94:97]
	v_mfma_f32_16x16x32_f16 v[90:93], v[166:169], v[206:209], v[90:93]
	v_mfma_f32_16x16x32_f16 v[78:81], v[146:149], v[214:217], v[78:81]
	v_mfma_f32_16x16x32_f16 v[74:77], v[166:169], v[214:217], v[74:77]
	v_mfma_f32_16x16x32_f16 v[126:129], v[162:165], v[194:197], v[126:129]
	v_mfma_f32_16x16x32_f16 v[122:125], v[170:173], v[194:197], v[122:125]
	v_mfma_f32_16x16x32_f16 v[110:113], v[162:165], v[202:205], v[110:113]
	v_mfma_f32_16x16x32_f16 v[106:109], v[170:173], v[202:205], v[106:109]
	v_mfma_f32_16x16x32_f16 v[94:97], v[162:165], v[210:213], v[94:97]
	v_mfma_f32_16x16x32_f16 v[90:93], v[170:173], v[210:213], v[90:93]
	v_mfma_f32_16x16x32_f16 v[78:81], v[162:165], v[218:221], v[78:81]
	v_mfma_f32_16x16x32_f16 v[74:77], v[170:173], v[218:221], v[74:77]
	v_mfma_f32_16x16x32_f16 v[118:121], v[174:177], v[190:193], v[118:121]
	v_mfma_f32_16x16x32_f16 v[114:117], v[182:185], v[190:193], v[114:117]
	v_mfma_f32_16x16x32_f16 v[102:105], v[174:177], v[198:201], v[102:105]
	v_mfma_f32_16x16x32_f16 v[98:101], v[182:185], v[198:201], v[98:101]
	v_mfma_f32_16x16x32_f16 v[86:89], v[174:177], v[206:209], v[86:89]
	v_mfma_f32_16x16x32_f16 v[82:85], v[182:185], v[206:209], v[82:85]
	v_mfma_f32_16x16x32_f16 v[70:73], v[174:177], v[214:217], v[70:73]
	v_mfma_f32_16x16x32_f16 v[66:69], v[182:185], v[214:217], v[66:69]
	v_mfma_f32_16x16x32_f16 v[118:121], v[178:181], v[194:197], v[118:121]
	v_mfma_f32_16x16x32_f16 v[114:117], v[186:189], v[194:197], v[114:117]
	v_mfma_f32_16x16x32_f16 v[102:105], v[178:181], v[202:205], v[102:105]
	v_mfma_f32_16x16x32_f16 v[98:101], v[186:189], v[202:205], v[98:101]
	v_mfma_f32_16x16x32_f16 v[86:89], v[178:181], v[210:213], v[86:89]
	v_mfma_f32_16x16x32_f16 v[82:85], v[186:189], v[210:213], v[82:85]
	v_mfma_f32_16x16x32_f16 v[70:73], v[178:181], v[218:221], v[70:73]
	v_mfma_f32_16x16x32_f16 v[66:69], v[186:189], v[218:221], v[66:69]
	s_barrier
; #define GM_STAGE(bufoff, gbase, voff) do { _Pragma("unroll") for (int _i = 0; _i < 2; ++_i) \
;         __builtin_amdgcn_global_load_lds((const unsigned*)((const char*)(gbase) + (voff)[_i]), (LAS unsigned*)(lds + (bufoff) + ldsw + _i * 8192), 16, 0, 0); } while (0)
; #define GM_LDA(dst, b, h) do { _Pragma("unroll") for (int m = 0; m < 4; ++m) _Pragma("unroll") for (int k = 0; k < 2; ++k) dst[m][k] = *(const LAS s16x8*)(lds + GM_SA(b, h) + aoff + m * 2048 + k * 1024); } while (0)
; #define GM_MMA(ai, bj, At, Bt) do { __builtin_amdgcn_s_setprio(1); _Pragma("unroll") for (int m = 0; m < 4; ++m) _Pragma("unroll") for (int n = 0; n < 2; ++n) _Pragma("unroll") for (int k = 0; k < 2; ++k) \
;         acc[ai][bj][m][n] = mma16<BF>(Bt[n][k], At[m][k], acc[ai][bj][m][n]); __builtin_amdgcn_s_setprio(0); } while (0)
; #define GM_WAIT_V(n) asm volatile("s_waitcnt vmcnt(" #n ")" ::: "memory")
; #define GM_WAIT_L(n) asm volatile("s_waitcnt lgkmcnt(" #n ")" ::: "memory")
; #define GM_BAR __builtin_amdgcn_s_barrier()
; #define GM_SCHED __builtin_amdgcn_sched_barrier(0)
; #define GM_STA_H0(buf, p, o0) do { if constexpr (GATHER) GM_STAGE(buf, p, o0); else GM_STAGE(buf, p, voffA); } while (0)
; template <bool BF, bool GATHER = false, class Epi, class Hook>
; __device__ __forceinline__ void gemm_phase(LAS unsigned char* lds, const Gemm g, const Order& S, const Epi& E, Hook& HK) {
;     ...
;             GM_LDA(At, 1, 1); GM_STAGE(GM_SB(1, 0), b3, voffB); GM_STAGE(GM_SB(1, 1), b3 + hstepB, voffB); GM_STA_H0(GM_SA(1, 0), a3, s0);
;             GM_WAIT_V(8); GM_WAIT_L(0); GM_BAR; GM_MMA(1, 0, At, B0); GM_MMA(1, 1, At, B1); GM_BAR; GM_SCHED;
;         }
;         if (wr == 0) GM_BAR;
	s_add_i32 s30, s52, s35
	v_lshl_add_u64 v[150:151], v[150:151], 0, s[14:15]
	s_mov_b32 m0, s30
	s_nop 0
	global_load_lds_dwordx4 v[150:151], off
	s_add_i32 m0, s30, 0x2000
	s_add_u32 s28, s28, 0x40080
	v_lshl_add_u64 v[150:151], v[222:223], 0, s[14:15]
	s_addc_u32 s29, s29, 0
	s_add_i32 s30, s53, s35
	global_load_lds_dwordx4 v[150:151], off
	v_lshl_add_u64 v[150:151], s[28:29], 0, v[132:133]
	s_mov_b32 m0, s30
	s_nop 0
	global_load_lds_dwordx4 v[150:151], off
	v_lshl_add_u64 v[150:151], s[28:29], 0, v[136:137]
	s_add_i32 m0, s30, 0x2000
	s_nop 0
	global_load_lds_dwordx4 v[150:151], off
	v_lshl_add_u64 v[150:151], v[224:225], 0, s[14:15]
	s_mov_b32 m0, s42
	s_nop 0
	global_load_lds_dwordx4 v[150:151], off
	v_lshl_add_u64 v[150:151], v[226:227], 0, s[14:15]
	s_mov_b32 m0, s43
	s_nop 0
	global_load_lds_dwordx4 v[150:151], off
	ds_read_b128 v[190:193], v160 offset:49152
	ds_read_b128 v[194:197], v160 offset:50176
	ds_read_b128 v[198:201], v160 offset:51200
	ds_read_b128 v[202:205], v160 offset:52224
	ds_read_b128 v[206:209], v160 offset:53248
	ds_read_b128 v[210:213], v160 offset:54272
	ds_read_b128 v[214:217], v160 offset:55296
	ds_read_b128 v[218:221], v160 offset:56320
	s_waitcnt vmcnt(8)
	s_waitcnt lgkmcnt(0)
	s_barrier
	v_mfma_f32_16x16x32_f16 v[62:65], v[146:149], v[190:193], v[62:65]
	v_mfma_f32_16x16x32_f16 v[58:61], v[166:169], v[190:193], v[58:61]
	v_mfma_f32_16x16x32_f16 v[46:49], v[146:149], v[198:201], v[46:49]
	v_mfma_f32_16x16x32_f16 v[42:45], v[166:169], v[198:201], v[42:45]
	v_mfma_f32_16x16x32_f16 v[30:33], v[146:149], v[206:209], v[30:33]
	v_mfma_f32_16x16x32_f16 v[26:29], v[166:169], v[206:209], v[26:29]
	v_mfma_f32_16x16x32_f16 v[14:17], v[146:149], v[214:217], v[14:17]
	v_mfma_f32_16x16x32_f16 v[10:13], v[166:169], v[214:217], v[10:13]
	v_mfma_f32_16x16x32_f16 v[62:65], v[162:165], v[194:197], v[62:65]
	v_mfma_f32_16x16x32_f16 v[58:61], v[170:173], v[194:197], v[58:61]
	v_mfma_f32_16x16x32_f16 v[46:49], v[162:165], v[202:205], v[46:49]
	v_mfma_f32_16x16x32_f16 v[42:45], v[170:173], v[202:205], v[42:45]
	v_mfma_f32_16x16x32_f16 v[30:33], v[162:165], v[210:213], v[30:33]
	v_mfma_f32_16x16x32_f16 v[26:29], v[170:173], v[210:213], v[26:29]
	v_mfma_f32_16x16x32_f16 v[14:17], v[162:165], v[218:221], v[14:17]
	v_mfma_f32_16x16x32_f16 v[10:13], v[170:173], v[218:221], v[10:13]
	v_mfma_f32_16x16x32_f16 v[54:57], v[174:177], v[190:193], v[54:57]
	v_mfma_f32_16x16x32_f16 v[50:53], v[182:185], v[190:193], v[50:53]
	v_mfma_f32_16x16x32_f16 v[38:41], v[174:177], v[198:201], v[38:41]
	v_mfma_f32_16x16x32_f16 v[34:37], v[182:185], v[198:201], v[34:37]
	v_mfma_f32_16x16x32_f16 v[22:25], v[174:177], v[206:209], v[22:25]
	v_mfma_f32_16x16x32_f16 v[18:21], v[182:185], v[206:209], v[18:21]
	v_mfma_f32_16x16x32_f16 v[6:9], v[174:177], v[214:217], v[6:9]
	v_mfma_f32_16x16x32_f16 v[2:5], v[182:185], v[214:217], v[2:5]
	v_mfma_f32_16x16x32_f16 v[54:57], v[178:181], v[194:197], v[54:57]
	v_mfma_f32_16x16x32_f16 v[50:53], v[186:189], v[194:197], v[50:53]
	v_mfma_f32_16x16x32_f16 v[38:41], v[178:181], v[202:205], v[38:41]
	v_mfma_f32_16x16x32_f16 v[34:37], v[186:189], v[202:205], v[34:37]
	v_mfma_f32_16x16x32_f16 v[22:25], v[178:181], v[210:213], v[22:25]
	v_mfma_f32_16x16x32_f16 v[18:21], v[186:189], v[210:213], v[18:21]
	v_mfma_f32_16x16x32_f16 v[6:9], v[178:181], v[218:221], v[6:9]
	v_mfma_f32_16x16x32_f16 v[2:5], v[186:189], v[218:221], v[2:5]
	s_barrier
	s_add_i32 s51, s51, 2
	s_add_u32 s2, s2, 0x100
	s_addc_u32 s3, s3, 0
	s_add_u32 s49, s49, 0x100
	s_addc_u32 s50, s50, 0
	s_cmp_gt_u32 s51, 13
	s_cbranch_scc0 .LBB0_380
	s_and_b64 vcc, exec, s[16:17]
	s_cbranch_vccz .LBB0_383
	s_barrier

; #define GM_STAGE(bufoff, gbase, voff) do { _Pragma("unroll") for (int _i = 0; _i < 2; ++_i) \
;         __builtin_amdgcn_global_load_lds((const unsigned*)((const char*)(gbase) + (voff)[_i]), (LAS unsigned*)(lds + (bufoff) + ldsw + _i * 8192), 16, 0, 0); } while (0)
; #define GM_LDA(dst, b, h) do { _Pragma("unroll") for (int m = 0; m < 4; ++m) _Pragma("unroll") for (int k = 0; k < 2; ++k) dst[m][k] = *(const LAS s16x8*)(lds + GM_SA(b, h) + aoff + m * 2048 + k * 1024); } while (0)
; #define GM_LDB(dst, b, h) do { _Pragma("unroll") for (int n = 0; n < 2; ++n) _Pragma("unroll") for (int k = 0; k < 2; ++k) dst[n][k] = *(const LAS s16x8*)(lds + GM_SB(b, h) + boff + n * 2048 + k * 1024); } while (0)
; #define GM_MMA(ai, bj, At, Bt) do { __builtin_amdgcn_s_setprio(1); _Pragma("unroll") for (int m = 0; m < 4; ++m) _Pragma("unroll") for (int n = 0; n < 2; ++n) _Pragma("unroll") for (int k = 0; k < 2; ++k) \
;         acc[ai][bj][m][n] = mma16<BF>(Bt[n][k], At[m][k], acc[ai][bj][m][n]); __builtin_amdgcn_s_setprio(0); } while (0)
; #define GM_WAIT_V(n) asm volatile("s_waitcnt vmcnt(" #n ")" ::: "memory")
; #define GM_WAIT_L(n) asm volatile("s_waitcnt lgkmcnt(" #n ")" ::: "memory")
; template <bool BF, bool GATHER = false, class Epi, class Hook>
; __device__ __forceinline__ void gemm_phase(LAS unsigned char* lds, const Gemm g, const Order& S, const Epi& E, Hook& HK) {
;     ...
;             const bool last = (t == nt - 2);
;             const char* a1 = cA + (size_t)(t + 1) * kstep;
;             const char* a2 = last ? nA : cA + (size_t)(t + 2) * kstep; const char* b2 = last ? nB : cB + (size_t)(t + 2) * kstep;
;             const char* a3 = a2 + kstep; const char* b3 = b2 + kstep;
;             unsigned s0[2], s1[2];
;             if constexpr (GATHER) { s0[0] = last ? nA0[0] : gA0[0]; s0[1] = last ? nA0[1] : gA0[1]; s1[0] = last ? nA1[0] : gA1[0]; s1[1] = last ? nA1[1] : gA1[1]; }
;             GM_LDB(B0, 0, 0); GM_LDB(B1, 0, 1); GM_SCHED; GM_LDA(At, 0, 0); GM_STA_H1(GM_SA(1, 1), a1, gA1);
;             GM_WAIT_V(8); GM_WAIT_L(0); GM_BAR; GM_MMA(0, 0, At, B0); GM_MMA(0, 1, At, B1); GM_BAR; GM_SCHED;
;             GM_LDA(At, 0, 1); GM_STAGE(GM_SB(0, 0), b2, voffB); GM_STAGE(GM_SB(0, 1), b2 + hstepB, voffB); GM_STA_H0(GM_SA(0, 0), a2, s0);
;             GM_WAIT_V(8); GM_WAIT_L(0); GM_BAR; GM_MMA(1, 0, At, B0); GM_MMA(1, 1, At, B1); GM_BAR; GM_SCHED;
.LBB0_715:
	s_add_u32 s22, s20, 0xfffc0080
	s_addc_u32 s23, s21, -1
	s_cmp_eq_u32 s47, 12
	s_cselect_b32 s25, s13, s23
	s_cselect_b32 s24, s43, s22
	s_cselect_b32 s23, s15, s46
	s_cselect_b32 s22, s44, s45
	v_lshl_add_u64 v[216:217], s[20:21], 0, v[154:155]
	s_add_i32 m0, s30, 0xc000
	s_nop 0
	global_load_lds_dwordx4 v[216:217], off
	v_lshl_add_u64 v[216:217], s[20:21], 0, v[156:157]
	s_add_i32 m0, s30, 0xe000
	s_nop 0
	global_load_lds_dwordx4 v[216:217], off
	ds_read_b128 v[130:133], v168
	ds_read_b128 v[134:137], v168 offset:1024
	ds_read_b128 v[138:141], v168 offset:2048
	ds_read_b128 v[142:145], v168 offset:3072
	ds_read_b128 v[162:165], v169
	ds_read_b128 v[172:175], v169 offset:1024
	ds_read_b128 v[176:179], v169 offset:2048
	ds_read_b128 v[180:183], v169 offset:3072
	ds_read_b128 v[184:187], v170
	ds_read_b128 v[188:191], v170 offset:1024
	ds_read_b128 v[192:195], v170 offset:2048
	ds_read_b128 v[196:199], v170 offset:3072
	ds_read_b128 v[200:203], v170 offset:4096
	ds_read_b128 v[204:207], v170 offset:5120
	ds_read_b128 v[208:211], v170 offset:6144
	ds_read_b128 v[212:215], v170 offset:7168
	s_waitcnt vmcnt(8)
	s_waitcnt lgkmcnt(0)
	s_barrier
	v_mfma_f32_16x16x32_f16 v[126:129], v[130:133], v[184:187], v[126:129]
	v_mfma_f32_16x16x32_f16 v[122:125], v[138:141], v[184:187], v[122:125]
	v_mfma_f32_16x16x32_f16 v[110:113], v[130:133], v[192:195], v[110:113]
	v_mfma_f32_16x16x32_f16 v[106:109], v[138:141], v[192:195], v[106:109]
	v_mfma_f32_16x16x32_f16 v[94:97], v[130:133], v[200:203], v[94:97]
	v_mfma_f32_16x16x32_f16 v[90:93], v[138:141], v[200:203], v[90:93]
	v_mfma_f32_16x16x32_f16 v[78:81], v[130:133], v[208:211], v[78:81]
	v_mfma_f32_16x16x32_f16 v[74:77], v[138:141], v[208:211], v[74:77]
	v_mfma_f32_16x16x32_f16 v[126:129], v[134:137], v[188:191], v[126:129]
	v_mfma_f32_16x16x32_f16 v[122:125], v[142:145], v[188:191], v[122:125]
	v_mfma_f32_16x16x32_f16 v[110:113], v[134:137], v[196:199], v[110:113]
	v_mfma_f32_16x16x32_f16 v[106:109], v[142:145], v[196:199], v[106:109]
	v_mfma_f32_16x16x32_f16 v[94:97], v[134:137], v[204:207], v[94:97]
	v_mfma_f32_16x16x32_f16 v[90:93], v[142:145], v[204:207], v[90:93]
	v_mfma_f32_16x16x32_f16 v[78:81], v[134:137], v[212:215], v[78:81]
	v_mfma_f32_16x16x32_f16 v[74:77], v[142:145], v[212:215], v[74:77]
	v_mfma_f32_16x16x32_f16 v[118:121], v[162:165], v[184:187], v[118:121]
	v_mfma_f32_16x16x32_f16 v[114:117], v[176:179], v[184:187], v[114:117]
	v_mfma_f32_16x16x32_f16 v[102:105], v[162:165], v[192:195], v[102:105]
	v_mfma_f32_16x16x32_f16 v[98:101], v[176:179], v[192:195], v[98:101]
	v_mfma_f32_16x16x32_f16 v[86:89], v[162:165], v[200:203], v[86:89]
	v_mfma_f32_16x16x32_f16 v[82:85], v[176:179], v[200:203], v[82:85]
	v_mfma_f32_16x16x32_f16 v[70:73], v[162:165], v[208:211], v[70:73]
	v_mfma_f32_16x16x32_f16 v[66:69], v[176:179], v[208:211], v[66:69]
	v_mfma_f32_16x16x32_f16 v[118:121], v[172:175], v[188:191], v[118:121]
	v_mfma_f32_16x16x32_f16 v[114:117], v[180:183], v[188:191], v[114:117]
	v_mfma_f32_16x16x32_f16 v[102:105], v[172:175], v[196:199], v[102:105]
	v_mfma_f32_16x16x32_f16 v[98:101], v[180:183], v[196:199], v[98:101]
	v_mfma_f32_16x16x32_f16 v[86:89], v[172:175], v[204:207], v[86:89]
	v_mfma_f32_16x16x32_f16 v[82:85], v[180:183], v[204:207], v[82:85]
	v_mfma_f32_16x16x32_f16 v[70:73], v[172:175], v[212:215], v[70:73]
	v_mfma_f32_16x16x32_f16 v[66:69], v[180:183], v[212:215], v[66:69]
	s_barrier
	s_add_i32 s48, s41, s29
	v_lshl_add_u64 v[216:217], s[22:23], 0, v[148:149]
	s_mov_b32 m0, s48
	s_nop 0
	global_load_lds_dwordx4 v[216:217], off
	s_add_i32 m0, s48, 0x2000
	s_add_u32 s48, s22, 0x40000
	v_lshl_add_u64 v[218:219], s[22:23], 0, v[152:153]
	s_addc_u32 s49, s23, 0
	s_add_i32 s50, s42, s29
	global_load_lds_dwordx4 v[218:219], off
	v_lshl_add_u64 v[220:221], s[48:49], 0, v[148:149]
	s_mov_b32 m0, s50
	v_lshl_add_u64 v[222:223], s[24:25], 0, v[150:151]
	global_load_lds_dwordx4 v[220:221], off
	v_lshl_add_u64 v[220:221], s[48:49], 0, v[152:153]
	s_add_i32 m0, s50, 0x2000
	s_nop 0
	global_load_lds_dwordx4 v[220:221], off
	v_lshl_add_u64 v[220:221], s[24:25], 0, v[146:147]
	s_mov_b32 m0, s30
	s_nop 0
	global_load_lds_dwordx4 v[220:221], off
	s_mov_b32 m0, s31
	s_nop 0
	global_load_lds_dwordx4 v[222:223], off
	ds_read_b128 v[184:187], v170 offset:16384
	ds_read_b128 v[188:191], v170 offset:17408
	ds_read_b128 v[192:195], v170 offset:18432
	ds_read_b128 v[196:199], v170 offset:19456
	ds_read_b128 v[200:203], v170 offset:20480
	ds_read_b128 v[204:207], v170 offset:21504
	ds_read_b128 v[208:211], v170 offset:22528
	ds_read_b128 v[212:215], v170 offset:23552
	s_waitcnt vmcnt(8)
	s_waitcnt lgkmcnt(0)
	s_barrier
; #define GM_LDA(dst, b, h) do { _Pragma("unroll") for (int m = 0; m < 4; ++m) _Pragma("unroll") for (int k = 0; k < 2; ++k) dst[m][k] = *(const LAS s16x8*)(lds + GM_SA(b, h) + aoff + m * 2048 + k * 1024); } while (0)
; #define GM_LDB(dst, b, h) do { _Pragma("unroll") for (int n = 0; n < 2; ++n) _Pragma("unroll") for (int k = 0; k < 2; ++k) dst[n][k] = *(const LAS s16x8*)(lds + GM_SB(b, h) + boff + n * 2048 + k * 1024); } while (0)
; #define GM_MMA(ai, bj, At, Bt) do { __builtin_amdgcn_s_setprio(1); _Pragma("unroll") for (int m = 0; m < 4; ++m) _Pragma("unroll") for (int n = 0; n < 2; ++n) _Pragma("unroll") for (int k = 0; k < 2; ++k) \
;         acc[ai][bj][m][n] = mma16<BF>(Bt[n][k], At[m][k], acc[ai][bj][m][n]); __builtin_amdgcn_s_setprio(0); } while (0)
; #define GM_WAIT_V(n) asm volatile("s_waitcnt vmcnt(" #n ")" ::: "memory")
; #define GM_WAIT_L(n) asm volatile("s_waitcnt lgkmcnt(" #n ")" ::: "memory")
; #define GM_BAR __builtin_amdgcn_s_barrier()
; #define GM_SCHED __builtin_amdgcn_sched_barrier(0)
; #define GM_STA_H1(buf, p, o1) do { if constexpr (GATHER) GM_STAGE(buf, p, o1); else GM_STAGE(buf, (p) + hstepB, voffA); } while (0)
; template <bool BF, bool GATHER = false, class Epi, class Hook>
; __device__ __forceinline__ void gemm_phase(LAS unsigned char* lds, const Gemm g, const Order& S, const Epi& E, Hook& HK) {
;     ...
;             GM_WAIT_V(8); GM_WAIT_L(0); GM_BAR; GM_MMA(1, 0, At, B0); GM_MMA(1, 1, At, B1); GM_BAR; GM_SCHED;
;             GM_LDB(B0, 1, 0); GM_LDB(B1, 1, 1); GM_SCHED; GM_LDA(At, 1, 0); GM_STA_H1(GM_SA(0, 1), a2, s1);
;             GM_WAIT_V(8); GM_WAIT_L(0); GM_BAR; GM_MMA(0, 0, At, B0); GM_MMA(0, 1, At, B1); GM_BAR; GM_SCHED;
	v_mfma_f32_16x16x32_f16 v[62:65], v[130:133], v[184:187], v[62:65]
	v_mfma_f32_16x16x32_f16 v[58:61], v[138:141], v[184:187], v[58:61]
	v_mfma_f32_16x16x32_f16 v[46:49], v[130:133], v[192:195], v[46:49]
	v_mfma_f32_16x16x32_f16 v[42:45], v[138:141], v[192:195], v[42:45]
	v_mfma_f32_16x16x32_f16 v[30:33], v[130:133], v[200:203], v[30:33]
	v_mfma_f32_16x16x32_f16 v[26:29], v[138:141], v[200:203], v[26:29]
	v_mfma_f32_16x16x32_f16 v[14:17], v[130:133], v[208:211], v[14:17]
	v_mfma_f32_16x16x32_f16 v[10:13], v[138:141], v[208:211], v[10:13]
	v_mfma_f32_16x16x32_f16 v[62:65], v[134:137], v[188:191], v[62:65]
	v_mfma_f32_16x16x32_f16 v[58:61], v[142:145], v[188:191], v[58:61]
	v_mfma_f32_16x16x32_f16 v[46:49], v[134:137], v[196:199], v[46:49]
	v_mfma_f32_16x16x32_f16 v[42:45], v[142:145], v[196:199], v[42:45]
	v_mfma_f32_16x16x32_f16 v[30:33], v[134:137], v[204:207], v[30:33]
	v_mfma_f32_16x16x32_f16 v[26:29], v[142:145], v[204:207], v[26:29]
	v_mfma_f32_16x16x32_f16 v[14:17], v[134:137], v[212:215], v[14:17]
	v_mfma_f32_16x16x32_f16 v[10:13], v[142:145], v[212:215], v[10:13]
	v_mfma_f32_16x16x32_f16 v[54:57], v[162:165], v[184:187], v[54:57]
	v_mfma_f32_16x16x32_f16 v[50:53], v[176:179], v[184:187], v[50:53]
	v_mfma_f32_16x16x32_f16 v[38:41], v[162:165], v[192:195], v[38:41]
	v_mfma_f32_16x16x32_f16 v[34:37], v[176:179], v[192:195], v[34:37]
	v_mfma_f32_16x16x32_f16 v[22:25], v[162:165], v[200:203], v[22:25]
	v_mfma_f32_16x16x32_f16 v[18:21], v[176:179], v[200:203], v[18:21]
	v_mfma_f32_16x16x32_f16 v[6:9], v[162:165], v[208:211], v[6:9]
	v_mfma_f32_16x16x32_f16 v[2:5], v[176:179], v[208:211], v[2:5]
	v_mfma_f32_16x16x32_f16 v[54:57], v[172:175], v[188:191], v[54:57]
	v_mfma_f32_16x16x32_f16 v[50:53], v[180:183], v[188:191], v[50:53]
	v_mfma_f32_16x16x32_f16 v[38:41], v[172:175], v[196:199], v[38:41]
	v_mfma_f32_16x16x32_f16 v[34:37], v[180:183], v[196:199], v[34:37]
	v_mfma_f32_16x16x32_f16 v[22:25], v[172:175], v[204:207], v[22:25]
	v_mfma_f32_16x16x32_f16 v[18:21], v[180:183], v[204:207], v[18:21]
	v_mfma_f32_16x16x32_f16 v[6:9], v[172:175], v[212:215], v[6:9]
	v_mfma_f32_16x16x32_f16 v[2:5], v[180:183], v[212:215], v[2:5]
	s_barrier
	s_add_u32 s24, s24, 0x40000
	s_addc_u32 s25, s25, 0
	s_mov_b32 m0, s33
	v_lshl_add_u64 v[224:225], s[24:25], 0, v[146:147]
	global_load_lds_dwordx4 v[224:225], off
	v_lshl_add_u64 v[224:225], s[24:25], 0, v[150:151]
	s_mov_b32 m0, s34
	s_nop 0
	global_load_lds_dwordx4 v[224:225], off
	s_mov_b32 s49, 0x1c000
	s_mov_b32 s48, 0x18000
	v_add_u32_e32 v244, s48, v166
	v_add_u32_e32 v245, s49, v166
	ds_read_b128 v[130:133], v244
	ds_read_b128 v[134:137], v244 offset:1024
	ds_read_b128 v[138:141], v244 offset:2048
	ds_read_b128 v[142:145], v244 offset:3072
	ds_read_b128 v[162:165], v245
	ds_read_b128 v[172:175], v245 offset:1024
	ds_read_b128 v[176:179], v245 offset:2048
	ds_read_b128 v[180:183], v245 offset:3072
	ds_read_b128 v[184:187], v170 offset:32768
	ds_read_b128 v[188:191], v170 offset:33792
	ds_read_b128 v[192:195], v170 offset:34816
	ds_read_b128 v[196:199], v170 offset:35840
	ds_read_b128 v[200:203], v170 offset:36864
	ds_read_b128 v[204:207], v170 offset:37888
	ds_read_b128 v[208:211], v170 offset:38912
	ds_read_b128 v[212:215], v170 offset:39936
	s_waitcnt vmcnt(8)
	s_waitcnt lgkmcnt(0)
	s_barrier
	v_mfma_f32_16x16x32_f16 v[126:129], v[130:133], v[184:187], v[126:129]
	v_mfma_f32_16x16x32_f16 v[122:125], v[138:141], v[184:187], v[122:125]
	v_mfma_f32_16x16x32_f16 v[110:113], v[130:133], v[192:195], v[110:113]
	v_mfma_f32_16x16x32_f16 v[106:109], v[138:141], v[192:195], v[106:109]
	v_mfma_f32_16x16x32_f16 v[94:97], v[130:133], v[200:203], v[94:97]
	v_mfma_f32_16x16x32_f16 v[90:93], v[138:141], v[200:203], v[90:93]
	v_mfma_f32_16x16x32_f16 v[78:81], v[130:133], v[208:211], v[78:81]
	v_mfma_f32_16x16x32_f16 v[74:77], v[138:141], v[208:211], v[74:77]
	v_mfma_f32_16x16x32_f16 v[126:129], v[134:137], v[188:191], v[126:129]
	v_mfma_f32_16x16x32_f16 v[122:125], v[142:145], v[188:191], v[122:125]
	v_mfma_f32_16x16x32_f16 v[110:113], v[134:137], v[196:199], v[110:113]
	v_mfma_f32_16x16x32_f16 v[106:109], v[142:145], v[196:199], v[106:109]
	v_mfma_f32_16x16x32_f16 v[94:97], v[134:137], v[204:207], v[94:97]
	v_mfma_f32_16x16x32_f16 v[90:93], v[142:145], v[204:207], v[90:93]
	v_mfma_f32_16x16x32_f16 v[78:81], v[134:137], v[212:215], v[78:81]
	v_mfma_f32_16x16x32_f16 v[74:77], v[142:145], v[212:215], v[74:77]
	v_mfma_f32_16x16x32_f16 v[118:121], v[162:165], v[184:187], v[118:121]
	v_mfma_f32_16x16x32_f16 v[114:117], v[176:179], v[184:187], v[114:117]
	v_mfma_f32_16x16x32_f16 v[102:105], v[162:165], v[192:195], v[102:105]
	v_mfma_f32_16x16x32_f16 v[98:101], v[176:179], v[192:195], v[98:101]
	v_mfma_f32_16x16x32_f16 v[86:89], v[162:165], v[200:203], v[86:89]
	v_mfma_f32_16x16x32_f16 v[82:85], v[176:179], v[200:203], v[82:85]
	v_mfma_f32_16x16x32_f16 v[70:73], v[162:165], v[208:211], v[70:73]
	v_mfma_f32_16x16x32_f16 v[66:69], v[176:179], v[208:211], v[66:69]
	v_mfma_f32_16x16x32_f16 v[118:121], v[172:175], v[188:191], v[118:121]
	v_mfma_f32_16x16x32_f16 v[114:117], v[180:183], v[188:191], v[114:117]
	v_mfma_f32_16x16x32_f16 v[102:105], v[172:175], v[196:199], v[102:105]
	v_mfma_f32_16x16x32_f16 v[98:101], v[180:183], v[196:199], v[98:101]
	v_mfma_f32_16x16x32_f16 v[86:89], v[172:175], v[204:207], v[86:89]
	v_mfma_f32_16x16x32_f16 v[82:85], v[180:183], v[204:207], v[82:85]
	v_mfma_f32_16x16x32_f16 v[70:73], v[172:175], v[212:215], v[70:73]
	v_mfma_f32_16x16x32_f16 v[66:69], v[180:183], v[212:215], v[66:69]
	s_barrier
; #define GM_STAGE(bufoff, gbase, voff) do { _Pragma("unroll") for (int _i = 0; _i < 2; ++_i) \
;         __builtin_amdgcn_global_load_lds((const unsigned*)((const char*)(gbase) + (voff)[_i]), (LAS unsigned*)(lds + (bufoff) + ldsw + _i * 8192), 16, 0, 0); } while (0)
; #define GM_LDA(dst, b, h) do { _Pragma("unroll") for (int m = 0; m < 4; ++m) _Pragma("unroll") for (int k = 0; k < 2; ++k) dst[m][k] = *(const LAS s16x8*)(lds + GM_SA(b, h) + aoff + m * 2048 + k * 1024); } while (0)
; #define GM_MMA(ai, bj, At, Bt) do { __builtin_amdgcn_s_setprio(1); _Pragma("unroll") for (int m = 0; m < 4; ++m) _Pragma("unroll") for (int n = 0; n < 2; ++n) _Pragma("unroll") for (int k = 0; k < 2; ++k) \
;         acc[ai][bj][m][n] = mma16<BF>(Bt[n][k], At[m][k], acc[ai][bj][m][n]); __builtin_amdgcn_s_setprio(0); } while (0)
; #define GM_WAIT_V(n) asm volatile("s_waitcnt vmcnt(" #n ")" ::: "memory")
; #define GM_WAIT_L(n) asm volatile("s_waitcnt lgkmcnt(" #n ")" ::: "memory")
; #define GM_BAR __builtin_amdgcn_s_barrier()
; #define GM_SCHED __builtin_amdgcn_sched_barrier(0)
; #define GM_STA_H0(buf, p, o0) do { if constexpr (GATHER) GM_STAGE(buf, p, o0); else GM_STAGE(buf, p, voffA); } while (0)
; template <bool BF, bool GATHER = false, class Epi, class Hook>
; __device__ __forceinline__ void gemm_phase(LAS unsigned char* lds, const Gemm g, const Order& S, const Epi& E, Hook& HK) {
;     ...
;             GM_LDA(At, 1, 1); GM_STAGE(GM_SB(1, 0), b3, voffB); GM_STAGE(GM_SB(1, 1), b3 + hstepB, voffB); GM_STA_H0(GM_SA(1, 0), a3, s0);
;             GM_WAIT_V(8); GM_WAIT_L(0); GM_BAR; GM_MMA(1, 0, At, B0); GM_MMA(1, 1, At, B1); GM_BAR; GM_SCHED;
;         }
;         if (wr == 0) GM_BAR;
	s_add_i32 s24, s48, s29
	v_lshl_add_u64 v[216:217], v[216:217], 0, s[8:9]
	s_mov_b32 m0, s24
	s_nop 0
	global_load_lds_dwordx4 v[216:217], off
	s_add_i32 m0, s24, 0x2000
	s_add_u32 s22, s22, 0x40080
	v_lshl_add_u64 v[216:217], v[218:219], 0, s[8:9]
	s_addc_u32 s23, s23, 0
	s_add_i32 s24, s49, s29
	global_load_lds_dwordx4 v[216:217], off
	v_lshl_add_u64 v[216:217], s[22:23], 0, v[148:149]
	s_mov_b32 m0, s24
	s_nop 0
	global_load_lds_dwordx4 v[216:217], off
	v_lshl_add_u64 v[216:217], s[22:23], 0, v[152:153]
	s_add_i32 m0, s24, 0x2000
	s_nop 0
	global_load_lds_dwordx4 v[216:217], off
	v_lshl_add_u64 v[216:217], v[220:221], 0, s[8:9]
	s_mov_b32 m0, s38
	s_nop 0
	global_load_lds_dwordx4 v[216:217], off
	v_lshl_add_u64 v[216:217], v[222:223], 0, s[8:9]
	s_mov_b32 m0, s39
	s_nop 0
	global_load_lds_dwordx4 v[216:217], off
	ds_read_b128 v[184:187], v170 offset:49152
	ds_read_b128 v[188:191], v170 offset:50176
	ds_read_b128 v[192:195], v170 offset:51200
	ds_read_b128 v[196:199], v170 offset:52224
	ds_read_b128 v[200:203], v170 offset:53248
	ds_read_b128 v[204:207], v170 offset:54272
	ds_read_b128 v[208:211], v170 offset:55296
	ds_read_b128 v[212:215], v170 offset:56320
	s_waitcnt vmcnt(8)
	s_waitcnt lgkmcnt(0)
	s_barrier
	v_mfma_f32_16x16x32_f16 v[62:65], v[130:133], v[184:187], v[62:65]
	v_mfma_f32_16x16x32_f16 v[58:61], v[138:141], v[184:187], v[58:61]
	v_mfma_f32_16x16x32_f16 v[46:49], v[130:133], v[192:195], v[46:49]
	v_mfma_f32_16x16x32_f16 v[42:45], v[138:141], v[192:195], v[42:45]
	v_mfma_f32_16x16x32_f16 v[30:33], v[130:133], v[200:203], v[30:33]
	v_mfma_f32_16x16x32_f16 v[26:29], v[138:141], v[200:203], v[26:29]
	v_mfma_f32_16x16x32_f16 v[14:17], v[130:133], v[208:211], v[14:17]
	v_mfma_f32_16x16x32_f16 v[10:13], v[138:141], v[208:211], v[10:13]
	v_mfma_f32_16x16x32_f16 v[62:65], v[134:137], v[188:191], v[62:65]
	v_mfma_f32_16x16x32_f16 v[58:61], v[142:145], v[188:191], v[58:61]
	v_mfma_f32_16x16x32_f16 v[46:49], v[134:137], v[196:199], v[46:49]
	v_mfma_f32_16x16x32_f16 v[42:45], v[142:145], v[196:199], v[42:45]
	v_mfma_f32_16x16x32_f16 v[30:33], v[134:137], v[204:207], v[30:33]
	v_mfma_f32_16x16x32_f16 v[26:29], v[142:145], v[204:207], v[26:29]
	v_mfma_f32_16x16x32_f16 v[14:17], v[134:137], v[212:215], v[14:17]
	v_mfma_f32_16x16x32_f16 v[10:13], v[142:145], v[212:215], v[10:13]
	v_mfma_f32_16x16x32_f16 v[54:57], v[162:165], v[184:187], v[54:57]
	v_mfma_f32_16x16x32_f16 v[50:53], v[176:179], v[184:187], v[50:53]
	v_mfma_f32_16x16x32_f16 v[38:41], v[162:165], v[192:195], v[38:41]
	v_mfma_f32_16x16x32_f16 v[34:37], v[176:179], v[192:195], v[34:37]
	v_mfma_f32_16x16x32_f16 v[22:25], v[162:165], v[200:203], v[22:25]
	v_mfma_f32_16x16x32_f16 v[18:21], v[176:179], v[200:203], v[18:21]
	v_mfma_f32_16x16x32_f16 v[6:9], v[162:165], v[208:211], v[6:9]
	v_mfma_f32_16x16x32_f16 v[2:5], v[176:179], v[208:211], v[2:5]
	v_mfma_f32_16x16x32_f16 v[54:57], v[172:175], v[188:191], v[54:57]
	v_mfma_f32_16x16x32_f16 v[50:53], v[180:183], v[188:191], v[50:53]
	v_mfma_f32_16x16x32_f16 v[38:41], v[172:175], v[196:199], v[38:41]
	v_mfma_f32_16x16x32_f16 v[34:37], v[180:183], v[196:199], v[34:37]
	v_mfma_f32_16x16x32_f16 v[22:25], v[172:175], v[204:207], v[22:25]
	v_mfma_f32_16x16x32_f16 v[18:21], v[180:183], v[204:207], v[18:21]
	v_mfma_f32_16x16x32_f16 v[6:9], v[172:175], v[212:215], v[6:9]
	v_mfma_f32_16x16x32_f16 v[2:5], v[180:183], v[212:215], v[2:5]
	s_barrier
	s_add_i32 s47, s47, 2
	s_add_u32 s20, s20, 0x100
	s_addc_u32 s21, s21, 0
	s_add_u32 s45, s45, 0x100
	s_addc_u32 s46, s46, 0
	s_cmp_gt_u32 s47, 13
	s_cbranch_scc0 .LBB0_715
	s_and_b64 vcc, exec, s[10:11]
	s_cbranch_vccz .LBB0_718
	s_barrier

; #define GM_STAGE(bufoff, gbase, voff) do { _Pragma("unroll") for (int _i = 0; _i < 2; ++_i) \
;         __builtin_amdgcn_global_load_lds((const unsigned*)((const char*)(gbase) + (voff)[_i]), (LAS unsigned*)(lds + (bufoff) + ldsw + _i * 8192), 16, 0, 0); } while (0)
; #define GM_LDA(dst, b, h) do { _Pragma("unroll") for (int m = 0; m < 4; ++m) _Pragma("unroll") for (int k = 0; k < 2; ++k) dst[m][k] = *(const LAS s16x8*)(lds + GM_SA(b, h) + aoff + m * 2048 + k * 1024); } while (0)
; #define GM_LDB(dst, b, h) do { _Pragma("unroll") for (int n = 0; n < 2; ++n) _Pragma("unroll") for (int k = 0; k < 2; ++k) dst[n][k] = *(const LAS s16x8*)(lds + GM_SB(b, h) + boff + n * 2048 + k * 1024); } while (0)
; #define GM_MMA(ai, bj, At, Bt) do { __builtin_amdgcn_s_setprio(1); _Pragma("unroll") for (int m = 0; m < 4; ++m) _Pragma("unroll") for (int n = 0; n < 2; ++n) _Pragma("unroll") for (int k = 0; k < 2; ++k) \
;         acc[ai][bj][m][n] = mma16<BF>(Bt[n][k], At[m][k], acc[ai][bj][m][n]); __builtin_amdgcn_s_setprio(0); } while (0)
; #define GM_WAIT_V(n) asm volatile("s_waitcnt vmcnt(" #n ")" ::: "memory")
; #define GM_WAIT_L(n) asm volatile("s_waitcnt lgkmcnt(" #n ")" ::: "memory")
; template <bool BF, bool GATHER = false, class Epi, class Hook>
; __device__ __forceinline__ void gemm_phase(LAS unsigned char* lds, const Gemm g, const Order& S, const Epi& E, Hook& HK) {
;     ...
;             const bool last = (t == nt - 2);
;             const char* a1 = cA + (size_t)(t + 1) * kstep;
;             const char* a2 = last ? nA : cA + (size_t)(t + 2) * kstep; const char* b2 = last ? nB : cB + (size_t)(t + 2) * kstep;
;             const char* a3 = a2 + kstep; const char* b3 = b2 + kstep;
;             unsigned s0[2], s1[2];
;             if constexpr (GATHER) { s0[0] = last ? nA0[0] : gA0[0]; s0[1] = last ? nA0[1] : gA0[1]; s1[0] = last ? nA1[0] : gA1[0]; s1[1] = last ? nA1[1] : gA1[1]; }
;             GM_LDB(B0, 0, 0); GM_LDB(B1, 0, 1); GM_SCHED; GM_LDA(At, 0, 0); GM_STA_H1(GM_SA(1, 1), a1, gA1);
;             GM_WAIT_V(8); GM_WAIT_L(0); GM_BAR; GM_MMA(0, 0, At, B0); GM_MMA(0, 1, At, B1); GM_BAR; GM_SCHED;
;             GM_LDA(At, 0, 1); GM_STAGE(GM_SB(0, 0), b2, voffB); GM_STAGE(GM_SB(0, 1), b2 + hstepB, voffB); GM_STA_H0(GM_SA(0, 0), a2, s0);
;             GM_WAIT_V(8); GM_WAIT_L(0); GM_BAR; GM_MMA(1, 0, At, B0); GM_MMA(1, 1, At, B1); GM_BAR; GM_SCHED;
.LBB0_1011:
	s_add_u32 s22, s90, s2
	s_addc_u32 s23, s91, s3
	s_add_u32 s24, s22, 0x11e00100
	s_addc_u32 s25, s23, 0
	s_add_u32 s44, s21, s2
	s_addc_u32 s45, s42, s3
	s_cmpk_eq_i32 s2, 0x700
	s_cselect_b64 vcc, -1, 0
	s_and_b64 s[22:23], vcc, exec
	v_cndmask_b32_e32 v134, v142, v159, vcc
	s_cselect_b32 s25, s69, s25
	s_cselect_b32 s24, s68, s24
	v_cndmask_b32_e32 v228, v146, v162, vcc
	v_cndmask_b32_e32 v141, v158, v160, vcc
	v_cndmask_b32_e32 v145, v157, v161, vcc
	s_cselect_b32 s23, s1, s45
	s_cselect_b32 s22, s0, s44
	v_lshl_add_u64 v[230:231], v[150:151], 0, s[2:3]
	s_add_i32 m0, s28, 0xc000
	s_nop 0
	global_load_lds_dwordx4 v[230:231], off
	v_lshl_add_u64 v[230:231], v[148:149], 0, s[2:3]
	s_add_i32 m0, s28, 0xe000
	s_nop 0
	global_load_lds_dwordx4 v[230:231], off
	v_add_u32_e32 v244, s35, v156
	ds_read_b128 v[164:167], v244
	ds_read_b128 v[168:171], v244 offset:1024
	ds_read_b128 v[172:175], v244 offset:2048
	ds_read_b128 v[176:179], v244 offset:3072
	v_add_u32_e32 v244, s36, v156
	ds_read_b128 v[180:183], v244
	ds_read_b128 v[184:187], v244 offset:1024
	ds_read_b128 v[188:191], v244 offset:2048
	ds_read_b128 v[192:195], v244 offset:3072
	ds_read_b128 v[196:199], v147
	ds_read_b128 v[200:203], v147 offset:1024
	ds_read_b128 v[204:207], v147 offset:2048
	ds_read_b128 v[208:211], v147 offset:3072
	ds_read_b128 v[212:215], v147 offset:4096
	ds_read_b128 v[216:219], v147 offset:5120
	ds_read_b128 v[220:223], v147 offset:6144
	ds_read_b128 v[224:227], v147 offset:7168
	s_waitcnt vmcnt(8)
	s_waitcnt lgkmcnt(0)
	s_barrier
	v_mfma_f32_16x16x32_bf16 v[98:101], v[164:167], v[196:199], v[98:101]
	v_mfma_f32_16x16x32_bf16 v[94:97], v[172:175], v[196:199], v[94:97]
	v_mfma_f32_16x16x32_bf16 v[90:93], v[164:167], v[204:207], v[90:93]
	v_mfma_f32_16x16x32_bf16 v[86:89], v[172:175], v[204:207], v[86:89]
	v_mfma_f32_16x16x32_bf16 v[82:85], v[164:167], v[212:215], v[82:85]
	v_mfma_f32_16x16x32_bf16 v[78:81], v[172:175], v[212:215], v[78:81]
	v_mfma_f32_16x16x32_bf16 v[74:77], v[164:167], v[220:223], v[74:77]
	v_mfma_f32_16x16x32_bf16 v[70:73], v[172:175], v[220:223], v[70:73]
	v_mfma_f32_16x16x32_bf16 v[98:101], v[168:171], v[200:203], v[98:101]
	v_mfma_f32_16x16x32_bf16 v[94:97], v[176:179], v[200:203], v[94:97]
	v_mfma_f32_16x16x32_bf16 v[90:93], v[168:171], v[208:211], v[90:93]
	v_mfma_f32_16x16x32_bf16 v[86:89], v[176:179], v[208:211], v[86:89]
	v_mfma_f32_16x16x32_bf16 v[82:85], v[168:171], v[216:219], v[82:85]
	v_mfma_f32_16x16x32_bf16 v[78:81], v[176:179], v[216:219], v[78:81]
	v_mfma_f32_16x16x32_bf16 v[74:77], v[168:171], v[224:227], v[74:77]
	v_mfma_f32_16x16x32_bf16 v[70:73], v[176:179], v[224:227], v[70:73]
	v_mfma_f32_16x16x32_bf16 v[66:69], v[180:183], v[196:199], v[66:69]
	v_mfma_f32_16x16x32_bf16 v[62:65], v[188:191], v[196:199], v[62:65]
	v_mfma_f32_16x16x32_bf16 v[58:61], v[180:183], v[204:207], v[58:61]
	v_mfma_f32_16x16x32_bf16 v[54:57], v[188:191], v[204:207], v[54:57]
	v_mfma_f32_16x16x32_bf16 v[50:53], v[180:183], v[212:215], v[50:53]
	v_mfma_f32_16x16x32_bf16 v[46:49], v[188:191], v[212:215], v[46:49]
	v_mfma_f32_16x16x32_bf16 v[42:45], v[180:183], v[220:223], v[42:45]
	v_mfma_f32_16x16x32_bf16 v[38:41], v[188:191], v[220:223], v[38:41]
	v_mfma_f32_16x16x32_bf16 v[66:69], v[184:187], v[200:203], v[66:69]
	v_mfma_f32_16x16x32_bf16 v[62:65], v[192:195], v[200:203], v[62:65]
	v_mfma_f32_16x16x32_bf16 v[58:61], v[184:187], v[208:211], v[58:61]
	v_mfma_f32_16x16x32_bf16 v[54:57], v[192:195], v[208:211], v[54:57]
	v_mfma_f32_16x16x32_bf16 v[50:53], v[184:187], v[216:219], v[50:53]
	v_mfma_f32_16x16x32_bf16 v[46:49], v[192:195], v[216:219], v[46:49]
	v_mfma_f32_16x16x32_bf16 v[42:45], v[184:187], v[224:227], v[42:45]
	v_mfma_f32_16x16x32_bf16 v[38:41], v[192:195], v[224:227], v[38:41]
	s_barrier
	s_add_i32 s44, s35, s11
	v_lshl_add_u64 v[230:231], s[22:23], 0, v[130:131]
	s_mov_b32 m0, s44
	s_nop 0
	global_load_lds_dwordx4 v[230:231], off
	s_add_i32 m0, s44, 0x2000
	s_add_u32 s44, s22, 0x40000
	v_lshl_add_u64 v[232:233], s[22:23], 0, v[132:133]
	s_addc_u32 s45, s23, 0
	s_add_i32 s46, s36, s11
	global_load_lds_dwordx4 v[232:233], off
	v_lshl_add_u64 v[234:235], s[44:45], 0, v[130:131]
	s_mov_b32 m0, s46
	v_mov_b32_e32 v229, v135
	global_load_lds_dwordx4 v[234:235], off
	v_lshl_add_u64 v[234:235], s[44:45], 0, v[132:133]
	s_add_i32 m0, s46, 0x2000
	s_nop 0
	global_load_lds_dwordx4 v[234:235], off
	s_mov_b32 m0, s28
	v_lshl_add_u64 v[234:235], s[24:25], 0, v[134:135]
	global_load_lds_dwordx4 v134, s[24:25]
	s_mov_b32 m0, s29
	s_nop 0
	global_load_lds_dwordx4 v228, s[24:25]
	v_lshl_add_u64 v[228:229], s[24:25], 0, v[228:229]
	ds_read_b128 v[196:199], v147 offset:16384
	ds_read_b128 v[200:203], v147 offset:17408
	ds_read_b128 v[204:207], v147 offset:18432
	ds_read_b128 v[208:211], v147 offset:19456
	ds_read_b128 v[212:215], v147 offset:20480
	ds_read_b128 v[216:219], v147 offset:21504
	ds_read_b128 v[220:223], v147 offset:22528
	ds_read_b128 v[224:227], v147 offset:23552
	s_waitcnt vmcnt(8)
	s_waitcnt lgkmcnt(0)
	s_barrier
; #define GM_LDA(dst, b, h) do { _Pragma("unroll") for (int m = 0; m < 4; ++m) _Pragma("unroll") for (int k = 0; k < 2; ++k) dst[m][k] = *(const LAS s16x8*)(lds + GM_SA(b, h) + aoff + m * 2048 + k * 1024); } while (0)
; #define GM_LDB(dst, b, h) do { _Pragma("unroll") for (int n = 0; n < 2; ++n) _Pragma("unroll") for (int k = 0; k < 2; ++k) dst[n][k] = *(const LAS s16x8*)(lds + GM_SB(b, h) + boff + n * 2048 + k * 1024); } while (0)
; #define GM_MMA(ai, bj, At, Bt) do { __builtin_amdgcn_s_setprio(1); _Pragma("unroll") for (int m = 0; m < 4; ++m) _Pragma("unroll") for (int n = 0; n < 2; ++n) _Pragma("unroll") for (int k = 0; k < 2; ++k) \
;         acc[ai][bj][m][n] = mma16<BF>(Bt[n][k], At[m][k], acc[ai][bj][m][n]); __builtin_amdgcn_s_setprio(0); } while (0)
; #define GM_WAIT_V(n) asm volatile("s_waitcnt vmcnt(" #n ")" ::: "memory")
; #define GM_WAIT_L(n) asm volatile("s_waitcnt lgkmcnt(" #n ")" ::: "memory")
; #define GM_BAR __builtin_amdgcn_s_barrier()
; #define GM_SCHED __builtin_amdgcn_sched_barrier(0)
; #define GM_STA_H1(buf, p, o1) do { if constexpr (GATHER) GM_STAGE(buf, p, o1); else GM_STAGE(buf, (p) + hstepB, voffA); } while (0)
; template <bool BF, bool GATHER = false, class Epi, class Hook>
; __device__ __forceinline__ void gemm_phase(LAS unsigned char* lds, const Gemm g, const Order& S, const Epi& E, Hook& HK) {
;     ...
;             GM_WAIT_V(8); GM_WAIT_L(0); GM_BAR; GM_MMA(1, 0, At, B0); GM_MMA(1, 1, At, B1); GM_BAR; GM_SCHED;
;             GM_LDB(B0, 1, 0); GM_LDB(B1, 1, 1); GM_SCHED; GM_LDA(At, 1, 0); GM_STA_H1(GM_SA(0, 1), a2, s1);
;             GM_WAIT_V(8); GM_WAIT_L(0); GM_BAR; GM_MMA(0, 0, At, B0); GM_MMA(0, 1, At, B1); GM_BAR; GM_SCHED;
	v_mfma_f32_16x16x32_bf16 v[34:37], v[164:167], v[196:199], v[34:37]
	v_mfma_f32_16x16x32_bf16 v[30:33], v[172:175], v[196:199], v[30:33]
	v_mfma_f32_16x16x32_bf16 v[26:29], v[164:167], v[204:207], v[26:29]
	v_mfma_f32_16x16x32_bf16 v[22:25], v[172:175], v[204:207], v[22:25]
	v_mfma_f32_16x16x32_bf16 v[18:21], v[164:167], v[212:215], v[18:21]
	v_mfma_f32_16x16x32_bf16 v[14:17], v[172:175], v[212:215], v[14:17]
	v_mfma_f32_16x16x32_bf16 v[10:13], v[164:167], v[220:223], v[10:13]
	v_mfma_f32_16x16x32_bf16 v[6:9], v[172:175], v[220:223], v[6:9]
	v_mfma_f32_16x16x32_bf16 v[34:37], v[168:171], v[200:203], v[34:37]
	v_mfma_f32_16x16x32_bf16 v[30:33], v[176:179], v[200:203], v[30:33]
	v_mfma_f32_16x16x32_bf16 v[26:29], v[168:171], v[208:211], v[26:29]
	v_mfma_f32_16x16x32_bf16 v[22:25], v[176:179], v[208:211], v[22:25]
	v_mfma_f32_16x16x32_bf16 v[18:21], v[168:171], v[216:219], v[18:21]
	v_mfma_f32_16x16x32_bf16 v[14:17], v[176:179], v[216:219], v[14:17]
	v_mfma_f32_16x16x32_bf16 v[10:13], v[168:171], v[224:227], v[10:13]
	v_mfma_f32_16x16x32_bf16 v[6:9], v[176:179], v[224:227], v[6:9]
	v_mfma_f32_16x16x32_bf16 v[2:5], v[180:183], v[196:199], v[2:5]
	v_mfma_f32_16x16x32_bf16 v[102:105], v[188:191], v[196:199], v[102:105]
	v_mfma_f32_16x16x32_bf16 v[106:109], v[180:183], v[204:207], v[106:109]
	v_mfma_f32_16x16x32_bf16 v[110:113], v[188:191], v[204:207], v[110:113]
	v_mfma_f32_16x16x32_bf16 v[114:117], v[180:183], v[212:215], v[114:117]
	v_mfma_f32_16x16x32_bf16 v[118:121], v[188:191], v[212:215], v[118:121]
	v_mfma_f32_16x16x32_bf16 v[122:125], v[180:183], v[220:223], v[122:125]
	v_mfma_f32_16x16x32_bf16 v[126:129], v[188:191], v[220:223], v[126:129]
	v_mfma_f32_16x16x32_bf16 v[2:5], v[184:187], v[200:203], v[2:5]
	v_mfma_f32_16x16x32_bf16 v[102:105], v[192:195], v[200:203], v[102:105]
	v_mfma_f32_16x16x32_bf16 v[106:109], v[184:187], v[208:211], v[106:109]
	v_mfma_f32_16x16x32_bf16 v[110:113], v[192:195], v[208:211], v[110:113]
	v_mfma_f32_16x16x32_bf16 v[114:117], v[184:187], v[216:219], v[114:117]
	v_mfma_f32_16x16x32_bf16 v[118:121], v[192:195], v[216:219], v[118:121]
	v_mfma_f32_16x16x32_bf16 v[122:125], v[184:187], v[224:227], v[122:125]
	v_mfma_f32_16x16x32_bf16 v[126:129], v[192:195], v[224:227], v[126:129]
	s_barrier
	s_mov_b32 m0, s30
	s_nop 0
	global_load_lds_dwordx4 v141, s[24:25]
	s_mov_b32 m0, s31
	s_nop 0
	global_load_lds_dwordx4 v145, s[24:25]
	s_mov_b32 s45, 0x1c000
	s_mov_b32 s44, 0x18000
	v_add_u32_e32 v245, s44, v156
	ds_read_b128 v[164:167], v245
	ds_read_b128 v[168:171], v245 offset:1024
	ds_read_b128 v[172:175], v245 offset:2048
	ds_read_b128 v[176:179], v245 offset:3072
	v_add_u32_e32 v245, s45, v156
	ds_read_b128 v[180:183], v245
	ds_read_b128 v[184:187], v245 offset:1024
	ds_read_b128 v[188:191], v245 offset:2048
	ds_read_b128 v[192:195], v245 offset:3072
	ds_read_b128 v[196:199], v147 offset:32768
	ds_read_b128 v[200:203], v147 offset:33792
	ds_read_b128 v[204:207], v147 offset:34816
	ds_read_b128 v[208:211], v147 offset:35840
	ds_read_b128 v[212:215], v147 offset:36864
	ds_read_b128 v[216:219], v147 offset:37888
	ds_read_b128 v[220:223], v147 offset:38912
	ds_read_b128 v[224:227], v147 offset:39936
	s_waitcnt vmcnt(8)
	s_waitcnt lgkmcnt(0)
	s_barrier
	v_mfma_f32_16x16x32_bf16 v[98:101], v[164:167], v[196:199], v[98:101]
	v_mfma_f32_16x16x32_bf16 v[94:97], v[172:175], v[196:199], v[94:97]
	v_mfma_f32_16x16x32_bf16 v[90:93], v[164:167], v[204:207], v[90:93]
	v_mfma_f32_16x16x32_bf16 v[86:89], v[172:175], v[204:207], v[86:89]
	v_mfma_f32_16x16x32_bf16 v[82:85], v[164:167], v[212:215], v[82:85]
	v_mfma_f32_16x16x32_bf16 v[78:81], v[172:175], v[212:215], v[78:81]
	v_mfma_f32_16x16x32_bf16 v[74:77], v[164:167], v[220:223], v[74:77]
	v_mfma_f32_16x16x32_bf16 v[70:73], v[172:175], v[220:223], v[70:73]
	v_mfma_f32_16x16x32_bf16 v[98:101], v[168:171], v[200:203], v[98:101]
	v_mfma_f32_16x16x32_bf16 v[94:97], v[176:179], v[200:203], v[94:97]
	v_mfma_f32_16x16x32_bf16 v[90:93], v[168:171], v[208:211], v[90:93]
	v_mfma_f32_16x16x32_bf16 v[86:89], v[176:179], v[208:211], v[86:89]
	v_mfma_f32_16x16x32_bf16 v[82:85], v[168:171], v[216:219], v[82:85]
	v_mfma_f32_16x16x32_bf16 v[78:81], v[176:179], v[216:219], v[78:81]
	v_mfma_f32_16x16x32_bf16 v[74:77], v[168:171], v[224:227], v[74:77]
	v_mfma_f32_16x16x32_bf16 v[70:73], v[176:179], v[224:227], v[70:73]
	v_mfma_f32_16x16x32_bf16 v[66:69], v[180:183], v[196:199], v[66:69]
	v_mfma_f32_16x16x32_bf16 v[62:65], v[188:191], v[196:199], v[62:65]
	v_mfma_f32_16x16x32_bf16 v[58:61], v[180:183], v[204:207], v[58:61]
	v_mfma_f32_16x16x32_bf16 v[54:57], v[188:191], v[204:207], v[54:57]
	v_mfma_f32_16x16x32_bf16 v[50:53], v[180:183], v[212:215], v[50:53]
	v_mfma_f32_16x16x32_bf16 v[46:49], v[188:191], v[212:215], v[46:49]
	v_mfma_f32_16x16x32_bf16 v[42:45], v[180:183], v[220:223], v[42:45]
	v_mfma_f32_16x16x32_bf16 v[38:41], v[188:191], v[220:223], v[38:41]
	v_mfma_f32_16x16x32_bf16 v[66:69], v[184:187], v[200:203], v[66:69]
	v_mfma_f32_16x16x32_bf16 v[62:65], v[192:195], v[200:203], v[62:65]
	v_mfma_f32_16x16x32_bf16 v[58:61], v[184:187], v[208:211], v[58:61]
	v_mfma_f32_16x16x32_bf16 v[54:57], v[192:195], v[208:211], v[54:57]
	v_mfma_f32_16x16x32_bf16 v[50:53], v[184:187], v[216:219], v[50:53]
	v_mfma_f32_16x16x32_bf16 v[46:49], v[192:195], v[216:219], v[46:49]
	v_mfma_f32_16x16x32_bf16 v[42:45], v[184:187], v[224:227], v[42:45]
	v_mfma_f32_16x16x32_bf16 v[38:41], v[192:195], v[224:227], v[38:41]
	s_barrier
; #define GM_STAGE(bufoff, gbase, voff) do { _Pragma("unroll") for (int _i = 0; _i < 2; ++_i) \
;         __builtin_amdgcn_global_load_lds((const unsigned*)((const char*)(gbase) + (voff)[_i]), (LAS unsigned*)(lds + (bufoff) + ldsw + _i * 8192), 16, 0, 0); } while (0)
; #define GM_LDA(dst, b, h) do { _Pragma("unroll") for (int m = 0; m < 4; ++m) _Pragma("unroll") for (int k = 0; k < 2; ++k) dst[m][k] = *(const LAS s16x8*)(lds + GM_SA(b, h) + aoff + m * 2048 + k * 1024); } while (0)
; #define GM_MMA(ai, bj, At, Bt) do { __builtin_amdgcn_s_setprio(1); _Pragma("unroll") for (int m = 0; m < 4; ++m) _Pragma("unroll") for (int n = 0; n < 2; ++n) _Pragma("unroll") for (int k = 0; k < 2; ++k) \
;         acc[ai][bj][m][n] = mma16<BF>(Bt[n][k], At[m][k], acc[ai][bj][m][n]); __builtin_amdgcn_s_setprio(0); } while (0)
; #define GM_WAIT_V(n) asm volatile("s_waitcnt vmcnt(" #n ")" ::: "memory")
; #define GM_WAIT_L(n) asm volatile("s_waitcnt lgkmcnt(" #n ")" ::: "memory")
; #define GM_BAR __builtin_amdgcn_s_barrier()
; #define GM_SCHED __builtin_amdgcn_sched_barrier(0)
; #define GM_STA_H0(buf, p, o0) do { if constexpr (GATHER) GM_STAGE(buf, p, o0); else GM_STAGE(buf, p, voffA); } while (0)
; template <bool BF, bool GATHER = false, class Epi, class Hook>
; __device__ __forceinline__ void gemm_phase(LAS unsigned char* lds, const Gemm g, const Order& S, const Epi& E, Hook& HK) {
;     ...
;             GM_LDA(At, 1, 1); GM_STAGE(GM_SB(1, 0), b3, voffB); GM_STAGE(GM_SB(1, 1), b3 + hstepB, voffB); GM_STA_H0(GM_SA(1, 0), a3, s0);
;             GM_WAIT_V(8); GM_WAIT_L(0); GM_BAR; GM_MMA(1, 0, At, B0); GM_MMA(1, 1, At, B1); GM_BAR; GM_SCHED;
;         }
;         if (wr == 0) GM_BAR;
	s_add_i32 s24, s44, s11
	v_lshl_add_u64 v[230:231], v[230:231], 0, s[14:15]
	s_mov_b32 m0, s24
	s_nop 0
	global_load_lds_dwordx4 v[230:231], off
	s_add_i32 m0, s24, 0x2000
	s_add_u32 s22, s22, 0x40080
	v_lshl_add_u64 v[230:231], v[232:233], 0, s[14:15]
	s_addc_u32 s23, s23, 0
	s_add_i32 s24, s45, s11
	global_load_lds_dwordx4 v[230:231], off
	v_lshl_add_u64 v[230:231], s[22:23], 0, v[130:131]
	s_mov_b32 m0, s24
	v_lshl_add_u64 v[228:229], v[228:229], 0, s[14:15]
	global_load_lds_dwordx4 v[230:231], off
	v_lshl_add_u64 v[230:231], s[22:23], 0, v[132:133]
	s_add_i32 m0, s24, 0x2000
	s_nop 0
	global_load_lds_dwordx4 v[230:231], off
	v_lshl_add_u64 v[230:231], v[234:235], 0, s[14:15]
	s_mov_b32 m0, s33
	s_nop 0
	global_load_lds_dwordx4 v[230:231], off
	s_mov_b32 m0, s34
	s_nop 0
	global_load_lds_dwordx4 v[228:229], off
	ds_read_b128 v[196:199], v147 offset:49152
	ds_read_b128 v[200:203], v147 offset:50176
	ds_read_b128 v[204:207], v147 offset:51200
	ds_read_b128 v[208:211], v147 offset:52224
	ds_read_b128 v[212:215], v147 offset:53248
	ds_read_b128 v[216:219], v147 offset:54272
	ds_read_b128 v[220:223], v147 offset:55296
	ds_read_b128 v[224:227], v147 offset:56320
	s_waitcnt vmcnt(8)
	s_waitcnt lgkmcnt(0)
	s_barrier
	v_mfma_f32_16x16x32_bf16 v[34:37], v[164:167], v[196:199], v[34:37]
	v_mfma_f32_16x16x32_bf16 v[30:33], v[172:175], v[196:199], v[30:33]
	v_mfma_f32_16x16x32_bf16 v[26:29], v[164:167], v[204:207], v[26:29]
	v_mfma_f32_16x16x32_bf16 v[22:25], v[172:175], v[204:207], v[22:25]
	v_mfma_f32_16x16x32_bf16 v[18:21], v[164:167], v[212:215], v[18:21]
	v_mfma_f32_16x16x32_bf16 v[14:17], v[172:175], v[212:215], v[14:17]
	v_mfma_f32_16x16x32_bf16 v[10:13], v[164:167], v[220:223], v[10:13]
	v_mfma_f32_16x16x32_bf16 v[6:9], v[172:175], v[220:223], v[6:9]
	v_mfma_f32_16x16x32_bf16 v[34:37], v[168:171], v[200:203], v[34:37]
	v_mfma_f32_16x16x32_bf16 v[30:33], v[176:179], v[200:203], v[30:33]
	v_mfma_f32_16x16x32_bf16 v[26:29], v[168:171], v[208:211], v[26:29]
	v_mfma_f32_16x16x32_bf16 v[22:25], v[176:179], v[208:211], v[22:25]
	v_mfma_f32_16x16x32_bf16 v[18:21], v[168:171], v[216:219], v[18:21]
	v_mfma_f32_16x16x32_bf16 v[14:17], v[176:179], v[216:219], v[14:17]
	v_mfma_f32_16x16x32_bf16 v[10:13], v[168:171], v[224:227], v[10:13]
	v_mfma_f32_16x16x32_bf16 v[6:9], v[176:179], v[224:227], v[6:9]
	v_mfma_f32_16x16x32_bf16 v[2:5], v[180:183], v[196:199], v[2:5]
	v_mfma_f32_16x16x32_bf16 v[102:105], v[188:191], v[196:199], v[102:105]
	v_mfma_f32_16x16x32_bf16 v[106:109], v[180:183], v[204:207], v[106:109]
	v_mfma_f32_16x16x32_bf16 v[110:113], v[188:191], v[204:207], v[110:113]
	v_mfma_f32_16x16x32_bf16 v[114:117], v[180:183], v[212:215], v[114:117]
	v_mfma_f32_16x16x32_bf16 v[118:121], v[188:191], v[212:215], v[118:121]
	v_mfma_f32_16x16x32_bf16 v[122:125], v[180:183], v[220:223], v[122:125]
	v_mfma_f32_16x16x32_bf16 v[126:129], v[188:191], v[220:223], v[126:129]
	v_mfma_f32_16x16x32_bf16 v[2:5], v[184:187], v[200:203], v[2:5]
	v_mfma_f32_16x16x32_bf16 v[102:105], v[192:195], v[200:203], v[102:105]
	v_mfma_f32_16x16x32_bf16 v[106:109], v[184:187], v[208:211], v[106:109]
	v_mfma_f32_16x16x32_bf16 v[110:113], v[192:195], v[208:211], v[110:113]
	v_mfma_f32_16x16x32_bf16 v[114:117], v[184:187], v[216:219], v[114:117]
	v_mfma_f32_16x16x32_bf16 v[118:121], v[192:195], v[216:219], v[118:121]
	v_mfma_f32_16x16x32_bf16 v[122:125], v[184:187], v[224:227], v[122:125]
	v_mfma_f32_16x16x32_bf16 v[126:129], v[192:195], v[224:227], v[126:129]
	s_barrier
	s_add_i32 s43, s43, 2
	s_add_u32 s2, s2, 0x100
	s_addc_u32 s3, s3, 0
	s_cmp_gt_u32 s43, 13
	s_cbranch_scc0 .LBB0_1011
	s_and_b64 vcc, exec, s[18:19]
	s_cbranch_vccz .LBB0_1014
	s_barrier

; #define GM_STAGE(bufoff, gbase, voff) do { _Pragma("unroll") for (int _i = 0; _i < 2; ++_i) \
;         __builtin_amdgcn_global_load_lds((const unsigned*)((const char*)(gbase) + (voff)[_i]), (LAS unsigned*)(lds + (bufoff) + ldsw + _i * 8192), 16, 0, 0); } while (0)
; #define GM_LDA(dst, b, h) do { _Pragma("unroll") for (int m = 0; m < 4; ++m) _Pragma("unroll") for (int k = 0; k < 2; ++k) dst[m][k] = *(const LAS s16x8*)(lds + GM_SA(b, h) + aoff + m * 2048 + k * 1024); } while (0)
; #define GM_LDB(dst, b, h) do { _Pragma("unroll") for (int n = 0; n < 2; ++n) _Pragma("unroll") for (int k = 0; k < 2; ++k) dst[n][k] = *(const LAS s16x8*)(lds + GM_SB(b, h) + boff + n * 2048 + k * 1024); } while (0)
; #define GM_MMA(ai, bj, At, Bt) do { __builtin_amdgcn_s_setprio(1); _Pragma("unroll") for (int m = 0; m < 4; ++m) _Pragma("unroll") for (int n = 0; n < 2; ++n) _Pragma("unroll") for (int k = 0; k < 2; ++k) \
;         acc[ai][bj][m][n] = mma16<BF>(Bt[n][k], At[m][k], acc[ai][bj][m][n]); __builtin_amdgcn_s_setprio(0); } while (0)
; #define GM_WAIT_V(n) asm volatile("s_waitcnt vmcnt(" #n ")" ::: "memory")
; #define GM_WAIT_L(n) asm volatile("s_waitcnt lgkmcnt(" #n ")" ::: "memory")
; template <bool BF, bool GATHER = false, class Epi, class Hook>
; __device__ __forceinline__ void gemm_phase(LAS unsigned char* lds, const Gemm g, const Order& S, const Epi& E, Hook& HK) {
;     ...
;             const bool last = (t == nt - 2);
;             const char* a1 = cA + (size_t)(t + 1) * kstep;
;             const char* a2 = last ? nA : cA + (size_t)(t + 2) * kstep; const char* b2 = last ? nB : cB + (size_t)(t + 2) * kstep;
;             const char* a3 = a2 + kstep; const char* b3 = b2 + kstep;
;             unsigned s0[2], s1[2];
;             if constexpr (GATHER) { s0[0] = last ? nA0[0] : gA0[0]; s0[1] = last ? nA0[1] : gA0[1]; s1[0] = last ? nA1[0] : gA1[0]; s1[1] = last ? nA1[1] : gA1[1]; }
;             GM_LDB(B0, 0, 0); GM_LDB(B1, 0, 1); GM_SCHED; GM_LDA(At, 0, 0); GM_STA_H1(GM_SA(1, 1), a1, gA1);
;             GM_WAIT_V(8); GM_WAIT_L(0); GM_BAR; GM_MMA(0, 0, At, B0); GM_MMA(0, 1, At, B1); GM_BAR; GM_SCHED;
;             GM_LDA(At, 0, 1); GM_STAGE(GM_SB(0, 0), b2, voffB); GM_STAGE(GM_SB(0, 1), b2 + hstepB, voffB); GM_STA_H0(GM_SA(0, 0), a2, s0);
;             GM_WAIT_V(8); GM_WAIT_L(0); GM_BAR; GM_MMA(1, 0, At, B0); GM_MMA(1, 1, At, B1); GM_BAR; GM_SCHED;
.LBB0_1102:
	s_add_u32 s22, s2, 0x100
	s_addc_u32 s23, s3, 0
	s_cmp_eq_u32 s51, 40
	s_cselect_b32 s27, s7, s23
	s_cselect_b32 s26, s6, s22
	s_cselect_b32 s25, s21, s50
	s_cselect_b32 s24, s20, s49
	v_lshl_add_u64 v[216:217], s[2:3], 0, v[138:139]
	s_add_i32 m0, s29, 0xc000
	s_nop 0
	global_load_lds_dwordx4 v[216:217], off
	v_lshl_add_u64 v[216:217], s[2:3], 0, v[140:141]
	s_add_i32 m0, s29, 0xe000
	s_nop 0
	global_load_lds_dwordx4 v[216:217], off
	ds_read_b128 v[146:149], v153
	ds_read_b128 v[156:159], v153 offset:1024
	ds_read_b128 v[160:163], v153 offset:2048
	ds_read_b128 v[164:167], v153 offset:3072
	ds_read_b128 v[168:171], v154
	ds_read_b128 v[172:175], v154 offset:1024
	ds_read_b128 v[176:179], v154 offset:2048
	ds_read_b128 v[180:183], v154 offset:3072
	ds_read_b128 v[184:187], v155
	ds_read_b128 v[188:191], v155 offset:1024
	ds_read_b128 v[192:195], v155 offset:2048
	ds_read_b128 v[196:199], v155 offset:3072
	ds_read_b128 v[200:203], v155 offset:4096
	ds_read_b128 v[204:207], v155 offset:5120
	ds_read_b128 v[208:211], v155 offset:6144
	ds_read_b128 v[212:215], v155 offset:7168
	s_waitcnt vmcnt(8)
	s_waitcnt lgkmcnt(0)
	s_barrier
	v_mfma_f32_16x16x32_bf16 v[126:129], v[146:149], v[184:187], v[126:129]
	v_mfma_f32_16x16x32_bf16 v[122:125], v[160:163], v[184:187], v[122:125]
	v_mfma_f32_16x16x32_bf16 v[110:113], v[146:149], v[192:195], v[110:113]
	v_mfma_f32_16x16x32_bf16 v[106:109], v[160:163], v[192:195], v[106:109]
	v_mfma_f32_16x16x32_bf16 v[94:97], v[146:149], v[200:203], v[94:97]
	v_mfma_f32_16x16x32_bf16 v[90:93], v[160:163], v[200:203], v[90:93]
	v_mfma_f32_16x16x32_bf16 v[78:81], v[146:149], v[208:211], v[78:81]
	v_mfma_f32_16x16x32_bf16 v[74:77], v[160:163], v[208:211], v[74:77]
	v_mfma_f32_16x16x32_bf16 v[126:129], v[156:159], v[188:191], v[126:129]
	v_mfma_f32_16x16x32_bf16 v[122:125], v[164:167], v[188:191], v[122:125]
	v_mfma_f32_16x16x32_bf16 v[110:113], v[156:159], v[196:199], v[110:113]
	v_mfma_f32_16x16x32_bf16 v[106:109], v[164:167], v[196:199], v[106:109]
	v_mfma_f32_16x16x32_bf16 v[94:97], v[156:159], v[204:207], v[94:97]
	v_mfma_f32_16x16x32_bf16 v[90:93], v[164:167], v[204:207], v[90:93]
	v_mfma_f32_16x16x32_bf16 v[78:81], v[156:159], v[212:215], v[78:81]
	v_mfma_f32_16x16x32_bf16 v[74:77], v[164:167], v[212:215], v[74:77]
	v_mfma_f32_16x16x32_bf16 v[118:121], v[168:171], v[184:187], v[118:121]
	v_mfma_f32_16x16x32_bf16 v[114:117], v[176:179], v[184:187], v[114:117]
	v_mfma_f32_16x16x32_bf16 v[102:105], v[168:171], v[192:195], v[102:105]
	v_mfma_f32_16x16x32_bf16 v[98:101], v[176:179], v[192:195], v[98:101]
	v_mfma_f32_16x16x32_bf16 v[86:89], v[168:171], v[200:203], v[86:89]
	v_mfma_f32_16x16x32_bf16 v[82:85], v[176:179], v[200:203], v[82:85]
	v_mfma_f32_16x16x32_bf16 v[70:73], v[168:171], v[208:211], v[70:73]
	v_mfma_f32_16x16x32_bf16 v[66:69], v[176:179], v[208:211], v[66:69]
	v_mfma_f32_16x16x32_bf16 v[118:121], v[172:175], v[188:191], v[118:121]
	v_mfma_f32_16x16x32_bf16 v[114:117], v[180:183], v[188:191], v[114:117]
	v_mfma_f32_16x16x32_bf16 v[102:105], v[172:175], v[196:199], v[102:105]
	v_mfma_f32_16x16x32_bf16 v[98:101], v[180:183], v[196:199], v[98:101]
	v_mfma_f32_16x16x32_bf16 v[86:89], v[172:175], v[204:207], v[86:89]
	v_mfma_f32_16x16x32_bf16 v[82:85], v[180:183], v[204:207], v[82:85]
	v_mfma_f32_16x16x32_bf16 v[70:73], v[172:175], v[212:215], v[70:73]
	v_mfma_f32_16x16x32_bf16 v[66:69], v[180:183], v[212:215], v[66:69]
	s_barrier
	s_add_i32 s2, s42, s28
	v_lshl_add_u64 v[216:217], s[24:25], 0, v[132:133]
	s_mov_b32 m0, s2
	s_nop 0
	global_load_lds_dwordx4 v[216:217], off
	s_add_i32 m0, s2, 0x2000
	s_add_u32 s2, s24, 0xb0000
	v_lshl_add_u64 v[218:219], s[24:25], 0, v[136:137]
	s_addc_u32 s3, s25, 0
	s_add_i32 s52, s43, s28
	global_load_lds_dwordx4 v[218:219], off
	v_lshl_add_u64 v[220:221], s[2:3], 0, v[132:133]
	s_mov_b32 m0, s52
	v_lshl_add_u64 v[222:223], s[26:27], 0, v[134:135]
	global_load_lds_dwordx4 v[220:221], off
	v_lshl_add_u64 v[220:221], s[2:3], 0, v[136:137]
	s_add_i32 m0, s52, 0x2000
	s_nop 0
	global_load_lds_dwordx4 v[220:221], off
	v_lshl_add_u64 v[220:221], s[26:27], 0, v[130:131]
	s_mov_b32 m0, s29
	s_nop 0
	global_load_lds_dwordx4 v[220:221], off
	s_mov_b32 m0, s30
	s_nop 0
	global_load_lds_dwordx4 v[222:223], off
	ds_read_b128 v[184:187], v155 offset:16384
	ds_read_b128 v[188:191], v155 offset:17408
	ds_read_b128 v[192:195], v155 offset:18432
	ds_read_b128 v[196:199], v155 offset:19456
	ds_read_b128 v[200:203], v155 offset:20480
	ds_read_b128 v[204:207], v155 offset:21504
	ds_read_b128 v[208:211], v155 offset:22528
	ds_read_b128 v[212:215], v155 offset:23552
	s_waitcnt vmcnt(8)
	s_waitcnt lgkmcnt(0)
	s_barrier
; #define GM_LDA(dst, b, h) do { _Pragma("unroll") for (int m = 0; m < 4; ++m) _Pragma("unroll") for (int k = 0; k < 2; ++k) dst[m][k] = *(const LAS s16x8*)(lds + GM_SA(b, h) + aoff + m * 2048 + k * 1024); } while (0)
; #define GM_LDB(dst, b, h) do { _Pragma("unroll") for (int n = 0; n < 2; ++n) _Pragma("unroll") for (int k = 0; k < 2; ++k) dst[n][k] = *(const LAS s16x8*)(lds + GM_SB(b, h) + boff + n * 2048 + k * 1024); } while (0)
; #define GM_MMA(ai, bj, At, Bt) do { __builtin_amdgcn_s_setprio(1); _Pragma("unroll") for (int m = 0; m < 4; ++m) _Pragma("unroll") for (int n = 0; n < 2; ++n) _Pragma("unroll") for (int k = 0; k < 2; ++k) \
;         acc[ai][bj][m][n] = mma16<BF>(Bt[n][k], At[m][k], acc[ai][bj][m][n]); __builtin_amdgcn_s_setprio(0); } while (0)
; #define GM_WAIT_V(n) asm volatile("s_waitcnt vmcnt(" #n ")" ::: "memory")
; #define GM_WAIT_L(n) asm volatile("s_waitcnt lgkmcnt(" #n ")" ::: "memory")
; #define GM_BAR __builtin_amdgcn_s_barrier()
; #define GM_SCHED __builtin_amdgcn_sched_barrier(0)
; #define GM_STA_H1(buf, p, o1) do { if constexpr (GATHER) GM_STAGE(buf, p, o1); else GM_STAGE(buf, (p) + hstepB, voffA); } while (0)
; template <bool BF, bool GATHER = false, class Epi, class Hook>
; __device__ __forceinline__ void gemm_phase(LAS unsigned char* lds, const Gemm g, const Order& S, const Epi& E, Hook& HK) {
;     ...
;             GM_WAIT_V(8); GM_WAIT_L(0); GM_BAR; GM_MMA(1, 0, At, B0); GM_MMA(1, 1, At, B1); GM_BAR; GM_SCHED;
;             GM_LDB(B0, 1, 0); GM_LDB(B1, 1, 1); GM_SCHED; GM_LDA(At, 1, 0); GM_STA_H1(GM_SA(0, 1), a2, s1);
;             GM_WAIT_V(8); GM_WAIT_L(0); GM_BAR; GM_MMA(0, 0, At, B0); GM_MMA(0, 1, At, B1); GM_BAR; GM_SCHED;
	v_mfma_f32_16x16x32_bf16 v[62:65], v[146:149], v[184:187], v[62:65]
	v_mfma_f32_16x16x32_bf16 v[58:61], v[160:163], v[184:187], v[58:61]
	v_mfma_f32_16x16x32_bf16 v[46:49], v[146:149], v[192:195], v[46:49]
	v_mfma_f32_16x16x32_bf16 v[42:45], v[160:163], v[192:195], v[42:45]
	v_mfma_f32_16x16x32_bf16 v[30:33], v[146:149], v[200:203], v[30:33]
	v_mfma_f32_16x16x32_bf16 v[26:29], v[160:163], v[200:203], v[26:29]
	v_mfma_f32_16x16x32_bf16 v[14:17], v[146:149], v[208:211], v[14:17]
	v_mfma_f32_16x16x32_bf16 v[10:13], v[160:163], v[208:211], v[10:13]
	v_mfma_f32_16x16x32_bf16 v[62:65], v[156:159], v[188:191], v[62:65]
	v_mfma_f32_16x16x32_bf16 v[58:61], v[164:167], v[188:191], v[58:61]
	v_mfma_f32_16x16x32_bf16 v[46:49], v[156:159], v[196:199], v[46:49]
	v_mfma_f32_16x16x32_bf16 v[42:45], v[164:167], v[196:199], v[42:45]
	v_mfma_f32_16x16x32_bf16 v[30:33], v[156:159], v[204:207], v[30:33]
	v_mfma_f32_16x16x32_bf16 v[26:29], v[164:167], v[204:207], v[26:29]
	v_mfma_f32_16x16x32_bf16 v[14:17], v[156:159], v[212:215], v[14:17]
	v_mfma_f32_16x16x32_bf16 v[10:13], v[164:167], v[212:215], v[10:13]
	v_mfma_f32_16x16x32_bf16 v[54:57], v[168:171], v[184:187], v[54:57]
	v_mfma_f32_16x16x32_bf16 v[50:53], v[176:179], v[184:187], v[50:53]
	v_mfma_f32_16x16x32_bf16 v[38:41], v[168:171], v[192:195], v[38:41]
	v_mfma_f32_16x16x32_bf16 v[34:37], v[176:179], v[192:195], v[34:37]
	v_mfma_f32_16x16x32_bf16 v[22:25], v[168:171], v[200:203], v[22:25]
	v_mfma_f32_16x16x32_bf16 v[18:21], v[176:179], v[200:203], v[18:21]
	v_mfma_f32_16x16x32_bf16 v[6:9], v[168:171], v[208:211], v[6:9]
	v_mfma_f32_16x16x32_bf16 v[2:5], v[176:179], v[208:211], v[2:5]
	v_mfma_f32_16x16x32_bf16 v[54:57], v[172:175], v[188:191], v[54:57]
	v_mfma_f32_16x16x32_bf16 v[50:53], v[180:183], v[188:191], v[50:53]
	v_mfma_f32_16x16x32_bf16 v[38:41], v[172:175], v[196:199], v[38:41]
	v_mfma_f32_16x16x32_bf16 v[34:37], v[180:183], v[196:199], v[34:37]
	v_mfma_f32_16x16x32_bf16 v[22:25], v[172:175], v[204:207], v[22:25]
	v_mfma_f32_16x16x32_bf16 v[18:21], v[180:183], v[204:207], v[18:21]
	v_mfma_f32_16x16x32_bf16 v[6:9], v[172:175], v[212:215], v[6:9]
	v_mfma_f32_16x16x32_bf16 v[2:5], v[180:183], v[212:215], v[2:5]
	s_barrier
	s_add_u32 s2, s26, 0xb0000
	s_addc_u32 s3, s27, 0
	s_mov_b32 m0, s31
	v_lshl_add_u64 v[224:225], s[2:3], 0, v[130:131]
	global_load_lds_dwordx4 v[224:225], off
	v_lshl_add_u64 v[224:225], s[2:3], 0, v[134:135]
	s_mov_b32 m0, s33
	s_nop 0
	global_load_lds_dwordx4 v[224:225], off
	s_mov_b32 s53, 0x1c000
	s_mov_b32 s52, 0x18000
	v_add_u32_e32 v244, s52, v150
	v_add_u32_e32 v245, s53, v150
	ds_read_b128 v[146:149], v244
	ds_read_b128 v[156:159], v244 offset:1024
	ds_read_b128 v[160:163], v244 offset:2048
	ds_read_b128 v[164:167], v244 offset:3072
	ds_read_b128 v[168:171], v245
	ds_read_b128 v[172:175], v245 offset:1024
	ds_read_b128 v[176:179], v245 offset:2048
	ds_read_b128 v[180:183], v245 offset:3072
	ds_read_b128 v[184:187], v155 offset:32768
	ds_read_b128 v[188:191], v155 offset:33792
	ds_read_b128 v[192:195], v155 offset:34816
	ds_read_b128 v[196:199], v155 offset:35840
	ds_read_b128 v[200:203], v155 offset:36864
	ds_read_b128 v[204:207], v155 offset:37888
	ds_read_b128 v[208:211], v155 offset:38912
	ds_read_b128 v[212:215], v155 offset:39936
	s_waitcnt vmcnt(8)
	s_waitcnt lgkmcnt(0)
	s_barrier
	v_mfma_f32_16x16x32_bf16 v[126:129], v[146:149], v[184:187], v[126:129]
	v_mfma_f32_16x16x32_bf16 v[122:125], v[160:163], v[184:187], v[122:125]
	v_mfma_f32_16x16x32_bf16 v[110:113], v[146:149], v[192:195], v[110:113]
	v_mfma_f32_16x16x32_bf16 v[106:109], v[160:163], v[192:195], v[106:109]
	v_mfma_f32_16x16x32_bf16 v[94:97], v[146:149], v[200:203], v[94:97]
	v_mfma_f32_16x16x32_bf16 v[90:93], v[160:163], v[200:203], v[90:93]
	v_mfma_f32_16x16x32_bf16 v[78:81], v[146:149], v[208:211], v[78:81]
	v_mfma_f32_16x16x32_bf16 v[74:77], v[160:163], v[208:211], v[74:77]
	v_mfma_f32_16x16x32_bf16 v[126:129], v[156:159], v[188:191], v[126:129]
	v_mfma_f32_16x16x32_bf16 v[122:125], v[164:167], v[188:191], v[122:125]
	v_mfma_f32_16x16x32_bf16 v[110:113], v[156:159], v[196:199], v[110:113]
	v_mfma_f32_16x16x32_bf16 v[106:109], v[164:167], v[196:199], v[106:109]
	v_mfma_f32_16x16x32_bf16 v[94:97], v[156:159], v[204:207], v[94:97]
	v_mfma_f32_16x16x32_bf16 v[90:93], v[164:167], v[204:207], v[90:93]
	v_mfma_f32_16x16x32_bf16 v[78:81], v[156:159], v[212:215], v[78:81]
	v_mfma_f32_16x16x32_bf16 v[74:77], v[164:167], v[212:215], v[74:77]
	v_mfma_f32_16x16x32_bf16 v[118:121], v[168:171], v[184:187], v[118:121]
	v_mfma_f32_16x16x32_bf16 v[114:117], v[176:179], v[184:187], v[114:117]
	v_mfma_f32_16x16x32_bf16 v[102:105], v[168:171], v[192:195], v[102:105]
	v_mfma_f32_16x16x32_bf16 v[98:101], v[176:179], v[192:195], v[98:101]
	v_mfma_f32_16x16x32_bf16 v[86:89], v[168:171], v[200:203], v[86:89]
	v_mfma_f32_16x16x32_bf16 v[82:85], v[176:179], v[200:203], v[82:85]
	v_mfma_f32_16x16x32_bf16 v[70:73], v[168:171], v[208:211], v[70:73]
	v_mfma_f32_16x16x32_bf16 v[66:69], v[176:179], v[208:211], v[66:69]
	v_mfma_f32_16x16x32_bf16 v[118:121], v[172:175], v[188:191], v[118:121]
	v_mfma_f32_16x16x32_bf16 v[114:117], v[180:183], v[188:191], v[114:117]
	v_mfma_f32_16x16x32_bf16 v[102:105], v[172:175], v[196:199], v[102:105]
	v_mfma_f32_16x16x32_bf16 v[98:101], v[180:183], v[196:199], v[98:101]
	v_mfma_f32_16x16x32_bf16 v[86:89], v[172:175], v[204:207], v[86:89]
	v_mfma_f32_16x16x32_bf16 v[82:85], v[180:183], v[204:207], v[82:85]
	v_mfma_f32_16x16x32_bf16 v[70:73], v[172:175], v[212:215], v[70:73]
	v_mfma_f32_16x16x32_bf16 v[66:69], v[180:183], v[212:215], v[66:69]
	s_barrier
; #define GM_STAGE(bufoff, gbase, voff) do { _Pragma("unroll") for (int _i = 0; _i < 2; ++_i) \
;         __builtin_amdgcn_global_load_lds((const unsigned*)((const char*)(gbase) + (voff)[_i]), (LAS unsigned*)(lds + (bufoff) + ldsw + _i * 8192), 16, 0, 0); } while (0)
; #define GM_LDA(dst, b, h) do { _Pragma("unroll") for (int m = 0; m < 4; ++m) _Pragma("unroll") for (int k = 0; k < 2; ++k) dst[m][k] = *(const LAS s16x8*)(lds + GM_SA(b, h) + aoff + m * 2048 + k * 1024); } while (0)
; #define GM_MMA(ai, bj, At, Bt) do { __builtin_amdgcn_s_setprio(1); _Pragma("unroll") for (int m = 0; m < 4; ++m) _Pragma("unroll") for (int n = 0; n < 2; ++n) _Pragma("unroll") for (int k = 0; k < 2; ++k) \
;         acc[ai][bj][m][n] = mma16<BF>(Bt[n][k], At[m][k], acc[ai][bj][m][n]); __builtin_amdgcn_s_setprio(0); } while (0)
; #define GM_WAIT_V(n) asm volatile("s_waitcnt vmcnt(" #n ")" ::: "memory")
; #define GM_WAIT_L(n) asm volatile("s_waitcnt lgkmcnt(" #n ")" ::: "memory")
; #define GM_BAR __builtin_amdgcn_s_barrier()
; #define GM_SCHED __builtin_amdgcn_sched_barrier(0)
; #define GM_STA_H0(buf, p, o0) do { if constexpr (GATHER) GM_STAGE(buf, p, o0); else GM_STAGE(buf, p, voffA); } while (0)
; template <bool BF, bool GATHER = false, class Epi, class Hook>
; __device__ __forceinline__ void gemm_phase(LAS unsigned char* lds, const Gemm g, const Order& S, const Epi& E, Hook& HK) {
;     ...
;             GM_LDA(At, 1, 1); GM_STAGE(GM_SB(1, 0), b3, voffB); GM_STAGE(GM_SB(1, 1), b3 + hstepB, voffB); GM_STA_H0(GM_SA(1, 0), a3, s0);
;             GM_WAIT_V(8); GM_WAIT_L(0); GM_BAR; GM_MMA(1, 0, At, B0); GM_MMA(1, 1, At, B1); GM_BAR; GM_SCHED;
;         }
;         if (wr == 0) GM_BAR;
	s_add_i32 s2, s52, s28
	v_lshl_add_u64 v[216:217], v[216:217], 0, s[12:13]
	s_mov_b32 m0, s2
	s_nop 0
	global_load_lds_dwordx4 v[216:217], off
	s_add_i32 m0, s2, 0x2000
	s_add_u32 s2, s24, 0xb0080
	v_lshl_add_u64 v[216:217], v[218:219], 0, s[12:13]
	s_addc_u32 s3, s25, 0
	s_add_i32 s24, s53, s28
	global_load_lds_dwordx4 v[216:217], off
	v_lshl_add_u64 v[216:217], s[2:3], 0, v[132:133]
	s_mov_b32 m0, s24
	s_nop 0
	global_load_lds_dwordx4 v[216:217], off
	v_lshl_add_u64 v[216:217], s[2:3], 0, v[136:137]
	s_add_i32 m0, s24, 0x2000
	s_nop 0
	global_load_lds_dwordx4 v[216:217], off
	v_lshl_add_u64 v[216:217], v[220:221], 0, s[12:13]
	s_mov_b32 m0, s36
	s_nop 0
	global_load_lds_dwordx4 v[216:217], off
	v_lshl_add_u64 v[216:217], v[222:223], 0, s[12:13]
	s_mov_b32 m0, s37
	s_nop 0
	global_load_lds_dwordx4 v[216:217], off
	ds_read_b128 v[184:187], v155 offset:49152
	ds_read_b128 v[188:191], v155 offset:50176
	ds_read_b128 v[192:195], v155 offset:51200
	ds_read_b128 v[196:199], v155 offset:52224
	ds_read_b128 v[200:203], v155 offset:53248
	ds_read_b128 v[204:207], v155 offset:54272
	ds_read_b128 v[208:211], v155 offset:55296
	ds_read_b128 v[212:215], v155 offset:56320
	s_waitcnt vmcnt(8)
	s_waitcnt lgkmcnt(0)
	s_barrier
	v_mfma_f32_16x16x32_bf16 v[62:65], v[146:149], v[184:187], v[62:65]
	v_mfma_f32_16x16x32_bf16 v[58:61], v[160:163], v[184:187], v[58:61]
	v_mfma_f32_16x16x32_bf16 v[46:49], v[146:149], v[192:195], v[46:49]
	v_mfma_f32_16x16x32_bf16 v[42:45], v[160:163], v[192:195], v[42:45]
	v_mfma_f32_16x16x32_bf16 v[30:33], v[146:149], v[200:203], v[30:33]
	v_mfma_f32_16x16x32_bf16 v[26:29], v[160:163], v[200:203], v[26:29]
	v_mfma_f32_16x16x32_bf16 v[14:17], v[146:149], v[208:211], v[14:17]
	v_mfma_f32_16x16x32_bf16 v[10:13], v[160:163], v[208:211], v[10:13]
	v_mfma_f32_16x16x32_bf16 v[62:65], v[156:159], v[188:191], v[62:65]
	v_mfma_f32_16x16x32_bf16 v[58:61], v[164:167], v[188:191], v[58:61]
	v_mfma_f32_16x16x32_bf16 v[46:49], v[156:159], v[196:199], v[46:49]
	v_mfma_f32_16x16x32_bf16 v[42:45], v[164:167], v[196:199], v[42:45]
	v_mfma_f32_16x16x32_bf16 v[30:33], v[156:159], v[204:207], v[30:33]
	v_mfma_f32_16x16x32_bf16 v[26:29], v[164:167], v[204:207], v[26:29]
	v_mfma_f32_16x16x32_bf16 v[14:17], v[156:159], v[212:215], v[14:17]
	v_mfma_f32_16x16x32_bf16 v[10:13], v[164:167], v[212:215], v[10:13]
	v_mfma_f32_16x16x32_bf16 v[54:57], v[168:171], v[184:187], v[54:57]
	v_mfma_f32_16x16x32_bf16 v[50:53], v[176:179], v[184:187], v[50:53]
	v_mfma_f32_16x16x32_bf16 v[38:41], v[168:171], v[192:195], v[38:41]
	v_mfma_f32_16x16x32_bf16 v[34:37], v[176:179], v[192:195], v[34:37]
	v_mfma_f32_16x16x32_bf16 v[22:25], v[168:171], v[200:203], v[22:25]
	v_mfma_f32_16x16x32_bf16 v[18:21], v[176:179], v[200:203], v[18:21]
	v_mfma_f32_16x16x32_bf16 v[6:9], v[168:171], v[208:211], v[6:9]
	v_mfma_f32_16x16x32_bf16 v[2:5], v[176:179], v[208:211], v[2:5]
	v_mfma_f32_16x16x32_bf16 v[54:57], v[172:175], v[188:191], v[54:57]
	v_mfma_f32_16x16x32_bf16 v[50:53], v[180:183], v[188:191], v[50:53]
	v_mfma_f32_16x16x32_bf16 v[38:41], v[172:175], v[196:199], v[38:41]
	v_mfma_f32_16x16x32_bf16 v[34:37], v[180:183], v[196:199], v[34:37]
	v_mfma_f32_16x16x32_bf16 v[22:25], v[172:175], v[204:207], v[22:25]
	v_mfma_f32_16x16x32_bf16 v[18:21], v[180:183], v[204:207], v[18:21]
	v_mfma_f32_16x16x32_bf16 v[6:9], v[172:175], v[212:215], v[6:9]
	v_mfma_f32_16x16x32_bf16 v[2:5], v[180:183], v[212:215], v[2:5]
	s_barrier
	s_add_i32 s51, s51, 2
	s_add_u32 s49, s49, 0x100
	s_addc_u32 s50, s50, 0
	s_cmp_gt_u32 s51, 41
	s_mov_b64 s[2:3], s[22:23]
	s_cbranch_scc0 .LBB0_1102
	s_and_b64 vcc, exec, s[14:15]
	s_cbranch_vccz .LBB0_1105
	s_barrier

; #define GM_STAGE(bufoff, gbase, voff) do { _Pragma("unroll") for (int _i = 0; _i < 2; ++_i) \
;         __builtin_amdgcn_global_load_lds((const unsigned*)((const char*)(gbase) + (voff)[_i]), (LAS unsigned*)(lds + (bufoff) + ldsw + _i * 8192), 16, 0, 0); } while (0)
; #define GM_LDA(dst, b, h) do { _Pragma("unroll") for (int m = 0; m < 4; ++m) _Pragma("unroll") for (int k = 0; k < 2; ++k) dst[m][k] = *(const LAS s16x8*)(lds + GM_SA(b, h) + aoff + m * 2048 + k * 1024); } while (0)
; #define GM_LDB(dst, b, h) do { _Pragma("unroll") for (int n = 0; n < 2; ++n) _Pragma("unroll") for (int k = 0; k < 2; ++k) dst[n][k] = *(const LAS s16x8*)(lds + GM_SB(b, h) + boff + n * 2048 + k * 1024); } while (0)
; #define GM_MMA(ai, bj, At, Bt) do { __builtin_amdgcn_s_setprio(1); _Pragma("unroll") for (int m = 0; m < 4; ++m) _Pragma("unroll") for (int n = 0; n < 2; ++n) _Pragma("unroll") for (int k = 0; k < 2; ++k) \
;         acc[ai][bj][m][n] = mma16<BF>(Bt[n][k], At[m][k], acc[ai][bj][m][n]); __builtin_amdgcn_s_setprio(0); } while (0)
; #define GM_WAIT_V(n) asm volatile("s_waitcnt vmcnt(" #n ")" ::: "memory")
; #define GM_WAIT_L(n) asm volatile("s_waitcnt lgkmcnt(" #n ")" ::: "memory")
; template <bool BF, bool GATHER = false, class Epi, class Hook>
; __device__ __forceinline__ void gemm_phase(LAS unsigned char* lds, const Gemm g, const Order& S, const Epi& E, Hook& HK) {
;     ...
;             const bool last = (t == nt - 2);
;             const char* a1 = cA + (size_t)(t + 1) * kstep;
;             const char* a2 = last ? nA : cA + (size_t)(t + 2) * kstep; const char* b2 = last ? nB : cB + (size_t)(t + 2) * kstep;
;             const char* a3 = a2 + kstep; const char* b3 = b2 + kstep;
;             unsigned s0[2], s1[2];
;             if constexpr (GATHER) { s0[0] = last ? nA0[0] : gA0[0]; s0[1] = last ? nA0[1] : gA0[1]; s1[0] = last ? nA1[0] : gA1[0]; s1[1] = last ? nA1[1] : gA1[1]; }
;             GM_LDB(B0, 0, 0); GM_LDB(B1, 0, 1); GM_SCHED; GM_LDA(At, 0, 0); GM_STA_H1(GM_SA(1, 1), a1, gA1);
;             GM_WAIT_V(8); GM_WAIT_L(0); GM_BAR; GM_MMA(0, 0, At, B0); GM_MMA(0, 1, At, B1); GM_BAR; GM_SCHED;
;             GM_LDA(At, 0, 1); GM_STAGE(GM_SB(0, 0), b2, voffB); GM_STAGE(GM_SB(0, 1), b2 + hstepB, voffB); GM_STA_H0(GM_SA(0, 0), a2, s0);
;             GM_WAIT_V(8); GM_WAIT_L(0); GM_BAR; GM_MMA(1, 0, At, B0); GM_MMA(1, 1, At, B1); GM_BAR; GM_SCHED;
.LBB0_1281:
	s_add_u32 s22, s20, 0xfffc0080
	s_addc_u32 s23, s21, -1
	s_cmp_eq_u32 s47, 12
	s_cselect_b32 s25, s3, s23
	s_cselect_b32 s24, s13, s22
	s_cselect_b32 s23, s15, s46
	s_cselect_b32 s22, s44, s45
	v_lshl_add_u64 v[218:219], s[20:21], 0, v[140:141]
	s_add_i32 m0, s30, 0xc000
	s_nop 0
	global_load_lds_dwordx4 v[218:219], off
	v_lshl_add_u64 v[218:219], s[20:21], 0, v[142:143]
	s_add_i32 m0, s30, 0xe000
	s_nop 0
	global_load_lds_dwordx4 v[218:219], off
	ds_read_b128 v[154:157], v151
	ds_read_b128 v[158:161], v151 offset:1024
	ds_read_b128 v[162:165], v151 offset:2048
	ds_read_b128 v[166:169], v151 offset:3072
	ds_read_b128 v[170:173], v152
	ds_read_b128 v[174:177], v152 offset:1024
	ds_read_b128 v[178:181], v152 offset:2048
	ds_read_b128 v[182:185], v152 offset:3072
	ds_read_b128 v[186:189], v153
	ds_read_b128 v[190:193], v153 offset:1024
	ds_read_b128 v[194:197], v153 offset:2048
	ds_read_b128 v[198:201], v153 offset:3072
	ds_read_b128 v[202:205], v153 offset:4096
	ds_read_b128 v[206:209], v153 offset:5120
	ds_read_b128 v[210:213], v153 offset:6144
	ds_read_b128 v[214:217], v153 offset:7168
	s_waitcnt vmcnt(8)
	s_waitcnt lgkmcnt(0)
	s_barrier
	v_mfma_f32_16x16x32_f16 v[126:129], v[154:157], v[186:189], v[126:129]
	v_mfma_f32_16x16x32_f16 v[118:121], v[162:165], v[186:189], v[118:121]
	v_mfma_f32_16x16x32_f16 v[110:113], v[154:157], v[194:197], v[110:113]
	v_mfma_f32_16x16x32_f16 v[102:105], v[162:165], v[194:197], v[102:105]
	v_mfma_f32_16x16x32_f16 v[94:97], v[154:157], v[202:205], v[94:97]
	v_mfma_f32_16x16x32_f16 v[86:89], v[162:165], v[202:205], v[86:89]
	v_mfma_f32_16x16x32_f16 v[78:81], v[154:157], v[210:213], v[78:81]
	v_mfma_f32_16x16x32_f16 v[70:73], v[162:165], v[210:213], v[70:73]
	v_mfma_f32_16x16x32_f16 v[126:129], v[158:161], v[190:193], v[126:129]
	v_mfma_f32_16x16x32_f16 v[118:121], v[166:169], v[190:193], v[118:121]
	v_mfma_f32_16x16x32_f16 v[110:113], v[158:161], v[198:201], v[110:113]
	v_mfma_f32_16x16x32_f16 v[102:105], v[166:169], v[198:201], v[102:105]
	v_mfma_f32_16x16x32_f16 v[94:97], v[158:161], v[206:209], v[94:97]
	v_mfma_f32_16x16x32_f16 v[86:89], v[166:169], v[206:209], v[86:89]
	v_mfma_f32_16x16x32_f16 v[78:81], v[158:161], v[214:217], v[78:81]
	v_mfma_f32_16x16x32_f16 v[70:73], v[166:169], v[214:217], v[70:73]
	v_mfma_f32_16x16x32_f16 v[122:125], v[170:173], v[186:189], v[122:125]
	v_mfma_f32_16x16x32_f16 v[114:117], v[178:181], v[186:189], v[114:117]
	v_mfma_f32_16x16x32_f16 v[106:109], v[170:173], v[194:197], v[106:109]
	v_mfma_f32_16x16x32_f16 v[98:101], v[178:181], v[194:197], v[98:101]
	v_mfma_f32_16x16x32_f16 v[90:93], v[170:173], v[202:205], v[90:93]
	v_mfma_f32_16x16x32_f16 v[82:85], v[178:181], v[202:205], v[82:85]
	v_mfma_f32_16x16x32_f16 v[74:77], v[170:173], v[210:213], v[74:77]
	v_mfma_f32_16x16x32_f16 v[66:69], v[178:181], v[210:213], v[66:69]
	v_mfma_f32_16x16x32_f16 v[122:125], v[174:177], v[190:193], v[122:125]
	v_mfma_f32_16x16x32_f16 v[114:117], v[182:185], v[190:193], v[114:117]
	v_mfma_f32_16x16x32_f16 v[106:109], v[174:177], v[198:201], v[106:109]
	v_mfma_f32_16x16x32_f16 v[98:101], v[182:185], v[198:201], v[98:101]
	v_mfma_f32_16x16x32_f16 v[90:93], v[174:177], v[206:209], v[90:93]
	v_mfma_f32_16x16x32_f16 v[82:85], v[182:185], v[206:209], v[82:85]
	v_mfma_f32_16x16x32_f16 v[74:77], v[174:177], v[214:217], v[74:77]
	v_mfma_f32_16x16x32_f16 v[66:69], v[182:185], v[214:217], v[66:69]
	s_barrier
	s_add_i32 s48, s40, s28
	v_lshl_add_u64 v[218:219], s[22:23], 0, v[134:135]
	s_mov_b32 m0, s48
	s_nop 0
	global_load_lds_dwordx4 v[218:219], off
	s_add_i32 m0, s48, 0x2000
	s_add_u32 s48, s22, 0x40000
	v_lshl_add_u64 v[220:221], s[22:23], 0, v[130:131]
	s_addc_u32 s49, s23, 0
	s_add_i32 s50, s41, s28
	global_load_lds_dwordx4 v[220:221], off
	v_lshl_add_u64 v[222:223], s[48:49], 0, v[134:135]
	s_mov_b32 m0, s50
	v_lshl_add_u64 v[224:225], s[24:25], 0, v[132:133]
	global_load_lds_dwordx4 v[222:223], off
	v_lshl_add_u64 v[222:223], s[48:49], 0, v[130:131]
	s_add_i32 m0, s50, 0x2000
	s_nop 0
	global_load_lds_dwordx4 v[222:223], off
	v_lshl_add_u64 v[222:223], s[24:25], 0, v[136:137]
	s_mov_b32 m0, s30
	s_nop 0
	global_load_lds_dwordx4 v[222:223], off
	s_mov_b32 m0, s31
	s_nop 0
	global_load_lds_dwordx4 v[224:225], off
	ds_read_b128 v[186:189], v153 offset:16384
	ds_read_b128 v[190:193], v153 offset:17408
	ds_read_b128 v[194:197], v153 offset:18432
	ds_read_b128 v[198:201], v153 offset:19456
	ds_read_b128 v[202:205], v153 offset:20480
	ds_read_b128 v[206:209], v153 offset:21504
	ds_read_b128 v[210:213], v153 offset:22528
	ds_read_b128 v[214:217], v153 offset:23552
	s_waitcnt vmcnt(8)
	s_waitcnt lgkmcnt(0)
	s_barrier
; #define GM_LDA(dst, b, h) do { _Pragma("unroll") for (int m = 0; m < 4; ++m) _Pragma("unroll") for (int k = 0; k < 2; ++k) dst[m][k] = *(const LAS s16x8*)(lds + GM_SA(b, h) + aoff + m * 2048 + k * 1024); } while (0)
; #define GM_LDB(dst, b, h) do { _Pragma("unroll") for (int n = 0; n < 2; ++n) _Pragma("unroll") for (int k = 0; k < 2; ++k) dst[n][k] = *(const LAS s16x8*)(lds + GM_SB(b, h) + boff + n * 2048 + k * 1024); } while (0)
; #define GM_MMA(ai, bj, At, Bt) do { __builtin_amdgcn_s_setprio(1); _Pragma("unroll") for (int m = 0; m < 4; ++m) _Pragma("unroll") for (int n = 0; n < 2; ++n) _Pragma("unroll") for (int k = 0; k < 2; ++k) \
;         acc[ai][bj][m][n] = mma16<BF>(Bt[n][k], At[m][k], acc[ai][bj][m][n]); __builtin_amdgcn_s_setprio(0); } while (0)
; #define GM_WAIT_V(n) asm volatile("s_waitcnt vmcnt(" #n ")" ::: "memory")
; #define GM_WAIT_L(n) asm volatile("s_waitcnt lgkmcnt(" #n ")" ::: "memory")
; #define GM_BAR __builtin_amdgcn_s_barrier()
; #define GM_SCHED __builtin_amdgcn_sched_barrier(0)
; #define GM_STA_H1(buf, p, o1) do { if constexpr (GATHER) GM_STAGE(buf, p, o1); else GM_STAGE(buf, (p) + hstepB, voffA); } while (0)
; template <bool BF, bool GATHER = false, class Epi, class Hook>
; __device__ __forceinline__ void gemm_phase(LAS unsigned char* lds, const Gemm g, const Order& S, const Epi& E, Hook& HK) {
;     ...
;             GM_WAIT_V(8); GM_WAIT_L(0); GM_BAR; GM_MMA(1, 0, At, B0); GM_MMA(1, 1, At, B1); GM_BAR; GM_SCHED;
;             GM_LDB(B0, 1, 0); GM_LDB(B1, 1, 1); GM_SCHED; GM_LDA(At, 1, 0); GM_STA_H1(GM_SA(0, 1), a2, s1);
;             GM_WAIT_V(8); GM_WAIT_L(0); GM_BAR; GM_MMA(0, 0, At, B0); GM_MMA(0, 1, At, B1); GM_BAR; GM_SCHED;
	v_mfma_f32_16x16x32_f16 v[62:65], v[154:157], v[186:189], v[62:65]
	v_mfma_f32_16x16x32_f16 v[54:57], v[162:165], v[186:189], v[54:57]
	v_mfma_f32_16x16x32_f16 v[46:49], v[154:157], v[194:197], v[46:49]
	v_mfma_f32_16x16x32_f16 v[38:41], v[162:165], v[194:197], v[38:41]
	v_mfma_f32_16x16x32_f16 v[30:33], v[154:157], v[202:205], v[30:33]
	v_mfma_f32_16x16x32_f16 v[22:25], v[162:165], v[202:205], v[22:25]
	v_mfma_f32_16x16x32_f16 v[14:17], v[154:157], v[210:213], v[14:17]
	v_mfma_f32_16x16x32_f16 v[6:9], v[162:165], v[210:213], v[6:9]
	v_mfma_f32_16x16x32_f16 v[62:65], v[158:161], v[190:193], v[62:65]
	v_mfma_f32_16x16x32_f16 v[54:57], v[166:169], v[190:193], v[54:57]
	v_mfma_f32_16x16x32_f16 v[46:49], v[158:161], v[198:201], v[46:49]
	v_mfma_f32_16x16x32_f16 v[38:41], v[166:169], v[198:201], v[38:41]
	v_mfma_f32_16x16x32_f16 v[30:33], v[158:161], v[206:209], v[30:33]
	v_mfma_f32_16x16x32_f16 v[22:25], v[166:169], v[206:209], v[22:25]
	v_mfma_f32_16x16x32_f16 v[14:17], v[158:161], v[214:217], v[14:17]
	v_mfma_f32_16x16x32_f16 v[6:9], v[166:169], v[214:217], v[6:9]
	v_mfma_f32_16x16x32_f16 v[58:61], v[170:173], v[186:189], v[58:61]
	v_mfma_f32_16x16x32_f16 v[50:53], v[178:181], v[186:189], v[50:53]
	v_mfma_f32_16x16x32_f16 v[42:45], v[170:173], v[194:197], v[42:45]
	v_mfma_f32_16x16x32_f16 v[34:37], v[178:181], v[194:197], v[34:37]
	v_mfma_f32_16x16x32_f16 v[26:29], v[170:173], v[202:205], v[26:29]
	v_mfma_f32_16x16x32_f16 v[18:21], v[178:181], v[202:205], v[18:21]
	v_mfma_f32_16x16x32_f16 v[10:13], v[170:173], v[210:213], v[10:13]
	v_mfma_f32_16x16x32_f16 v[2:5], v[178:181], v[210:213], v[2:5]
	v_mfma_f32_16x16x32_f16 v[58:61], v[174:177], v[190:193], v[58:61]
	v_mfma_f32_16x16x32_f16 v[50:53], v[182:185], v[190:193], v[50:53]
	v_mfma_f32_16x16x32_f16 v[42:45], v[174:177], v[198:201], v[42:45]
	v_mfma_f32_16x16x32_f16 v[34:37], v[182:185], v[198:201], v[34:37]
	v_mfma_f32_16x16x32_f16 v[26:29], v[174:177], v[206:209], v[26:29]
	v_mfma_f32_16x16x32_f16 v[18:21], v[182:185], v[206:209], v[18:21]
	v_mfma_f32_16x16x32_f16 v[10:13], v[174:177], v[214:217], v[10:13]
	v_mfma_f32_16x16x32_f16 v[2:5], v[182:185], v[214:217], v[2:5]
	s_barrier
	s_add_u32 s24, s24, 0x40000
	s_addc_u32 s25, s25, 0
	s_mov_b32 m0, s33
	v_lshl_add_u64 v[226:227], s[24:25], 0, v[136:137]
	global_load_lds_dwordx4 v[226:227], off
	v_lshl_add_u64 v[226:227], s[24:25], 0, v[132:133]
	s_mov_b32 m0, s34
	s_nop 0
	global_load_lds_dwordx4 v[226:227], off
	s_mov_b32 s49, 0x1c000
	s_mov_b32 s48, 0x18000
	v_add_u32_e32 v244, s48, v148
	ds_read_b128 v[154:157], v244
	ds_read_b128 v[158:161], v244 offset:1024
	ds_read_b128 v[162:165], v244 offset:2048
	ds_read_b128 v[166:169], v244 offset:3072
	v_add_u32_e32 v244, s49, v148
	ds_read_b128 v[170:173], v244
	ds_read_b128 v[174:177], v244 offset:1024
	ds_read_b128 v[178:181], v244 offset:2048
	ds_read_b128 v[182:185], v244 offset:3072
	ds_read_b128 v[186:189], v153 offset:32768
	ds_read_b128 v[190:193], v153 offset:33792
	ds_read_b128 v[194:197], v153 offset:34816
	ds_read_b128 v[198:201], v153 offset:35840
	ds_read_b128 v[202:205], v153 offset:36864
	ds_read_b128 v[206:209], v153 offset:37888
	ds_read_b128 v[210:213], v153 offset:38912
	ds_read_b128 v[214:217], v153 offset:39936
	s_waitcnt vmcnt(8)
	s_waitcnt lgkmcnt(0)
	s_barrier
	v_mfma_f32_16x16x32_f16 v[126:129], v[154:157], v[186:189], v[126:129]
	v_mfma_f32_16x16x32_f16 v[118:121], v[162:165], v[186:189], v[118:121]
	v_mfma_f32_16x16x32_f16 v[110:113], v[154:157], v[194:197], v[110:113]
	v_mfma_f32_16x16x32_f16 v[102:105], v[162:165], v[194:197], v[102:105]
	v_mfma_f32_16x16x32_f16 v[94:97], v[154:157], v[202:205], v[94:97]
	v_mfma_f32_16x16x32_f16 v[86:89], v[162:165], v[202:205], v[86:89]
	v_mfma_f32_16x16x32_f16 v[78:81], v[154:157], v[210:213], v[78:81]
	v_mfma_f32_16x16x32_f16 v[70:73], v[162:165], v[210:213], v[70:73]
	v_mfma_f32_16x16x32_f16 v[126:129], v[158:161], v[190:193], v[126:129]
	v_mfma_f32_16x16x32_f16 v[118:121], v[166:169], v[190:193], v[118:121]
	v_mfma_f32_16x16x32_f16 v[110:113], v[158:161], v[198:201], v[110:113]
	v_mfma_f32_16x16x32_f16 v[102:105], v[166:169], v[198:201], v[102:105]
	v_mfma_f32_16x16x32_f16 v[94:97], v[158:161], v[206:209], v[94:97]
	v_mfma_f32_16x16x32_f16 v[86:89], v[166:169], v[206:209], v[86:89]
	v_mfma_f32_16x16x32_f16 v[78:81], v[158:161], v[214:217], v[78:81]
	v_mfma_f32_16x16x32_f16 v[70:73], v[166:169], v[214:217], v[70:73]
	v_mfma_f32_16x16x32_f16 v[122:125], v[170:173], v[186:189], v[122:125]
	v_mfma_f32_16x16x32_f16 v[114:117], v[178:181], v[186:189], v[114:117]
	v_mfma_f32_16x16x32_f16 v[106:109], v[170:173], v[194:197], v[106:109]
	v_mfma_f32_16x16x32_f16 v[98:101], v[178:181], v[194:197], v[98:101]
	v_mfma_f32_16x16x32_f16 v[90:93], v[170:173], v[202:205], v[90:93]
	v_mfma_f32_16x16x32_f16 v[82:85], v[178:181], v[202:205], v[82:85]
	v_mfma_f32_16x16x32_f16 v[74:77], v[170:173], v[210:213], v[74:77]
	v_mfma_f32_16x16x32_f16 v[66:69], v[178:181], v[210:213], v[66:69]
	v_mfma_f32_16x16x32_f16 v[122:125], v[174:177], v[190:193], v[122:125]
	v_mfma_f32_16x16x32_f16 v[114:117], v[182:185], v[190:193], v[114:117]
	v_mfma_f32_16x16x32_f16 v[106:109], v[174:177], v[198:201], v[106:109]
	v_mfma_f32_16x16x32_f16 v[98:101], v[182:185], v[198:201], v[98:101]
	v_mfma_f32_16x16x32_f16 v[90:93], v[174:177], v[206:209], v[90:93]
	v_mfma_f32_16x16x32_f16 v[82:85], v[182:185], v[206:209], v[82:85]
	v_mfma_f32_16x16x32_f16 v[74:77], v[174:177], v[214:217], v[74:77]
	v_mfma_f32_16x16x32_f16 v[66:69], v[182:185], v[214:217], v[66:69]
	s_barrier
; #define GM_STAGE(bufoff, gbase, voff) do { _Pragma("unroll") for (int _i = 0; _i < 2; ++_i) \
;         __builtin_amdgcn_global_load_lds((const unsigned*)((const char*)(gbase) + (voff)[_i]), (LAS unsigned*)(lds + (bufoff) + ldsw + _i * 8192), 16, 0, 0); } while (0)
; #define GM_LDA(dst, b, h) do { _Pragma("unroll") for (int m = 0; m < 4; ++m) _Pragma("unroll") for (int k = 0; k < 2; ++k) dst[m][k] = *(const LAS s16x8*)(lds + GM_SA(b, h) + aoff + m * 2048 + k * 1024); } while (0)
; #define GM_MMA(ai, bj, At, Bt) do { __builtin_amdgcn_s_setprio(1); _Pragma("unroll") for (int m = 0; m < 4; ++m) _Pragma("unroll") for (int n = 0; n < 2; ++n) _Pragma("unroll") for (int k = 0; k < 2; ++k) \
;         acc[ai][bj][m][n] = mma16<BF>(Bt[n][k], At[m][k], acc[ai][bj][m][n]); __builtin_amdgcn_s_setprio(0); } while (0)
; #define GM_WAIT_V(n) asm volatile("s_waitcnt vmcnt(" #n ")" ::: "memory")
; #define GM_WAIT_L(n) asm volatile("s_waitcnt lgkmcnt(" #n ")" ::: "memory")
; #define GM_BAR __builtin_amdgcn_s_barrier()
; #define GM_SCHED __builtin_amdgcn_sched_barrier(0)
; #define GM_STA_H0(buf, p, o0) do { if constexpr (GATHER) GM_STAGE(buf, p, o0); else GM_STAGE(buf, p, voffA); } while (0)
;     __device__ __forceinline__ void operator()(const Acc& acc, const Unit& u, int wr, int wc, int fr, int fq) const {
;         const int row0 = u.pm * BM + wr * 64 + fr;
;         if (u.pn < 8) {
; template <bool BF, bool GATHER = false, class Epi, class Hook>
; __device__ __forceinline__ void gemm_phase(LAS unsigned char* lds, const Gemm g, const Order& S, const Epi& E, Hook& HK) {
;     ...
;             GM_LDA(At, 1, 1); GM_STAGE(GM_SB(1, 0), b3, voffB); GM_STAGE(GM_SB(1, 1), b3 + hstepB, voffB); GM_STA_H0(GM_SA(1, 0), a3, s0);
;             GM_WAIT_V(8); GM_WAIT_L(0); GM_BAR; GM_MMA(1, 0, At, B0); GM_MMA(1, 1, At, B1); GM_BAR; GM_SCHED;
;         }
;         if (wr == 0) GM_BAR;
	s_add_i32 s24, s48, s28
	v_lshl_add_u64 v[218:219], v[218:219], 0, s[8:9]
	s_mov_b32 m0, s24
	s_nop 0
	global_load_lds_dwordx4 v[218:219], off
	s_add_i32 m0, s24, 0x2000
	s_add_u32 s22, s22, 0x40080
	v_lshl_add_u64 v[218:219], v[220:221], 0, s[8:9]
	s_addc_u32 s23, s23, 0
	s_add_i32 s24, s49, s28
	global_load_lds_dwordx4 v[218:219], off
	v_lshl_add_u64 v[218:219], s[22:23], 0, v[134:135]
	s_mov_b32 m0, s24
	s_nop 0
	global_load_lds_dwordx4 v[218:219], off
	v_lshl_add_u64 v[218:219], s[22:23], 0, v[130:131]
	s_add_i32 m0, s24, 0x2000
	s_nop 0
	global_load_lds_dwordx4 v[218:219], off
	v_lshl_add_u64 v[218:219], v[222:223], 0, s[8:9]
	s_mov_b32 m0, s37
	s_nop 0
	global_load_lds_dwordx4 v[218:219], off
	v_lshl_add_u64 v[218:219], v[224:225], 0, s[8:9]
	s_mov_b32 m0, s38
	s_nop 0
	global_load_lds_dwordx4 v[218:219], off
	ds_read_b128 v[186:189], v153 offset:49152
	ds_read_b128 v[190:193], v153 offset:50176
	ds_read_b128 v[194:197], v153 offset:51200
	ds_read_b128 v[198:201], v153 offset:52224
	ds_read_b128 v[202:205], v153 offset:53248
	ds_read_b128 v[206:209], v153 offset:54272
	ds_read_b128 v[210:213], v153 offset:55296
	ds_read_b128 v[214:217], v153 offset:56320
	s_waitcnt vmcnt(8)
	s_waitcnt lgkmcnt(0)
	s_barrier
	v_mfma_f32_16x16x32_f16 v[62:65], v[154:157], v[186:189], v[62:65]
	v_mfma_f32_16x16x32_f16 v[54:57], v[162:165], v[186:189], v[54:57]
	v_mfma_f32_16x16x32_f16 v[46:49], v[154:157], v[194:197], v[46:49]
	v_mfma_f32_16x16x32_f16 v[38:41], v[162:165], v[194:197], v[38:41]
	v_mfma_f32_16x16x32_f16 v[30:33], v[154:157], v[202:205], v[30:33]
	v_mfma_f32_16x16x32_f16 v[22:25], v[162:165], v[202:205], v[22:25]
	v_mfma_f32_16x16x32_f16 v[14:17], v[154:157], v[210:213], v[14:17]
	v_mfma_f32_16x16x32_f16 v[6:9], v[162:165], v[210:213], v[6:9]
	v_mfma_f32_16x16x32_f16 v[62:65], v[158:161], v[190:193], v[62:65]
	v_mfma_f32_16x16x32_f16 v[54:57], v[166:169], v[190:193], v[54:57]
	v_mfma_f32_16x16x32_f16 v[46:49], v[158:161], v[198:201], v[46:49]
	v_mfma_f32_16x16x32_f16 v[38:41], v[166:169], v[198:201], v[38:41]
	v_mfma_f32_16x16x32_f16 v[30:33], v[158:161], v[206:209], v[30:33]
	v_mfma_f32_16x16x32_f16 v[22:25], v[166:169], v[206:209], v[22:25]
	v_mfma_f32_16x16x32_f16 v[14:17], v[158:161], v[214:217], v[14:17]
	v_mfma_f32_16x16x32_f16 v[6:9], v[166:169], v[214:217], v[6:9]
	v_mfma_f32_16x16x32_f16 v[58:61], v[170:173], v[186:189], v[58:61]
	v_mfma_f32_16x16x32_f16 v[50:53], v[178:181], v[186:189], v[50:53]
	v_mfma_f32_16x16x32_f16 v[42:45], v[170:173], v[194:197], v[42:45]
	v_mfma_f32_16x16x32_f16 v[34:37], v[178:181], v[194:197], v[34:37]
	v_mfma_f32_16x16x32_f16 v[26:29], v[170:173], v[202:205], v[26:29]
	v_mfma_f32_16x16x32_f16 v[18:21], v[178:181], v[202:205], v[18:21]
	v_mfma_f32_16x16x32_f16 v[10:13], v[170:173], v[210:213], v[10:13]
	v_mfma_f32_16x16x32_f16 v[2:5], v[178:181], v[210:213], v[2:5]
	v_mfma_f32_16x16x32_f16 v[58:61], v[174:177], v[190:193], v[58:61]
	v_mfma_f32_16x16x32_f16 v[50:53], v[182:185], v[190:193], v[50:53]
	v_mfma_f32_16x16x32_f16 v[42:45], v[174:177], v[198:201], v[42:45]
	v_mfma_f32_16x16x32_f16 v[34:37], v[182:185], v[198:201], v[34:37]
	v_mfma_f32_16x16x32_f16 v[26:29], v[174:177], v[206:209], v[26:29]
	v_mfma_f32_16x16x32_f16 v[18:21], v[182:185], v[206:209], v[18:21]
	v_mfma_f32_16x16x32_f16 v[10:13], v[174:177], v[214:217], v[10:13]
	v_mfma_f32_16x16x32_f16 v[2:5], v[182:185], v[214:217], v[2:5]
	s_barrier
	s_add_i32 s47, s47, 2
	s_add_u32 s20, s20, 0x100
	s_addc_u32 s21, s21, 0
	s_add_u32 s45, s45, 0x100
	s_addc_u32 s46, s46, 0
	s_cmp_gt_u32 s47, 13
	s_cbranch_scc0 .LBB0_1281
	s_and_b64 vcc, exec, s[10:11]
	s_cbranch_vccnz .LBB0_1286
	v_lshl_add_u32 v154, s2, 8, v1
	s_cmp_gt_i32 s43, 7
	s_mov_b64 s[2:3], -1
	s_cbranch_scc1 .LBB0_1287

; #define GM_STAGE(bufoff, gbase, voff) do { _Pragma("unroll") for (int _i = 0; _i < 2; ++_i) \
;         __builtin_amdgcn_global_load_lds((const unsigned*)((const char*)(gbase) + (voff)[_i]), (LAS unsigned*)(lds + (bufoff) + ldsw + _i * 8192), 16, 0, 0); } while (0)
; #define GM_LDA(dst, b, h) do { _Pragma("unroll") for (int m = 0; m < 4; ++m) _Pragma("unroll") for (int k = 0; k < 2; ++k) dst[m][k] = *(const LAS s16x8*)(lds + GM_SA(b, h) + aoff + m * 2048 + k * 1024); } while (0)
; #define GM_LDB(dst, b, h) do { _Pragma("unroll") for (int n = 0; n < 2; ++n) _Pragma("unroll") for (int k = 0; k < 2; ++k) dst[n][k] = *(const LAS s16x8*)(lds + GM_SB(b, h) + boff + n * 2048 + k * 1024); } while (0)
; #define GM_MMA(ai, bj, At, Bt) do { __builtin_amdgcn_s_setprio(1); _Pragma("unroll") for (int m = 0; m < 4; ++m) _Pragma("unroll") for (int n = 0; n < 2; ++n) _Pragma("unroll") for (int k = 0; k < 2; ++k) \
;         acc[ai][bj][m][n] = mma16<BF>(Bt[n][k], At[m][k], acc[ai][bj][m][n]); __builtin_amdgcn_s_setprio(0); } while (0)
; #define GM_WAIT_V(n) asm volatile("s_waitcnt vmcnt(" #n ")" ::: "memory")
; #define GM_WAIT_L(n) asm volatile("s_waitcnt lgkmcnt(" #n ")" ::: "memory")
; #define GM_BAR __builtin_amdgcn_s_barrier()
; template <bool BF, bool GATHER = false, class Epi, class Hook>
; __device__ __forceinline__ void gemm_phase(LAS unsigned char* lds, const Gemm g, const Order& S, const Epi& E, Hook& HK) {
;     ...
;         for (int t = 0; t < nt; t += 2) {
;             const bool last = (t == nt - 2);
;             const char* a1 = cA + (size_t)(t + 1) * kstep;
;             const char* a2 = last ? nA : cA + (size_t)(t + 2) * kstep; const char* b2 = last ? nB : cB + (size_t)(t + 2) * kstep;
;             const char* a3 = a2 + kstep; const char* b3 = b2 + kstep;
;             unsigned s0[2], s1[2];
;             if constexpr (GATHER) { s0[0] = last ? nA0[0] : gA0[0]; s0[1] = last ? nA0[1] : gA0[1]; s1[0] = last ? nA1[0] : gA1[0]; s1[1] = last ? nA1[1] : gA1[1]; }
;             GM_LDB(B0, 0, 0); GM_LDB(B1, 0, 1); GM_SCHED; GM_LDA(At, 0, 0); GM_STA_H1(GM_SA(1, 1), a1, gA1);
;             GM_WAIT_V(8); GM_WAIT_L(0); GM_BAR; GM_MMA(0, 0, At, B0); GM_MMA(0, 1, At, B1); GM_BAR; GM_SCHED;
;             GM_LDA(At, 0, 1); GM_STAGE(GM_SB(0, 0), b2, voffB); GM_STAGE(GM_SB(0, 1), b2 + hstepB, voffB); GM_STA_H0(GM_SA(0, 0), a2, s0);
.LBB0_1480:
	s_add_u32 s24, s22, 0xfffc0080
	s_addc_u32 s25, s23, -1
	s_cmp_eq_u32 s49, 12
	s_cselect_b32 s27, s15, s25
	s_cselect_b32 s26, s45, s24
	s_cselect_b32 s25, s17, s48
	s_cselect_b32 s24, s46, s47
	v_lshl_add_u64 v[216:217], s[22:23], 0, v[154:155]
	s_add_i32 m0, s33, 0xc000
	s_nop 0
	global_load_lds_dwordx4 v[216:217], off
	v_lshl_add_u64 v[216:217], s[22:23], 0, v[156:157]
	s_add_i32 m0, s33, 0xe000
	s_nop 0
	global_load_lds_dwordx4 v[216:217], off
	ds_read_b128 v[122:125], v168
	ds_read_b128 v[126:129], v168 offset:1024
	ds_read_b128 v[130:133], v168 offset:2048
	ds_read_b128 v[134:137], v168 offset:3072
	ds_read_b128 v[162:165], v169
	ds_read_b128 v[172:175], v169 offset:1024
	ds_read_b128 v[176:179], v169 offset:2048
	ds_read_b128 v[180:183], v169 offset:3072
	ds_read_b128 v[184:187], v170
	ds_read_b128 v[188:191], v170 offset:1024
	ds_read_b128 v[192:195], v170 offset:2048
	ds_read_b128 v[196:199], v170 offset:3072
	ds_read_b128 v[200:203], v170 offset:4096
	ds_read_b128 v[204:207], v170 offset:5120
	ds_read_b128 v[208:211], v170 offset:6144
	ds_read_b128 v[212:215], v170 offset:7168
	s_waitcnt vmcnt(8)
	s_waitcnt lgkmcnt(0)
	s_barrier
	v_mfma_f32_16x16x32_f16 v[142:145], v[122:125], v[184:187], v[142:145]
	v_mfma_f32_16x16x32_f16 v[138:141], v[130:133], v[184:187], v[138:141]
	v_mfma_f32_16x16x32_f16 v[110:113], v[122:125], v[192:195], v[110:113]
	v_mfma_f32_16x16x32_f16 v[106:109], v[130:133], v[192:195], v[106:109]
	v_mfma_f32_16x16x32_f16 v[94:97], v[122:125], v[200:203], v[94:97]
	v_mfma_f32_16x16x32_f16 v[90:93], v[130:133], v[200:203], v[90:93]
	v_mfma_f32_16x16x32_f16 v[78:81], v[122:125], v[208:211], v[78:81]
	v_mfma_f32_16x16x32_f16 v[74:77], v[130:133], v[208:211], v[74:77]
	v_mfma_f32_16x16x32_f16 v[142:145], v[126:129], v[188:191], v[142:145]
	v_mfma_f32_16x16x32_f16 v[138:141], v[134:137], v[188:191], v[138:141]
	v_mfma_f32_16x16x32_f16 v[110:113], v[126:129], v[196:199], v[110:113]
	v_mfma_f32_16x16x32_f16 v[106:109], v[134:137], v[196:199], v[106:109]
	v_mfma_f32_16x16x32_f16 v[94:97], v[126:129], v[204:207], v[94:97]
	v_mfma_f32_16x16x32_f16 v[90:93], v[134:137], v[204:207], v[90:93]
	v_mfma_f32_16x16x32_f16 v[78:81], v[126:129], v[212:215], v[78:81]
	v_mfma_f32_16x16x32_f16 v[74:77], v[134:137], v[212:215], v[74:77]
	v_mfma_f32_16x16x32_f16 v[118:121], v[162:165], v[184:187], v[118:121]
	v_mfma_f32_16x16x32_f16 v[114:117], v[176:179], v[184:187], v[114:117]
	v_mfma_f32_16x16x32_f16 v[102:105], v[162:165], v[192:195], v[102:105]
	v_mfma_f32_16x16x32_f16 v[98:101], v[176:179], v[192:195], v[98:101]
	v_mfma_f32_16x16x32_f16 v[86:89], v[162:165], v[200:203], v[86:89]
	v_mfma_f32_16x16x32_f16 v[82:85], v[176:179], v[200:203], v[82:85]
	v_mfma_f32_16x16x32_f16 v[70:73], v[162:165], v[208:211], v[70:73]
	v_mfma_f32_16x16x32_f16 v[66:69], v[176:179], v[208:211], v[66:69]
	v_mfma_f32_16x16x32_f16 v[118:121], v[172:175], v[188:191], v[118:121]
	v_mfma_f32_16x16x32_f16 v[114:117], v[180:183], v[188:191], v[114:117]
	v_mfma_f32_16x16x32_f16 v[102:105], v[172:175], v[196:199], v[102:105]
	v_mfma_f32_16x16x32_f16 v[98:101], v[180:183], v[196:199], v[98:101]
	v_mfma_f32_16x16x32_f16 v[86:89], v[172:175], v[204:207], v[86:89]
	v_mfma_f32_16x16x32_f16 v[82:85], v[180:183], v[204:207], v[82:85]
	v_mfma_f32_16x16x32_f16 v[70:73], v[172:175], v[212:215], v[70:73]
	v_mfma_f32_16x16x32_f16 v[66:69], v[180:183], v[212:215], v[66:69]
	s_barrier
	s_add_i32 s50, s43, s31
	v_lshl_add_u64 v[216:217], s[24:25], 0, v[148:149]
	s_mov_b32 m0, s50
	s_nop 0
	global_load_lds_dwordx4 v[216:217], off
	s_add_i32 m0, s50, 0x2000
	s_add_u32 s50, s24, 0x40000
	v_lshl_add_u64 v[218:219], s[24:25], 0, v[152:153]
	s_addc_u32 s51, s25, 0
	s_add_i32 s52, s44, s31
	global_load_lds_dwordx4 v[218:219], off
	v_lshl_add_u64 v[220:221], s[50:51], 0, v[148:149]
	s_mov_b32 m0, s52
	v_lshl_add_u64 v[222:223], s[26:27], 0, v[150:151]
	global_load_lds_dwordx4 v[220:221], off
	v_lshl_add_u64 v[220:221], s[50:51], 0, v[152:153]
	s_add_i32 m0, s52, 0x2000
	s_nop 0
	global_load_lds_dwordx4 v[220:221], off
	v_lshl_add_u64 v[220:221], s[26:27], 0, v[146:147]
	s_mov_b32 m0, s33
	s_nop 0
	global_load_lds_dwordx4 v[220:221], off
	s_mov_b32 m0, s34
	s_nop 0
	global_load_lds_dwordx4 v[222:223], off
	ds_read_b128 v[184:187], v170 offset:16384
	ds_read_b128 v[188:191], v170 offset:17408
	ds_read_b128 v[192:195], v170 offset:18432
	ds_read_b128 v[196:199], v170 offset:19456
	ds_read_b128 v[200:203], v170 offset:20480
	ds_read_b128 v[204:207], v170 offset:21504
	ds_read_b128 v[208:211], v170 offset:22528
	ds_read_b128 v[212:215], v170 offset:23552
	s_waitcnt vmcnt(8)
	s_waitcnt lgkmcnt(0)
	s_barrier
; #define GM_LDA(dst, b, h) do { _Pragma("unroll") for (int m = 0; m < 4; ++m) _Pragma("unroll") for (int k = 0; k < 2; ++k) dst[m][k] = *(const LAS s16x8*)(lds + GM_SA(b, h) + aoff + m * 2048 + k * 1024); } while (0)
; #define GM_LDB(dst, b, h) do { _Pragma("unroll") for (int n = 0; n < 2; ++n) _Pragma("unroll") for (int k = 0; k < 2; ++k) dst[n][k] = *(const LAS s16x8*)(lds + GM_SB(b, h) + boff + n * 2048 + k * 1024); } while (0)
; #define GM_MMA(ai, bj, At, Bt) do { __builtin_amdgcn_s_setprio(1); _Pragma("unroll") for (int m = 0; m < 4; ++m) _Pragma("unroll") for (int n = 0; n < 2; ++n) _Pragma("unroll") for (int k = 0; k < 2; ++k) \
;         acc[ai][bj][m][n] = mma16<BF>(Bt[n][k], At[m][k], acc[ai][bj][m][n]); __builtin_amdgcn_s_setprio(0); } while (0)
; #define GM_WAIT_V(n) asm volatile("s_waitcnt vmcnt(" #n ")" ::: "memory")
; #define GM_WAIT_L(n) asm volatile("s_waitcnt lgkmcnt(" #n ")" ::: "memory")
; #define GM_BAR __builtin_amdgcn_s_barrier()
; #define GM_SCHED __builtin_amdgcn_sched_barrier(0)
; #define GM_STA_H1(buf, p, o1) do { if constexpr (GATHER) GM_STAGE(buf, p, o1); else GM_STAGE(buf, (p) + hstepB, voffA); } while (0)
; template <bool BF, bool GATHER = false, class Epi, class Hook>
; __device__ __forceinline__ void gemm_phase(LAS unsigned char* lds, const Gemm g, const Order& S, const Epi& E, Hook& HK) {
;     ...
;             GM_WAIT_V(8); GM_WAIT_L(0); GM_BAR; GM_MMA(1, 0, At, B0); GM_MMA(1, 1, At, B1); GM_BAR; GM_SCHED;
;             GM_LDB(B0, 1, 0); GM_LDB(B1, 1, 1); GM_SCHED; GM_LDA(At, 1, 0); GM_STA_H1(GM_SA(0, 1), a2, s1);
;             GM_WAIT_V(8); GM_WAIT_L(0); GM_BAR; GM_MMA(0, 0, At, B0); GM_MMA(0, 1, At, B1); GM_BAR; GM_SCHED;
	v_mfma_f32_16x16x32_f16 v[62:65], v[122:125], v[184:187], v[62:65]
	v_mfma_f32_16x16x32_f16 v[58:61], v[130:133], v[184:187], v[58:61]
	v_mfma_f32_16x16x32_f16 v[46:49], v[122:125], v[192:195], v[46:49]
	v_mfma_f32_16x16x32_f16 v[42:45], v[130:133], v[192:195], v[42:45]
	v_mfma_f32_16x16x32_f16 v[30:33], v[122:125], v[200:203], v[30:33]
	v_mfma_f32_16x16x32_f16 v[26:29], v[130:133], v[200:203], v[26:29]
	v_mfma_f32_16x16x32_f16 v[14:17], v[122:125], v[208:211], v[14:17]
	v_mfma_f32_16x16x32_f16 v[10:13], v[130:133], v[208:211], v[10:13]
	v_mfma_f32_16x16x32_f16 v[62:65], v[126:129], v[188:191], v[62:65]
	v_mfma_f32_16x16x32_f16 v[58:61], v[134:137], v[188:191], v[58:61]
	v_mfma_f32_16x16x32_f16 v[46:49], v[126:129], v[196:199], v[46:49]
	v_mfma_f32_16x16x32_f16 v[42:45], v[134:137], v[196:199], v[42:45]
	v_mfma_f32_16x16x32_f16 v[30:33], v[126:129], v[204:207], v[30:33]
	v_mfma_f32_16x16x32_f16 v[26:29], v[134:137], v[204:207], v[26:29]
	v_mfma_f32_16x16x32_f16 v[14:17], v[126:129], v[212:215], v[14:17]
	v_mfma_f32_16x16x32_f16 v[10:13], v[134:137], v[212:215], v[10:13]
	v_mfma_f32_16x16x32_f16 v[54:57], v[162:165], v[184:187], v[54:57]
	v_mfma_f32_16x16x32_f16 v[50:53], v[176:179], v[184:187], v[50:53]
	v_mfma_f32_16x16x32_f16 v[38:41], v[162:165], v[192:195], v[38:41]
	v_mfma_f32_16x16x32_f16 v[34:37], v[176:179], v[192:195], v[34:37]
	v_mfma_f32_16x16x32_f16 v[22:25], v[162:165], v[200:203], v[22:25]
	v_mfma_f32_16x16x32_f16 v[18:21], v[176:179], v[200:203], v[18:21]
	v_mfma_f32_16x16x32_f16 v[6:9], v[162:165], v[208:211], v[6:9]
	v_mfma_f32_16x16x32_f16 v[2:5], v[176:179], v[208:211], v[2:5]
	v_mfma_f32_16x16x32_f16 v[54:57], v[172:175], v[188:191], v[54:57]
	v_mfma_f32_16x16x32_f16 v[50:53], v[180:183], v[188:191], v[50:53]
	v_mfma_f32_16x16x32_f16 v[38:41], v[172:175], v[196:199], v[38:41]
	v_mfma_f32_16x16x32_f16 v[34:37], v[180:183], v[196:199], v[34:37]
	v_mfma_f32_16x16x32_f16 v[22:25], v[172:175], v[204:207], v[22:25]
	v_mfma_f32_16x16x32_f16 v[18:21], v[180:183], v[204:207], v[18:21]
	v_mfma_f32_16x16x32_f16 v[6:9], v[172:175], v[212:215], v[6:9]
	v_mfma_f32_16x16x32_f16 v[2:5], v[180:183], v[212:215], v[2:5]
	s_barrier
	s_add_u32 s26, s26, 0x40000
	s_addc_u32 s27, s27, 0
	s_mov_b32 m0, s35
	v_lshl_add_u64 v[224:225], s[26:27], 0, v[146:147]
	global_load_lds_dwordx4 v[224:225], off
	v_lshl_add_u64 v[224:225], s[26:27], 0, v[150:151]
	s_mov_b32 m0, s36
	s_nop 0
	global_load_lds_dwordx4 v[224:225], off
	s_mov_b32 s51, 0x1c000
	s_mov_b32 s50, 0x18000
	v_add_u32_e32 v244, s50, v166
	v_add_u32_e32 v245, s51, v166
	ds_read_b128 v[122:125], v244
	ds_read_b128 v[126:129], v244 offset:1024
	ds_read_b128 v[130:133], v244 offset:2048
	ds_read_b128 v[134:137], v244 offset:3072
	ds_read_b128 v[162:165], v245
	ds_read_b128 v[172:175], v245 offset:1024
	ds_read_b128 v[176:179], v245 offset:2048
	ds_read_b128 v[180:183], v245 offset:3072
	ds_read_b128 v[184:187], v170 offset:32768
	ds_read_b128 v[188:191], v170 offset:33792
	ds_read_b128 v[192:195], v170 offset:34816
	ds_read_b128 v[196:199], v170 offset:35840
	ds_read_b128 v[200:203], v170 offset:36864
	ds_read_b128 v[204:207], v170 offset:37888
	ds_read_b128 v[208:211], v170 offset:38912
	ds_read_b128 v[212:215], v170 offset:39936
	s_waitcnt vmcnt(8)
	s_waitcnt lgkmcnt(0)
	s_barrier
	v_mfma_f32_16x16x32_f16 v[142:145], v[122:125], v[184:187], v[142:145]
	v_mfma_f32_16x16x32_f16 v[138:141], v[130:133], v[184:187], v[138:141]
	v_mfma_f32_16x16x32_f16 v[110:113], v[122:125], v[192:195], v[110:113]
	v_mfma_f32_16x16x32_f16 v[106:109], v[130:133], v[192:195], v[106:109]
	v_mfma_f32_16x16x32_f16 v[94:97], v[122:125], v[200:203], v[94:97]
	v_mfma_f32_16x16x32_f16 v[90:93], v[130:133], v[200:203], v[90:93]
	v_mfma_f32_16x16x32_f16 v[78:81], v[122:125], v[208:211], v[78:81]
	v_mfma_f32_16x16x32_f16 v[74:77], v[130:133], v[208:211], v[74:77]
	v_mfma_f32_16x16x32_f16 v[142:145], v[126:129], v[188:191], v[142:145]
	v_mfma_f32_16x16x32_f16 v[138:141], v[134:137], v[188:191], v[138:141]
	v_mfma_f32_16x16x32_f16 v[110:113], v[126:129], v[196:199], v[110:113]
	v_mfma_f32_16x16x32_f16 v[106:109], v[134:137], v[196:199], v[106:109]
	v_mfma_f32_16x16x32_f16 v[94:97], v[126:129], v[204:207], v[94:97]
	v_mfma_f32_16x16x32_f16 v[90:93], v[134:137], v[204:207], v[90:93]
	v_mfma_f32_16x16x32_f16 v[78:81], v[126:129], v[212:215], v[78:81]
	v_mfma_f32_16x16x32_f16 v[74:77], v[134:137], v[212:215], v[74:77]
	v_mfma_f32_16x16x32_f16 v[118:121], v[162:165], v[184:187], v[118:121]
	v_mfma_f32_16x16x32_f16 v[114:117], v[176:179], v[184:187], v[114:117]
	v_mfma_f32_16x16x32_f16 v[102:105], v[162:165], v[192:195], v[102:105]
	v_mfma_f32_16x16x32_f16 v[98:101], v[176:179], v[192:195], v[98:101]
	v_mfma_f32_16x16x32_f16 v[86:89], v[162:165], v[200:203], v[86:89]
	v_mfma_f32_16x16x32_f16 v[82:85], v[176:179], v[200:203], v[82:85]
	v_mfma_f32_16x16x32_f16 v[70:73], v[162:165], v[208:211], v[70:73]
	v_mfma_f32_16x16x32_f16 v[66:69], v[176:179], v[208:211], v[66:69]
	v_mfma_f32_16x16x32_f16 v[118:121], v[172:175], v[188:191], v[118:121]
	v_mfma_f32_16x16x32_f16 v[114:117], v[180:183], v[188:191], v[114:117]
	v_mfma_f32_16x16x32_f16 v[102:105], v[172:175], v[196:199], v[102:105]
	v_mfma_f32_16x16x32_f16 v[98:101], v[180:183], v[196:199], v[98:101]
	v_mfma_f32_16x16x32_f16 v[86:89], v[172:175], v[204:207], v[86:89]
	v_mfma_f32_16x16x32_f16 v[82:85], v[180:183], v[204:207], v[82:85]
	v_mfma_f32_16x16x32_f16 v[70:73], v[172:175], v[212:215], v[70:73]
	v_mfma_f32_16x16x32_f16 v[66:69], v[180:183], v[212:215], v[66:69]
	s_barrier
; #define GM_STAGE(bufoff, gbase, voff) do { _Pragma("unroll") for (int _i = 0; _i < 2; ++_i) \
;         __builtin_amdgcn_global_load_lds((const unsigned*)((const char*)(gbase) + (voff)[_i]), (LAS unsigned*)(lds + (bufoff) + ldsw + _i * 8192), 16, 0, 0); } while (0)
; #define GM_LDA(dst, b, h) do { _Pragma("unroll") for (int m = 0; m < 4; ++m) _Pragma("unroll") for (int k = 0; k < 2; ++k) dst[m][k] = *(const LAS s16x8*)(lds + GM_SA(b, h) + aoff + m * 2048 + k * 1024); } while (0)
; #define GM_MMA(ai, bj, At, Bt) do { __builtin_amdgcn_s_setprio(1); _Pragma("unroll") for (int m = 0; m < 4; ++m) _Pragma("unroll") for (int n = 0; n < 2; ++n) _Pragma("unroll") for (int k = 0; k < 2; ++k) \
;         acc[ai][bj][m][n] = mma16<BF>(Bt[n][k], At[m][k], acc[ai][bj][m][n]); __builtin_amdgcn_s_setprio(0); } while (0)
; #define GM_WAIT_V(n) asm volatile("s_waitcnt vmcnt(" #n ")" ::: "memory")
; #define GM_WAIT_L(n) asm volatile("s_waitcnt lgkmcnt(" #n ")" ::: "memory")
; #define GM_BAR __builtin_amdgcn_s_barrier()
; #define GM_SCHED __builtin_amdgcn_sched_barrier(0)
; #define GM_STA_H0(buf, p, o0) do { if constexpr (GATHER) GM_STAGE(buf, p, o0); else GM_STAGE(buf, p, voffA); } while (0)
; template <bool BF, bool GATHER = false, class Epi, class Hook>
; __device__ __forceinline__ void gemm_phase(LAS unsigned char* lds, const Gemm g, const Order& S, const Epi& E, Hook& HK) {
;     ...
;             GM_LDA(At, 1, 1); GM_STAGE(GM_SB(1, 0), b3, voffB); GM_STAGE(GM_SB(1, 1), b3 + hstepB, voffB); GM_STA_H0(GM_SA(1, 0), a3, s0);
;             GM_WAIT_V(8); GM_WAIT_L(0); GM_BAR; GM_MMA(1, 0, At, B0); GM_MMA(1, 1, At, B1); GM_BAR; GM_SCHED;
;         }
;         if (wr == 0) GM_BAR;
	s_add_i32 s26, s50, s31
	v_lshl_add_u64 v[216:217], v[216:217], 0, s[10:11]
	s_mov_b32 m0, s26
	s_nop 0
	global_load_lds_dwordx4 v[216:217], off
	s_add_i32 m0, s26, 0x2000
	s_add_u32 s24, s24, 0x40080
	v_lshl_add_u64 v[216:217], v[218:219], 0, s[10:11]
	s_addc_u32 s25, s25, 0
	s_add_i32 s26, s51, s31
	global_load_lds_dwordx4 v[216:217], off
	v_lshl_add_u64 v[216:217], s[24:25], 0, v[148:149]
	s_mov_b32 m0, s26
	s_nop 0
	global_load_lds_dwordx4 v[216:217], off
	v_lshl_add_u64 v[216:217], s[24:25], 0, v[152:153]
	s_add_i32 m0, s26, 0x2000
	s_nop 0
	global_load_lds_dwordx4 v[216:217], off
	v_lshl_add_u64 v[216:217], v[220:221], 0, s[10:11]
	s_mov_b32 m0, s40
	s_nop 0
	global_load_lds_dwordx4 v[216:217], off
	v_lshl_add_u64 v[216:217], v[222:223], 0, s[10:11]
	s_mov_b32 m0, s41
	s_nop 0
	global_load_lds_dwordx4 v[216:217], off
	ds_read_b128 v[184:187], v170 offset:49152
	ds_read_b128 v[188:191], v170 offset:50176
	ds_read_b128 v[192:195], v170 offset:51200
	ds_read_b128 v[196:199], v170 offset:52224
	ds_read_b128 v[200:203], v170 offset:53248
	ds_read_b128 v[204:207], v170 offset:54272
	ds_read_b128 v[208:211], v170 offset:55296
	ds_read_b128 v[212:215], v170 offset:56320
	s_waitcnt vmcnt(8)
	s_waitcnt lgkmcnt(0)
	s_barrier
	v_mfma_f32_16x16x32_f16 v[62:65], v[122:125], v[184:187], v[62:65]
	v_mfma_f32_16x16x32_f16 v[58:61], v[130:133], v[184:187], v[58:61]
	v_mfma_f32_16x16x32_f16 v[46:49], v[122:125], v[192:195], v[46:49]
	v_mfma_f32_16x16x32_f16 v[42:45], v[130:133], v[192:195], v[42:45]
	v_mfma_f32_16x16x32_f16 v[30:33], v[122:125], v[200:203], v[30:33]
	v_mfma_f32_16x16x32_f16 v[26:29], v[130:133], v[200:203], v[26:29]
	v_mfma_f32_16x16x32_f16 v[14:17], v[122:125], v[208:211], v[14:17]
	v_mfma_f32_16x16x32_f16 v[10:13], v[130:133], v[208:211], v[10:13]
	v_mfma_f32_16x16x32_f16 v[62:65], v[126:129], v[188:191], v[62:65]
	v_mfma_f32_16x16x32_f16 v[58:61], v[134:137], v[188:191], v[58:61]
	v_mfma_f32_16x16x32_f16 v[46:49], v[126:129], v[196:199], v[46:49]
	v_mfma_f32_16x16x32_f16 v[42:45], v[134:137], v[196:199], v[42:45]
	v_mfma_f32_16x16x32_f16 v[30:33], v[126:129], v[204:207], v[30:33]
	v_mfma_f32_16x16x32_f16 v[26:29], v[134:137], v[204:207], v[26:29]
	v_mfma_f32_16x16x32_f16 v[14:17], v[126:129], v[212:215], v[14:17]
	v_mfma_f32_16x16x32_f16 v[10:13], v[134:137], v[212:215], v[10:13]
	v_mfma_f32_16x16x32_f16 v[54:57], v[162:165], v[184:187], v[54:57]
	v_mfma_f32_16x16x32_f16 v[50:53], v[176:179], v[184:187], v[50:53]
	v_mfma_f32_16x16x32_f16 v[38:41], v[162:165], v[192:195], v[38:41]
	v_mfma_f32_16x16x32_f16 v[34:37], v[176:179], v[192:195], v[34:37]
	v_mfma_f32_16x16x32_f16 v[22:25], v[162:165], v[200:203], v[22:25]
	v_mfma_f32_16x16x32_f16 v[18:21], v[176:179], v[200:203], v[18:21]
	v_mfma_f32_16x16x32_f16 v[6:9], v[162:165], v[208:211], v[6:9]
	v_mfma_f32_16x16x32_f16 v[2:5], v[176:179], v[208:211], v[2:5]
	v_mfma_f32_16x16x32_f16 v[54:57], v[172:175], v[188:191], v[54:57]
	v_mfma_f32_16x16x32_f16 v[50:53], v[180:183], v[188:191], v[50:53]
	v_mfma_f32_16x16x32_f16 v[38:41], v[172:175], v[196:199], v[38:41]
	v_mfma_f32_16x16x32_f16 v[34:37], v[180:183], v[196:199], v[34:37]
	v_mfma_f32_16x16x32_f16 v[22:25], v[172:175], v[204:207], v[22:25]
	v_mfma_f32_16x16x32_f16 v[18:21], v[180:183], v[204:207], v[18:21]
	v_mfma_f32_16x16x32_f16 v[6:9], v[172:175], v[212:215], v[6:9]
	v_mfma_f32_16x16x32_f16 v[2:5], v[180:183], v[212:215], v[2:5]
	s_barrier
	s_add_i32 s49, s49, 2
	s_add_u32 s22, s22, 0x100
	s_addc_u32 s23, s23, 0
	s_add_u32 s47, s47, 0x100
	s_addc_u32 s48, s48, 0
	s_cmp_gt_u32 s49, 13
	s_cbranch_scc0 .LBB0_1480
	s_and_b64 vcc, exec, s[12:13]
	s_cbranch_vccz .LBB0_1483
	s_barrier

; #define GM_STAGE(bufoff, gbase, voff) do { _Pragma("unroll") for (int _i = 0; _i < 2; ++_i) \
;         __builtin_amdgcn_global_load_lds((const unsigned*)((const char*)(gbase) + (voff)[_i]), (LAS unsigned*)(lds + (bufoff) + ldsw + _i * 8192), 16, 0, 0); } while (0)
; #define GM_LDA(dst, b, h) do { _Pragma("unroll") for (int m = 0; m < 4; ++m) _Pragma("unroll") for (int k = 0; k < 2; ++k) dst[m][k] = *(const LAS s16x8*)(lds + GM_SA(b, h) + aoff + m * 2048 + k * 1024); } while (0)
; #define GM_LDB(dst, b, h) do { _Pragma("unroll") for (int n = 0; n < 2; ++n) _Pragma("unroll") for (int k = 0; k < 2; ++k) dst[n][k] = *(const LAS s16x8*)(lds + GM_SB(b, h) + boff + n * 2048 + k * 1024); } while (0)
; #define GM_MMA(ai, bj, At, Bt) do { __builtin_amdgcn_s_setprio(1); _Pragma("unroll") for (int m = 0; m < 4; ++m) _Pragma("unroll") for (int n = 0; n < 2; ++n) _Pragma("unroll") for (int k = 0; k < 2; ++k) \
;         acc[ai][bj][m][n] = mma16<BF>(Bt[n][k], At[m][k], acc[ai][bj][m][n]); __builtin_amdgcn_s_setprio(0); } while (0)
; #define GM_WAIT_V(n) asm volatile("s_waitcnt vmcnt(" #n ")" ::: "memory")
; #define GM_WAIT_L(n) asm volatile("s_waitcnt lgkmcnt(" #n ")" ::: "memory")
; #define GM_BAR __builtin_amdgcn_s_barrier()
; template <bool BF, bool GATHER = false, class Epi, class Hook>
; __device__ __forceinline__ void gemm_phase(LAS unsigned char* lds, const Gemm g, const Order& S, const Epi& E, Hook& HK) {
;     ...
;         for (int t = 0; t < nt; t += 2) {
;             const bool last = (t == nt - 2);
;             const char* a1 = cA + (size_t)(t + 1) * kstep;
;             const char* a2 = last ? nA : cA + (size_t)(t + 2) * kstep; const char* b2 = last ? nB : cB + (size_t)(t + 2) * kstep;
;             const char* a3 = a2 + kstep; const char* b3 = b2 + kstep;
;             unsigned s0[2], s1[2];
;             if constexpr (GATHER) { s0[0] = last ? nA0[0] : gA0[0]; s0[1] = last ? nA0[1] : gA0[1]; s1[0] = last ? nA1[0] : gA1[0]; s1[1] = last ? nA1[1] : gA1[1]; }
;             GM_LDB(B0, 0, 0); GM_LDB(B1, 0, 1); GM_SCHED; GM_LDA(At, 0, 0); GM_STA_H1(GM_SA(1, 1), a1, gA1);
;             GM_WAIT_V(8); GM_WAIT_L(0); GM_BAR; GM_MMA(0, 0, At, B0); GM_MMA(0, 1, At, B1); GM_BAR; GM_SCHED;
;             GM_LDA(At, 0, 1); GM_STAGE(GM_SB(0, 0), b2, voffB); GM_STAGE(GM_SB(0, 1), b2 + hstepB, voffB); GM_STA_H0(GM_SA(0, 0), a2, s0);
.LBB0_1867:
	s_add_u32 s22, s2, 0x100
	s_addc_u32 s23, s3, 0
	s_cmp_eq_u32 s52, 40
	s_cselect_b32 s27, s7, s23
	s_cselect_b32 s26, s6, s22
	s_cselect_b32 s25, s21, s51
	s_cselect_b32 s24, s20, s50
	v_lshl_add_u64 v[216:217], s[2:3], 0, v[138:139]
	s_add_i32 m0, s29, 0xc000
	s_nop 0
	global_load_lds_dwordx4 v[216:217], off
	v_lshl_add_u64 v[216:217], s[2:3], 0, v[140:141]
	s_add_i32 m0, s29, 0xe000
	s_nop 0
	global_load_lds_dwordx4 v[216:217], off
	ds_read_b128 v[146:149], v153
	ds_read_b128 v[156:159], v153 offset:1024
	ds_read_b128 v[160:163], v153 offset:2048
	ds_read_b128 v[164:167], v153 offset:3072
	ds_read_b128 v[168:171], v154
	ds_read_b128 v[172:175], v154 offset:1024
	ds_read_b128 v[176:179], v154 offset:2048
	ds_read_b128 v[180:183], v154 offset:3072
	ds_read_b128 v[184:187], v155
	ds_read_b128 v[188:191], v155 offset:1024
	ds_read_b128 v[192:195], v155 offset:2048
	ds_read_b128 v[196:199], v155 offset:3072
	ds_read_b128 v[200:203], v155 offset:4096
	ds_read_b128 v[204:207], v155 offset:5120
	ds_read_b128 v[208:211], v155 offset:6144
	ds_read_b128 v[212:215], v155 offset:7168
	s_waitcnt vmcnt(8)
	s_waitcnt lgkmcnt(0)
	s_barrier
	v_mfma_f32_16x16x32_bf16 v[126:129], v[146:149], v[184:187], v[126:129]
	v_mfma_f32_16x16x32_bf16 v[122:125], v[160:163], v[184:187], v[122:125]
	v_mfma_f32_16x16x32_bf16 v[110:113], v[146:149], v[192:195], v[110:113]
	v_mfma_f32_16x16x32_bf16 v[106:109], v[160:163], v[192:195], v[106:109]
	v_mfma_f32_16x16x32_bf16 v[94:97], v[146:149], v[200:203], v[94:97]
	v_mfma_f32_16x16x32_bf16 v[90:93], v[160:163], v[200:203], v[90:93]
	v_mfma_f32_16x16x32_bf16 v[78:81], v[146:149], v[208:211], v[78:81]
	v_mfma_f32_16x16x32_bf16 v[74:77], v[160:163], v[208:211], v[74:77]
	v_mfma_f32_16x16x32_bf16 v[126:129], v[156:159], v[188:191], v[126:129]
	v_mfma_f32_16x16x32_bf16 v[122:125], v[164:167], v[188:191], v[122:125]
	v_mfma_f32_16x16x32_bf16 v[110:113], v[156:159], v[196:199], v[110:113]
	v_mfma_f32_16x16x32_bf16 v[106:109], v[164:167], v[196:199], v[106:109]
	v_mfma_f32_16x16x32_bf16 v[94:97], v[156:159], v[204:207], v[94:97]
	v_mfma_f32_16x16x32_bf16 v[90:93], v[164:167], v[204:207], v[90:93]
	v_mfma_f32_16x16x32_bf16 v[78:81], v[156:159], v[212:215], v[78:81]
	v_mfma_f32_16x16x32_bf16 v[74:77], v[164:167], v[212:215], v[74:77]
	v_mfma_f32_16x16x32_bf16 v[118:121], v[168:171], v[184:187], v[118:121]
	v_mfma_f32_16x16x32_bf16 v[114:117], v[176:179], v[184:187], v[114:117]
	v_mfma_f32_16x16x32_bf16 v[102:105], v[168:171], v[192:195], v[102:105]
	v_mfma_f32_16x16x32_bf16 v[98:101], v[176:179], v[192:195], v[98:101]
	v_mfma_f32_16x16x32_bf16 v[86:89], v[168:171], v[200:203], v[86:89]
	v_mfma_f32_16x16x32_bf16 v[82:85], v[176:179], v[200:203], v[82:85]
	v_mfma_f32_16x16x32_bf16 v[70:73], v[168:171], v[208:211], v[70:73]
	v_mfma_f32_16x16x32_bf16 v[66:69], v[176:179], v[208:211], v[66:69]
	v_mfma_f32_16x16x32_bf16 v[118:121], v[172:175], v[188:191], v[118:121]
	v_mfma_f32_16x16x32_bf16 v[114:117], v[180:183], v[188:191], v[114:117]
	v_mfma_f32_16x16x32_bf16 v[102:105], v[172:175], v[196:199], v[102:105]
	v_mfma_f32_16x16x32_bf16 v[98:101], v[180:183], v[196:199], v[98:101]
	v_mfma_f32_16x16x32_bf16 v[86:89], v[172:175], v[204:207], v[86:89]
	v_mfma_f32_16x16x32_bf16 v[82:85], v[180:183], v[204:207], v[82:85]
	v_mfma_f32_16x16x32_bf16 v[70:73], v[172:175], v[212:215], v[70:73]
	v_mfma_f32_16x16x32_bf16 v[66:69], v[180:183], v[212:215], v[66:69]
	s_barrier
	s_add_i32 s2, s43, s28
	v_lshl_add_u64 v[216:217], s[24:25], 0, v[132:133]
	s_mov_b32 m0, s2
	s_nop 0
	global_load_lds_dwordx4 v[216:217], off
	s_add_i32 m0, s2, 0x2000
	s_add_u32 s2, s24, 0xb0000
	v_lshl_add_u64 v[218:219], s[24:25], 0, v[136:137]
	s_addc_u32 s3, s25, 0
	s_add_i32 s53, s44, s28
	global_load_lds_dwordx4 v[218:219], off
	v_lshl_add_u64 v[220:221], s[2:3], 0, v[132:133]
	s_mov_b32 m0, s53
	v_lshl_add_u64 v[222:223], s[26:27], 0, v[134:135]
	global_load_lds_dwordx4 v[220:221], off
	v_lshl_add_u64 v[220:221], s[2:3], 0, v[136:137]
	s_add_i32 m0, s53, 0x2000
	s_nop 0
	global_load_lds_dwordx4 v[220:221], off
	v_lshl_add_u64 v[220:221], s[26:27], 0, v[130:131]
	s_mov_b32 m0, s29
	s_nop 0
	global_load_lds_dwordx4 v[220:221], off
	s_mov_b32 m0, s30
	s_nop 0
	global_load_lds_dwordx4 v[222:223], off
	ds_read_b128 v[184:187], v155 offset:16384
	ds_read_b128 v[188:191], v155 offset:17408
	ds_read_b128 v[192:195], v155 offset:18432
	ds_read_b128 v[196:199], v155 offset:19456
	ds_read_b128 v[200:203], v155 offset:20480
	ds_read_b128 v[204:207], v155 offset:21504
	ds_read_b128 v[208:211], v155 offset:22528
	ds_read_b128 v[212:215], v155 offset:23552
	s_waitcnt vmcnt(8)
	s_waitcnt lgkmcnt(0)
	s_barrier
; #define GM_LDA(dst, b, h) do { _Pragma("unroll") for (int m = 0; m < 4; ++m) _Pragma("unroll") for (int k = 0; k < 2; ++k) dst[m][k] = *(const LAS s16x8*)(lds + GM_SA(b, h) + aoff + m * 2048 + k * 1024); } while (0)
; #define GM_LDB(dst, b, h) do { _Pragma("unroll") for (int n = 0; n < 2; ++n) _Pragma("unroll") for (int k = 0; k < 2; ++k) dst[n][k] = *(const LAS s16x8*)(lds + GM_SB(b, h) + boff + n * 2048 + k * 1024); } while (0)
; #define GM_MMA(ai, bj, At, Bt) do { __builtin_amdgcn_s_setprio(1); _Pragma("unroll") for (int m = 0; m < 4; ++m) _Pragma("unroll") for (int n = 0; n < 2; ++n) _Pragma("unroll") for (int k = 0; k < 2; ++k) \
;         acc[ai][bj][m][n] = mma16<BF>(Bt[n][k], At[m][k], acc[ai][bj][m][n]); __builtin_amdgcn_s_setprio(0); } while (0)
; #define GM_WAIT_V(n) asm volatile("s_waitcnt vmcnt(" #n ")" ::: "memory")
; #define GM_WAIT_L(n) asm volatile("s_waitcnt lgkmcnt(" #n ")" ::: "memory")
; #define GM_BAR __builtin_amdgcn_s_barrier()
; #define GM_SCHED __builtin_amdgcn_sched_barrier(0)
; #define GM_STA_H1(buf, p, o1) do { if constexpr (GATHER) GM_STAGE(buf, p, o1); else GM_STAGE(buf, (p) + hstepB, voffA); } while (0)
; template <bool BF, bool GATHER = false, class Epi, class Hook>
; __device__ __forceinline__ void gemm_phase(LAS unsigned char* lds, const Gemm g, const Order& S, const Epi& E, Hook& HK) {
;     ...
;             GM_WAIT_V(8); GM_WAIT_L(0); GM_BAR; GM_MMA(1, 0, At, B0); GM_MMA(1, 1, At, B1); GM_BAR; GM_SCHED;
;             GM_LDB(B0, 1, 0); GM_LDB(B1, 1, 1); GM_SCHED; GM_LDA(At, 1, 0); GM_STA_H1(GM_SA(0, 1), a2, s1);
;             GM_WAIT_V(8); GM_WAIT_L(0); GM_BAR; GM_MMA(0, 0, At, B0); GM_MMA(0, 1, At, B1); GM_BAR; GM_SCHED;
	v_mfma_f32_16x16x32_bf16 v[62:65], v[146:149], v[184:187], v[62:65]
	v_mfma_f32_16x16x32_bf16 v[58:61], v[160:163], v[184:187], v[58:61]
	v_mfma_f32_16x16x32_bf16 v[46:49], v[146:149], v[192:195], v[46:49]
	v_mfma_f32_16x16x32_bf16 v[42:45], v[160:163], v[192:195], v[42:45]
	v_mfma_f32_16x16x32_bf16 v[30:33], v[146:149], v[200:203], v[30:33]
	v_mfma_f32_16x16x32_bf16 v[26:29], v[160:163], v[200:203], v[26:29]
	v_mfma_f32_16x16x32_bf16 v[14:17], v[146:149], v[208:211], v[14:17]
	v_mfma_f32_16x16x32_bf16 v[10:13], v[160:163], v[208:211], v[10:13]
	v_mfma_f32_16x16x32_bf16 v[62:65], v[156:159], v[188:191], v[62:65]
	v_mfma_f32_16x16x32_bf16 v[58:61], v[164:167], v[188:191], v[58:61]
	v_mfma_f32_16x16x32_bf16 v[46:49], v[156:159], v[196:199], v[46:49]
	v_mfma_f32_16x16x32_bf16 v[42:45], v[164:167], v[196:199], v[42:45]
	v_mfma_f32_16x16x32_bf16 v[30:33], v[156:159], v[204:207], v[30:33]
	v_mfma_f32_16x16x32_bf16 v[26:29], v[164:167], v[204:207], v[26:29]
	v_mfma_f32_16x16x32_bf16 v[14:17], v[156:159], v[212:215], v[14:17]
	v_mfma_f32_16x16x32_bf16 v[10:13], v[164:167], v[212:215], v[10:13]
	v_mfma_f32_16x16x32_bf16 v[54:57], v[168:171], v[184:187], v[54:57]
	v_mfma_f32_16x16x32_bf16 v[50:53], v[176:179], v[184:187], v[50:53]
	v_mfma_f32_16x16x32_bf16 v[38:41], v[168:171], v[192:195], v[38:41]
	v_mfma_f32_16x16x32_bf16 v[34:37], v[176:179], v[192:195], v[34:37]
	v_mfma_f32_16x16x32_bf16 v[22:25], v[168:171], v[200:203], v[22:25]
	v_mfma_f32_16x16x32_bf16 v[18:21], v[176:179], v[200:203], v[18:21]
	v_mfma_f32_16x16x32_bf16 v[6:9], v[168:171], v[208:211], v[6:9]
	v_mfma_f32_16x16x32_bf16 v[2:5], v[176:179], v[208:211], v[2:5]
	v_mfma_f32_16x16x32_bf16 v[54:57], v[172:175], v[188:191], v[54:57]
	v_mfma_f32_16x16x32_bf16 v[50:53], v[180:183], v[188:191], v[50:53]
	v_mfma_f32_16x16x32_bf16 v[38:41], v[172:175], v[196:199], v[38:41]
	v_mfma_f32_16x16x32_bf16 v[34:37], v[180:183], v[196:199], v[34:37]
	v_mfma_f32_16x16x32_bf16 v[22:25], v[172:175], v[204:207], v[22:25]
	v_mfma_f32_16x16x32_bf16 v[18:21], v[180:183], v[204:207], v[18:21]
	v_mfma_f32_16x16x32_bf16 v[6:9], v[172:175], v[212:215], v[6:9]
	v_mfma_f32_16x16x32_bf16 v[2:5], v[180:183], v[212:215], v[2:5]
	s_barrier
	s_add_u32 s2, s26, 0xb0000
	s_addc_u32 s3, s27, 0
	s_mov_b32 m0, s31
	v_lshl_add_u64 v[224:225], s[2:3], 0, v[130:131]
	global_load_lds_dwordx4 v[224:225], off
	v_lshl_add_u64 v[224:225], s[2:3], 0, v[134:135]
	s_mov_b32 m0, s33
	s_nop 0
	global_load_lds_dwordx4 v[224:225], off
	s_mov_b32 s54, 0x1c000
	s_mov_b32 s53, 0x18000
	v_add_u32_e32 v244, s53, v150
	v_add_u32_e32 v245, s54, v150
	ds_read_b128 v[146:149], v244
	ds_read_b128 v[156:159], v244 offset:1024
	ds_read_b128 v[160:163], v244 offset:2048
	ds_read_b128 v[164:167], v244 offset:3072
	ds_read_b128 v[168:171], v245
	ds_read_b128 v[172:175], v245 offset:1024
	ds_read_b128 v[176:179], v245 offset:2048
	ds_read_b128 v[180:183], v245 offset:3072
	ds_read_b128 v[184:187], v155 offset:32768
	ds_read_b128 v[188:191], v155 offset:33792
	ds_read_b128 v[192:195], v155 offset:34816
	ds_read_b128 v[196:199], v155 offset:35840
	ds_read_b128 v[200:203], v155 offset:36864
	ds_read_b128 v[204:207], v155 offset:37888
	ds_read_b128 v[208:211], v155 offset:38912
	ds_read_b128 v[212:215], v155 offset:39936
	s_waitcnt vmcnt(8)
	s_waitcnt lgkmcnt(0)
	s_barrier
	v_mfma_f32_16x16x32_bf16 v[126:129], v[146:149], v[184:187], v[126:129]
	v_mfma_f32_16x16x32_bf16 v[122:125], v[160:163], v[184:187], v[122:125]
	v_mfma_f32_16x16x32_bf16 v[110:113], v[146:149], v[192:195], v[110:113]
	v_mfma_f32_16x16x32_bf16 v[106:109], v[160:163], v[192:195], v[106:109]
	v_mfma_f32_16x16x32_bf16 v[94:97], v[146:149], v[200:203], v[94:97]
	v_mfma_f32_16x16x32_bf16 v[90:93], v[160:163], v[200:203], v[90:93]
	v_mfma_f32_16x16x32_bf16 v[78:81], v[146:149], v[208:211], v[78:81]
	v_mfma_f32_16x16x32_bf16 v[74:77], v[160:163], v[208:211], v[74:77]
	v_mfma_f32_16x16x32_bf16 v[126:129], v[156:159], v[188:191], v[126:129]
	v_mfma_f32_16x16x32_bf16 v[122:125], v[164:167], v[188:191], v[122:125]
	v_mfma_f32_16x16x32_bf16 v[110:113], v[156:159], v[196:199], v[110:113]
	v_mfma_f32_16x16x32_bf16 v[106:109], v[164:167], v[196:199], v[106:109]
	v_mfma_f32_16x16x32_bf16 v[94:97], v[156:159], v[204:207], v[94:97]
	v_mfma_f32_16x16x32_bf16 v[90:93], v[164:167], v[204:207], v[90:93]
	v_mfma_f32_16x16x32_bf16 v[78:81], v[156:159], v[212:215], v[78:81]
	v_mfma_f32_16x16x32_bf16 v[74:77], v[164:167], v[212:215], v[74:77]
	v_mfma_f32_16x16x32_bf16 v[118:121], v[168:171], v[184:187], v[118:121]
	v_mfma_f32_16x16x32_bf16 v[114:117], v[176:179], v[184:187], v[114:117]
	v_mfma_f32_16x16x32_bf16 v[102:105], v[168:171], v[192:195], v[102:105]
	v_mfma_f32_16x16x32_bf16 v[98:101], v[176:179], v[192:195], v[98:101]
	v_mfma_f32_16x16x32_bf16 v[86:89], v[168:171], v[200:203], v[86:89]
	v_mfma_f32_16x16x32_bf16 v[82:85], v[176:179], v[200:203], v[82:85]
	v_mfma_f32_16x16x32_bf16 v[70:73], v[168:171], v[208:211], v[70:73]
	v_mfma_f32_16x16x32_bf16 v[66:69], v[176:179], v[208:211], v[66:69]
	v_mfma_f32_16x16x32_bf16 v[118:121], v[172:175], v[188:191], v[118:121]
	v_mfma_f32_16x16x32_bf16 v[114:117], v[180:183], v[188:191], v[114:117]
	v_mfma_f32_16x16x32_bf16 v[102:105], v[172:175], v[196:199], v[102:105]
	v_mfma_f32_16x16x32_bf16 v[98:101], v[180:183], v[196:199], v[98:101]
	v_mfma_f32_16x16x32_bf16 v[86:89], v[172:175], v[204:207], v[86:89]
	v_mfma_f32_16x16x32_bf16 v[82:85], v[180:183], v[204:207], v[82:85]
	v_mfma_f32_16x16x32_bf16 v[70:73], v[172:175], v[212:215], v[70:73]
	v_mfma_f32_16x16x32_bf16 v[66:69], v[180:183], v[212:215], v[66:69]
	s_barrier
; #define GM_STAGE(bufoff, gbase, voff) do { _Pragma("unroll") for (int _i = 0; _i < 2; ++_i) \
;         __builtin_amdgcn_global_load_lds((const unsigned*)((const char*)(gbase) + (voff)[_i]), (LAS unsigned*)(lds + (bufoff) + ldsw + _i * 8192), 16, 0, 0); } while (0)
; #define GM_LDA(dst, b, h) do { _Pragma("unroll") for (int m = 0; m < 4; ++m) _Pragma("unroll") for (int k = 0; k < 2; ++k) dst[m][k] = *(const LAS s16x8*)(lds + GM_SA(b, h) + aoff + m * 2048 + k * 1024); } while (0)
; #define GM_MMA(ai, bj, At, Bt) do { __builtin_amdgcn_s_setprio(1); _Pragma("unroll") for (int m = 0; m < 4; ++m) _Pragma("unroll") for (int n = 0; n < 2; ++n) _Pragma("unroll") for (int k = 0; k < 2; ++k) \
;         acc[ai][bj][m][n] = mma16<BF>(Bt[n][k], At[m][k], acc[ai][bj][m][n]); __builtin_amdgcn_s_setprio(0); } while (0)
; #define GM_WAIT_V(n) asm volatile("s_waitcnt vmcnt(" #n ")" ::: "memory")
; #define GM_WAIT_L(n) asm volatile("s_waitcnt lgkmcnt(" #n ")" ::: "memory")
; #define GM_BAR __builtin_amdgcn_s_barrier()
; #define GM_SCHED __builtin_amdgcn_sched_barrier(0)
; #define GM_STA_H0(buf, p, o0) do { if constexpr (GATHER) GM_STAGE(buf, p, o0); else GM_STAGE(buf, p, voffA); } while (0)
; template <bool BF, bool GATHER = false, class Epi, class Hook>
; __device__ __forceinline__ void gemm_phase(LAS unsigned char* lds, const Gemm g, const Order& S, const Epi& E, Hook& HK) {
;     ...
;             GM_LDA(At, 1, 1); GM_STAGE(GM_SB(1, 0), b3, voffB); GM_STAGE(GM_SB(1, 1), b3 + hstepB, voffB); GM_STA_H0(GM_SA(1, 0), a3, s0);
;             GM_WAIT_V(8); GM_WAIT_L(0); GM_BAR; GM_MMA(1, 0, At, B0); GM_MMA(1, 1, At, B1); GM_BAR; GM_SCHED;
;         }
;         if (wr == 0) GM_BAR;
	s_add_i32 s2, s53, s28
	v_lshl_add_u64 v[216:217], v[216:217], 0, s[12:13]
	s_mov_b32 m0, s2
	s_nop 0
	global_load_lds_dwordx4 v[216:217], off
	s_add_i32 m0, s2, 0x2000
	s_add_u32 s2, s24, 0xb0080
	v_lshl_add_u64 v[216:217], v[218:219], 0, s[12:13]
	s_addc_u32 s3, s25, 0
	s_add_i32 s24, s54, s28
	global_load_lds_dwordx4 v[216:217], off
	v_lshl_add_u64 v[216:217], s[2:3], 0, v[132:133]
	s_mov_b32 m0, s24
	s_nop 0
	global_load_lds_dwordx4 v[216:217], off
	v_lshl_add_u64 v[216:217], s[2:3], 0, v[136:137]
	s_add_i32 m0, s24, 0x2000
	s_nop 0
	global_load_lds_dwordx4 v[216:217], off
	v_lshl_add_u64 v[216:217], v[220:221], 0, s[12:13]
	s_mov_b32 m0, s36
	s_nop 0
	global_load_lds_dwordx4 v[216:217], off
	v_lshl_add_u64 v[216:217], v[222:223], 0, s[12:13]
	s_mov_b32 m0, s37
	s_nop 0
	global_load_lds_dwordx4 v[216:217], off
	ds_read_b128 v[184:187], v155 offset:49152
	ds_read_b128 v[188:191], v155 offset:50176
	ds_read_b128 v[192:195], v155 offset:51200
	ds_read_b128 v[196:199], v155 offset:52224
	ds_read_b128 v[200:203], v155 offset:53248
	ds_read_b128 v[204:207], v155 offset:54272
	ds_read_b128 v[208:211], v155 offset:55296
	ds_read_b128 v[212:215], v155 offset:56320
	s_waitcnt vmcnt(8)
	s_waitcnt lgkmcnt(0)
	s_barrier
	v_mfma_f32_16x16x32_bf16 v[62:65], v[146:149], v[184:187], v[62:65]
	v_mfma_f32_16x16x32_bf16 v[58:61], v[160:163], v[184:187], v[58:61]
	v_mfma_f32_16x16x32_bf16 v[46:49], v[146:149], v[192:195], v[46:49]
	v_mfma_f32_16x16x32_bf16 v[42:45], v[160:163], v[192:195], v[42:45]
	v_mfma_f32_16x16x32_bf16 v[30:33], v[146:149], v[200:203], v[30:33]
	v_mfma_f32_16x16x32_bf16 v[26:29], v[160:163], v[200:203], v[26:29]
	v_mfma_f32_16x16x32_bf16 v[14:17], v[146:149], v[208:211], v[14:17]
	v_mfma_f32_16x16x32_bf16 v[10:13], v[160:163], v[208:211], v[10:13]
	v_mfma_f32_16x16x32_bf16 v[62:65], v[156:159], v[188:191], v[62:65]
	v_mfma_f32_16x16x32_bf16 v[58:61], v[164:167], v[188:191], v[58:61]
	v_mfma_f32_16x16x32_bf16 v[46:49], v[156:159], v[196:199], v[46:49]
	v_mfma_f32_16x16x32_bf16 v[42:45], v[164:167], v[196:199], v[42:45]
	v_mfma_f32_16x16x32_bf16 v[30:33], v[156:159], v[204:207], v[30:33]
	v_mfma_f32_16x16x32_bf16 v[26:29], v[164:167], v[204:207], v[26:29]
	v_mfma_f32_16x16x32_bf16 v[14:17], v[156:159], v[212:215], v[14:17]
	v_mfma_f32_16x16x32_bf16 v[10:13], v[164:167], v[212:215], v[10:13]
	v_mfma_f32_16x16x32_bf16 v[54:57], v[168:171], v[184:187], v[54:57]
	v_mfma_f32_16x16x32_bf16 v[50:53], v[176:179], v[184:187], v[50:53]
	v_mfma_f32_16x16x32_bf16 v[38:41], v[168:171], v[192:195], v[38:41]
	v_mfma_f32_16x16x32_bf16 v[34:37], v[176:179], v[192:195], v[34:37]
	v_mfma_f32_16x16x32_bf16 v[22:25], v[168:171], v[200:203], v[22:25]
	v_mfma_f32_16x16x32_bf16 v[18:21], v[176:179], v[200:203], v[18:21]
	v_mfma_f32_16x16x32_bf16 v[6:9], v[168:171], v[208:211], v[6:9]
	v_mfma_f32_16x16x32_bf16 v[2:5], v[176:179], v[208:211], v[2:5]
	v_mfma_f32_16x16x32_bf16 v[54:57], v[172:175], v[188:191], v[54:57]
	v_mfma_f32_16x16x32_bf16 v[50:53], v[180:183], v[188:191], v[50:53]
	v_mfma_f32_16x16x32_bf16 v[38:41], v[172:175], v[196:199], v[38:41]
	v_mfma_f32_16x16x32_bf16 v[34:37], v[180:183], v[196:199], v[34:37]
	v_mfma_f32_16x16x32_bf16 v[22:25], v[172:175], v[204:207], v[22:25]
	v_mfma_f32_16x16x32_bf16 v[18:21], v[180:183], v[204:207], v[18:21]
	v_mfma_f32_16x16x32_bf16 v[6:9], v[172:175], v[212:215], v[6:9]
	v_mfma_f32_16x16x32_bf16 v[2:5], v[180:183], v[212:215], v[2:5]
	s_barrier
	s_add_i32 s52, s52, 2
	s_add_u32 s50, s50, 0x100
	s_addc_u32 s51, s51, 0
	s_cmp_gt_u32 s52, 41
	s_mov_b64 s[2:3], s[22:23]
	s_cbranch_scc0 .LBB0_1867
	s_and_b64 vcc, exec, s[14:15]
	s_cbranch_vccz .LBB0_1870
	s_barrier
